# hand-written mla_prep and prep phases: 16-lane DPP reductions instead of ds_bpermute butterflies, v_rsq instead of IEEE sqrt+div, 3-row load pipeline
# speedup vs baseline: 1.0232x; 1.0232x over previous
.LBB0_6295:
	s_andn2_b64 vcc, exec, s[0:1]
	s_cbranch_vccnz .LBB0_6363
	v_readlane_b32 s0, v251, 2
	s_nop 3
	s_cmpk_lg_u32 s0, 0x100
	s_cbranch_scc1 .Lpp_orig
	v_readlane_b32 s4, v251, 59
	v_readlane_b32 s5, v251, 60
	v_readlane_b32 s8, v255, 20
	v_readlane_b32 s10, v251, 61
	v_readfirstlane_b32 s0, v0
	v_readlane_b32 s70, v251, 11
	v_readlane_b32 s71, v251, 12
	v_readlane_b32 s72, v251, 13
	v_readlane_b32 s73, v251, 14
	v_readlane_b32 s74, v251, 15
	v_readlane_b32 s75, v251, 16
	v_readlane_b32 s76, v251, 17
	v_readlane_b32 s77, v251, 18
	v_readlane_b32 s78, v251, 7
	v_readlane_b32 s79, v251, 8
	s_nop 3
	s_lshr_b32 s0, s0, 6
	s_add_i32 s10, s10, s0
	s_lshl_b32 s1, s8, 9
	s_add_u32 s70, s70, s1
	s_addc_u32 s71, s71, 0
	s_add_u32 s72, s72, s1
	s_addc_u32 s73, s73, 0
	s_lshl_b32 s1, s8, 11
	s_add_u32 s74, s74, s1
	s_addc_u32 s75, s75, 0
	s_lshl_b32 s1, s8, 10
	s_add_u32 s76, s76, s1
	s_addc_u32 s77, s77, 0
	s_lshl_b32 s1, s8, 6
	s_add_u32 s78, s78, s1
	s_addc_u32 s79, s79, 0
	s_add_u32 s48, s4, 0x41491000
	s_addc_u32 s49, s5, 0
	s_add_u32 s50, s4, 0x4b690000
	s_addc_u32 s51, s5, 0
	s_add_u32 s52, s4, 0xe8000
	s_addc_u32 s53, s5, 0
	s_add_u32 s54, s4, 0x168000
	s_addc_u32 s55, s5, 0
	s_add_u32 s56, s4, 0x4bf90000
	s_addc_u32 s57, s5, 0
	s_add_u32 s58, s4, 0x4e390000
	s_addc_u32 s59, s5, 0
	s_add_u32 s62, s4, 0x4fe8fe00
	s_addc_u32 s63, s5, 0
	s_add_u32 s64, s4, 0x4ec90000
	s_addc_u32 s65, s5, 0
	s_mov_b32 s66, 0
	s_mov_b32 s67, -1
	s_mov_b32 s68, 0xf0f0f0f0
	s_mov_b32 s69, 0xf0f0f0f0
	s_mov_b32 s47, 0xbfb8aa3b
	v_and_b32_e32 v1, 63, v0
	v_and_b32_e32 v2, 15, v1
	v_lshlrev_b32_e32 v4, 4, v1
	v_mov_b32_e32 v176, 0x800
	v_mov_b32_e32 v177, 0xe00
	v_cndmask_b32_e64 v5, v176, v177, s[66:67]
	v_add_u32_e32 v5, v5, v4
	v_lshlrev_b32_e32 v6, 2, v2
	v_and_b32_e32 v7, 7, v1
	v_lshlrev_b32_e32 v7, 5, v7
	v_bfe_u32 v176, v1, 3, 1
	v_lshlrev_b32_e32 v176, 5, v176
	v_and_b32_e32 v177, 3, v1
	v_or_b32_e32 v176, v176, v177
	s_movk_i32 s0, 0x2400
	v_mul_u32_u24_e32 v176, s0, v176
	v_mov_b32_e32 v177, 0x268000
	v_mov_b32_e32 v178, 0x2f8000
	v_cndmask_b32_e64 v177, v177, v178, s[68:69]
	v_add_u32_e32 v8, v176, v177
	v_and_b32_e32 v9, 8, v1
	v_lshlrev_b32_e32 v9, 28, v9
	v_xor_b32_e32 v9, 0x80000000, v9
	v_mov_b32_e32 v176, 0x413504f3
	v_mov_b32_e32 v177, 0x41800000
	v_cndmask_b32_e64 v10, v176, v177, s[66:67]
	v_lshlrev_b32_e32 v176, 5, v2
	v_lshlrev_b32_e32 v177, 5, v1
	v_add_u32_e32 v178, 0xfffffc00, v177
	global_load_dwordx4 v[12:15], v176, s[70:71]
	global_load_dwordx4 v[16:19], v176, s[70:71] offset:16
	global_load_dwordx4 v[28:31], v177, s[74:75]
	global_load_dwordx4 v[32:35], v177, s[74:75] offset:16
	global_load_dword v11, v6, s[78:79]
	s_mov_b64 exec, 0xffffffff
	global_load_dwordx4 v[20:23], v176, s[72:73]
	global_load_dwordx4 v[24:27], v176, s[72:73] offset:16
	s_mov_b64 exec, s[66:67]
	global_load_dwordx4 v[20:23], v178, s[76:77]
	global_load_dwordx4 v[24:27], v178, s[76:77] offset:16
	s_mov_b64 exec, -1
	s_add_i32 s11, s10, 0x0
	s_lshr_b32 s0, s11, 8
	s_mul_i32 s0, s0, 57
	s_lshr_b32 s0, s0, 9
	s_mul_i32 s1, s0, 0x900
	s_sub_i32 s43, s11, s1
	s_sub_i32 s0, s43, 0x100
	s_max_i32 s0, s0, 0
	s_mul_i32 s1, s11, 0x2400
	s_add_u32 s12, s48, s1
	s_addc_u32 s13, s49, 0
	s_lshl_b32 s1, s11, 9
	s_add_u32 s14, s50, s1
	s_addc_u32 s15, s51, 0
	s_lshl_b32 s1, s0, 8
	s_add_u32 s16, s52, s1
	s_addc_u32 s17, s53, 0
	s_add_u32 s18, s54, s1
	s_addc_u32 s19, s55, 0
	global_load_dwordx4 v[36:39], v4, s[12:13]
	global_load_dwordx4 v[40:43], v4, s[12:13] offset:1024
	global_load_dwordx4 v[44:47], v5, s[12:13]
	global_load_dwordx4 v[48:51], v4, s[12:13] offset:3072
	global_load_dword v68, v6, s[14:15]
	global_load_dwordx4 v[52:55], v7, s[16:17]
	global_load_dwordx4 v[56:59], v7, s[16:17] offset:16
	global_load_dwordx4 v[60:63], v7, s[18:19]
	global_load_dwordx4 v[64:67], v7, s[18:19] offset:16
	s_add_i32 s11, s10, 0x800
	s_lshr_b32 s0, s11, 8
	s_mul_i32 s0, s0, 57
	s_lshr_b32 s0, s0, 9
	s_mul_i32 s1, s0, 0x900
	s_sub_i32 s43, s11, s1
	s_sub_i32 s0, s43, 0x100
	s_max_i32 s0, s0, 0
	s_mul_i32 s1, s11, 0x2400
	s_add_u32 s12, s48, s1
	s_addc_u32 s13, s49, 0
	s_lshl_b32 s1, s11, 9
	s_add_u32 s14, s50, s1
	s_addc_u32 s15, s51, 0
	s_lshl_b32 s1, s0, 8
	s_add_u32 s16, s52, s1
	s_addc_u32 s17, s53, 0
	s_add_u32 s18, s54, s1
	s_addc_u32 s19, s55, 0
	global_load_dwordx4 v[70:73], v4, s[12:13]
	global_load_dwordx4 v[74:77], v4, s[12:13] offset:1024
	global_load_dwordx4 v[78:81], v5, s[12:13]
	global_load_dwordx4 v[82:85], v4, s[12:13] offset:3072
	global_load_dword v102, v6, s[14:15]
	global_load_dwordx4 v[86:89], v7, s[16:17]
	global_load_dwordx4 v[90:93], v7, s[16:17] offset:16
	global_load_dwordx4 v[94:97], v7, s[18:19]
	global_load_dwordx4 v[98:101], v7, s[18:19] offset:16
	s_add_i32 s11, s10, 0x1000
	s_lshr_b32 s0, s11, 8
	s_mul_i32 s0, s0, 57
	s_lshr_b32 s0, s0, 9
	s_mul_i32 s1, s0, 0x900
	s_sub_i32 s43, s11, s1
	s_sub_i32 s0, s43, 0x100
	s_max_i32 s0, s0, 0
	s_mul_i32 s1, s11, 0x2400
	s_add_u32 s12, s48, s1
	s_addc_u32 s13, s49, 0
	s_lshl_b32 s1, s11, 9
	s_add_u32 s14, s50, s1
	s_addc_u32 s15, s51, 0
	s_lshl_b32 s1, s0, 8
	s_add_u32 s16, s52, s1
	s_addc_u32 s17, s53, 0
	s_add_u32 s18, s54, s1
	s_addc_u32 s19, s55, 0
	global_load_dwordx4 v[104:107], v4, s[12:13]
	global_load_dwordx4 v[108:111], v4, s[12:13] offset:1024
	global_load_dwordx4 v[112:115], v5, s[12:13]
	global_load_dwordx4 v[116:119], v4, s[12:13] offset:3072
	global_load_dword v136, v6, s[14:15]
	global_load_dwordx4 v[120:123], v7, s[16:17]
	global_load_dwordx4 v[124:127], v7, s[16:17] offset:16
	global_load_dwordx4 v[128:131], v7, s[18:19]
	global_load_dwordx4 v[132:135], v7, s[18:19] offset:16
	s_waitcnt vmcnt(27)
	v_mul_f32_e32 v12, 0x3fb8aa3b, v12
	v_mul_f32_e32 v13, 0x3fb8aa3b, v13
	v_mul_f32_e32 v14, 0x3fb8aa3b, v14
	v_mul_f32_e32 v15, 0x3fb8aa3b, v15
	v_mul_f32_e32 v16, 0x3fb8aa3b, v16
	v_mul_f32_e32 v17, 0x3fb8aa3b, v17
	v_mul_f32_e32 v18, 0x3fb8aa3b, v18
	v_mul_f32_e32 v19, 0x3fb8aa3b, v19
	v_mul_f32_e32 v20, v10, v20
	v_mul_f32_e32 v21, v10, v21
	v_mul_f32_e32 v22, v10, v22
	v_mul_f32_e32 v23, v10, v23
	v_mul_f32_e32 v24, v10, v24
	v_mul_f32_e32 v25, v10, v25
	v_mul_f32_e32 v26, v10, v26
	v_mul_f32_e32 v27, v10, v27
	v_mul_f32_e32 v28, 0x41b504f3, v28
	v_mul_f32_e32 v29, 0x41b504f3, v29
	v_mul_f32_e32 v30, 0x41b504f3, v30
	v_mul_f32_e32 v31, 0x41b504f3, v31
	v_mul_f32_e32 v32, 0x41b504f3, v32
	v_mul_f32_e32 v33, 0x41b504f3, v33
	v_mul_f32_e32 v34, 0x41b504f3, v34
	v_mul_f32_e32 v35, 0x41b504f3, v35
	s_waitcnt vmcnt(18)
	s_add_i32 s11, s10, 0x0
	s_lshr_b32 s0, s11, 8
	s_mul_i32 s0, s0, 57
	s_lshr_b32 s0, s0, 9
	s_mul_i32 s1, s0, 0x900
	s_sub_i32 s43, s11, s1
	s_mul_i32 s1, s0, 0x9000
	s_lshl_b32 s2, s43, 2
	s_add_i32 s1, s1, s2
	s_add_u32 s44, s4, s1
	s_addc_u32 s45, s5, 0
	s_lshl_b32 s1, s11, 11
	s_add_u32 s22, s56, s1
	s_addc_u32 s23, s57, 0
	s_lshl_b32 s1, s11, 9
	s_add_u32 s28, s58, s1
	s_addc_u32 s29, s59, 0
	s_add_u32 s30, s62, s1
	s_addc_u32 s31, s63, 0
	s_lshl_b32 s1, s11, 10
	s_add_u32 s34, s64, s1
	s_addc_u32 s35, s65, 0
	v_xor_b32_e32 v168, v9, v60
	v_xor_b32_e32 v169, v9, v61
	v_xor_b32_e32 v170, v9, v62
	v_xor_b32_e32 v171, v9, v63
	v_xor_b32_e32 v172, v9, v64
	v_xor_b32_e32 v173, v9, v65
	v_xor_b32_e32 v174, v9, v66
	v_xor_b32_e32 v175, v9, v67
	s_cmpk_ge_u32 s43, 0x100
	v_lshlrev_b32_e32 v148, 16, v36
	v_and_b32_e32 v149, 0xffff0000, v36
	v_lshlrev_b32_e32 v150, 16, v37
	v_and_b32_e32 v151, 0xffff0000, v37
	v_lshlrev_b32_e32 v152, 16, v38
	v_and_b32_e32 v153, 0xffff0000, v38
	v_lshlrev_b32_e32 v154, 16, v39
	v_and_b32_e32 v155, 0xffff0000, v39
	v_mul_f32_e32 v164, v148, v148
	v_fmac_f32_e32 v164, v149, v149
	v_fmac_f32_e32 v164, v150, v150
	v_fmac_f32_e32 v164, v151, v151
	v_fmac_f32_e32 v164, v152, v152
	v_fmac_f32_e32 v164, v153, v153
	v_fmac_f32_e32 v164, v154, v154
	v_fmac_f32_e32 v164, v155, v155
	v_mul_f32_e32 v148, v148, v12
	v_mul_f32_e32 v149, v149, v13
	v_add_f32_dpp v164, v164, v164 quad_perm:[1,0,3,2] row_mask:0xf bank_mask:0xf
	v_mul_f32_e32 v150, v150, v14
	v_mul_f32_e32 v151, v151, v15
	v_add_f32_dpp v164, v164, v164 quad_perm:[2,3,0,1] row_mask:0xf bank_mask:0xf
	v_mul_f32_e32 v152, v152, v16
	v_mul_f32_e32 v153, v153, v17
	v_add_f32_dpp v164, v164, v164 row_half_mirror row_mask:0xf bank_mask:0xf
	v_mul_f32_e32 v154, v154, v18
	v_mul_f32_e32 v155, v155, v19
	v_add_f32_dpp v164, v164, v164 row_mirror row_mask:0xf bank_mask:0xf
	v_add_f32_e32 v164, 0x390637bd, v164
	v_rsq_f32_e32 v165, v164
	s_nop 0
	v_mul_f32_e32 v148, v148, v165
	v_mul_f32_e32 v149, v149, v165
	v_mul_f32_e32 v150, v150, v165
	v_mul_f32_e32 v151, v151, v165
	v_mul_f32_e32 v152, v152, v165
	v_mul_f32_e32 v153, v153, v165
	v_mul_f32_e32 v154, v154, v165
	v_mul_f32_e32 v155, v155, v165
	s_cbranch_scc0 .Lpp_norope_q0_0
	v_mul_f32_dpp v156, v148, v168 row_ror:8 row_mask:0xf bank_mask:0xf
	v_mul_f32_dpp v157, v149, v169 row_ror:8 row_mask:0xf bank_mask:0xf
	v_mul_f32_dpp v158, v150, v170 row_ror:8 row_mask:0xf bank_mask:0xf
	v_mul_f32_dpp v159, v151, v171 row_ror:8 row_mask:0xf bank_mask:0xf
	v_mul_f32_dpp v160, v152, v172 row_ror:8 row_mask:0xf bank_mask:0xf
	v_mul_f32_dpp v161, v153, v173 row_ror:8 row_mask:0xf bank_mask:0xf
	v_mul_f32_dpp v162, v154, v174 row_ror:8 row_mask:0xf bank_mask:0xf
	v_mul_f32_dpp v163, v155, v175 row_ror:8 row_mask:0xf bank_mask:0xf
	v_fmac_f32_e32 v156, v148, v52
	v_fmac_f32_e32 v157, v149, v53
	v_fmac_f32_e32 v158, v150, v54
	v_fmac_f32_e32 v159, v151, v55
	v_fmac_f32_e32 v160, v152, v56
	v_fmac_f32_e32 v161, v153, v57
	v_fmac_f32_e32 v162, v154, v58
	v_fmac_f32_e32 v163, v155, v59
	s_branch .Lpp_ropedone_q0_0
.Lpp_norope_q0_0:
	v_mov_b32_e32 v156, v148
	v_mov_b32_e32 v157, v149
	v_mov_b32_e32 v158, v150
	v_mov_b32_e32 v159, v151
	v_mov_b32_e32 v160, v152
	v_mov_b32_e32 v161, v153
	v_mov_b32_e32 v162, v154
	v_mov_b32_e32 v163, v155
.Lpp_ropedone_q0_0:
	v_cvt_pk_bf16_f32 v156, v156, v157
	v_cvt_pk_bf16_f32 v157, v158, v159
	v_cvt_pk_bf16_f32 v158, v160, v161
	v_cvt_pk_bf16_f32 v159, v162, v163
	global_store_dwordx4 v4, v[156:159], s[22:23]
	s_nop 1
	v_lshlrev_b32_e32 v148, 16, v40
	v_and_b32_e32 v149, 0xffff0000, v40
	v_lshlrev_b32_e32 v150, 16, v41
	v_and_b32_e32 v151, 0xffff0000, v41
	v_lshlrev_b32_e32 v152, 16, v42
	v_and_b32_e32 v153, 0xffff0000, v42
	v_lshlrev_b32_e32 v154, 16, v43
	v_and_b32_e32 v155, 0xffff0000, v43
	v_mul_f32_e32 v164, v148, v148
	v_fmac_f32_e32 v164, v149, v149
	v_fmac_f32_e32 v164, v150, v150
	v_fmac_f32_e32 v164, v151, v151
	v_fmac_f32_e32 v164, v152, v152
	v_fmac_f32_e32 v164, v153, v153
	v_fmac_f32_e32 v164, v154, v154
	v_fmac_f32_e32 v164, v155, v155
	v_mul_f32_e32 v148, v148, v12
	v_mul_f32_e32 v149, v149, v13
	v_add_f32_dpp v164, v164, v164 quad_perm:[1,0,3,2] row_mask:0xf bank_mask:0xf
	v_mul_f32_e32 v150, v150, v14
	v_mul_f32_e32 v151, v151, v15
	v_add_f32_dpp v164, v164, v164 quad_perm:[2,3,0,1] row_mask:0xf bank_mask:0xf
	v_mul_f32_e32 v152, v152, v16
	v_mul_f32_e32 v153, v153, v17
	v_add_f32_dpp v164, v164, v164 row_half_mirror row_mask:0xf bank_mask:0xf
	v_mul_f32_e32 v154, v154, v18
	v_mul_f32_e32 v155, v155, v19
	v_add_f32_dpp v164, v164, v164 row_mirror row_mask:0xf bank_mask:0xf
	v_add_f32_e32 v164, 0x390637bd, v164
	v_rsq_f32_e32 v165, v164
	s_nop 0
	v_mul_f32_e32 v148, v148, v165
	v_mul_f32_e32 v149, v149, v165
	v_mul_f32_e32 v150, v150, v165
	v_mul_f32_e32 v151, v151, v165
	v_mul_f32_e32 v152, v152, v165
	v_mul_f32_e32 v153, v153, v165
	v_mul_f32_e32 v154, v154, v165
	v_mul_f32_e32 v155, v155, v165
	s_cbranch_scc0 .Lpp_norope_q1_0
	v_mul_f32_dpp v156, v148, v168 row_ror:8 row_mask:0xf bank_mask:0xf
	v_mul_f32_dpp v157, v149, v169 row_ror:8 row_mask:0xf bank_mask:0xf
	v_mul_f32_dpp v158, v150, v170 row_ror:8 row_mask:0xf bank_mask:0xf
	v_mul_f32_dpp v159, v151, v171 row_ror:8 row_mask:0xf bank_mask:0xf
	v_mul_f32_dpp v160, v152, v172 row_ror:8 row_mask:0xf bank_mask:0xf
	v_mul_f32_dpp v161, v153, v173 row_ror:8 row_mask:0xf bank_mask:0xf
	v_mul_f32_dpp v162, v154, v174 row_ror:8 row_mask:0xf bank_mask:0xf
	v_mul_f32_dpp v163, v155, v175 row_ror:8 row_mask:0xf bank_mask:0xf
	v_fmac_f32_e32 v156, v148, v52
	v_fmac_f32_e32 v157, v149, v53
	v_fmac_f32_e32 v158, v150, v54
	v_fmac_f32_e32 v159, v151, v55
	v_fmac_f32_e32 v160, v152, v56
	v_fmac_f32_e32 v161, v153, v57
	v_fmac_f32_e32 v162, v154, v58
	v_fmac_f32_e32 v163, v155, v59
	s_branch .Lpp_ropedone_q1_0

.Lpp_ropedone_q1_0:
	v_cvt_pk_bf16_f32 v156, v156, v157
	v_cvt_pk_bf16_f32 v157, v158, v159
	v_cvt_pk_bf16_f32 v158, v160, v161
	v_cvt_pk_bf16_f32 v159, v162, v163
	global_store_dwordx4 v4, v[156:159], s[22:23] offset:1024
	s_nop 1
	v_lshlrev_b32_e32 v148, 16, v44
	v_and_b32_e32 v149, 0xffff0000, v44
	v_lshlrev_b32_e32 v150, 16, v45
	v_and_b32_e32 v151, 0xffff0000, v45
	v_lshlrev_b32_e32 v152, 16, v46
	v_and_b32_e32 v153, 0xffff0000, v46
	v_lshlrev_b32_e32 v154, 16, v47
	v_and_b32_e32 v155, 0xffff0000, v47
	v_mul_f32_e32 v164, v148, v148
	v_fmac_f32_e32 v164, v149, v149
	v_fmac_f32_e32 v164, v150, v150
	v_fmac_f32_e32 v164, v151, v151
	v_fmac_f32_e32 v164, v152, v152
	v_fmac_f32_e32 v164, v153, v153
	v_fmac_f32_e32 v164, v154, v154
	v_fmac_f32_e32 v164, v155, v155
	v_mul_f32_e32 v148, v148, v20
	v_mul_f32_e32 v149, v149, v21
	v_add_f32_dpp v164, v164, v164 quad_perm:[1,0,3,2] row_mask:0xf bank_mask:0xf
	v_mul_f32_e32 v150, v150, v22
	v_mul_f32_e32 v151, v151, v23
	v_add_f32_dpp v164, v164, v164 quad_perm:[2,3,0,1] row_mask:0xf bank_mask:0xf
	v_mul_f32_e32 v152, v152, v24
	v_mul_f32_e32 v153, v153, v25
	v_add_f32_dpp v164, v164, v164 row_half_mirror row_mask:0xf bank_mask:0xf
	v_mul_f32_e32 v154, v154, v26
	v_mul_f32_e32 v155, v155, v27
	v_add_f32_dpp v164, v164, v164 row_mirror row_mask:0xf bank_mask:0xf
	s_nop 0
	v_readlane_b32 s0, v164, 32
	v_readlane_b32 s1, v164, 48
	v_add_f32_e32 v176, 0x390637bd, v164
	s_nop 1
	v_mov_b32_e32 v166, s0
	v_add_f32_e32 v166, s1, v166
	v_add_f32_e32 v166, 0x398637bd, v166
	v_cndmask_b32_e64 v176, v176, v166, s[66:67]
	v_rsq_f32_e32 v165, v176
	s_nop 0
	v_mul_f32_e32 v148, v148, v165
	v_mul_f32_e32 v149, v149, v165
	v_mul_f32_e32 v150, v150, v165
	v_mul_f32_e32 v151, v151, v165
	v_mul_f32_e32 v152, v152, v165
	v_mul_f32_e32 v153, v153, v165
	v_mul_f32_e32 v154, v154, v165
	v_mul_f32_e32 v155, v155, v165
	s_cbranch_scc0 .Lpp_norope_kk_0
	v_mov_b32_e32 v156, v148
	v_mov_b32_e32 v157, v149
	v_mov_b32_e32 v158, v150
	v_mov_b32_e32 v159, v151
	v_mov_b32_e32 v160, v152
	v_mov_b32_e32 v161, v153
	v_mov_b32_e32 v162, v154
	v_mov_b32_e32 v163, v155
	s_mov_b64 exec, 0xffffffff
	s_nop 4
	v_mul_f32_dpp v156, v148, v168 row_ror:8 row_mask:0xf bank_mask:0xf
	v_mul_f32_dpp v157, v149, v169 row_ror:8 row_mask:0xf bank_mask:0xf
	v_mul_f32_dpp v158, v150, v170 row_ror:8 row_mask:0xf bank_mask:0xf
	v_mul_f32_dpp v159, v151, v171 row_ror:8 row_mask:0xf bank_mask:0xf
	v_mul_f32_dpp v160, v152, v172 row_ror:8 row_mask:0xf bank_mask:0xf
	v_mul_f32_dpp v161, v153, v173 row_ror:8 row_mask:0xf bank_mask:0xf
	v_mul_f32_dpp v162, v154, v174 row_ror:8 row_mask:0xf bank_mask:0xf
	v_mul_f32_dpp v163, v155, v175 row_ror:8 row_mask:0xf bank_mask:0xf
	v_fmac_f32_e32 v156, v148, v52
	v_fmac_f32_e32 v157, v149, v53
	v_fmac_f32_e32 v158, v150, v54
	v_fmac_f32_e32 v159, v151, v55
	v_fmac_f32_e32 v160, v152, v56
	v_fmac_f32_e32 v161, v153, v57
	v_fmac_f32_e32 v162, v154, v58
	v_fmac_f32_e32 v163, v155, v59
	s_mov_b64 exec, -1
	s_branch .Lpp_ropedone_kk_0

.Lpp_ropedone_kk_0:
	v_cvt_pk_bf16_f32 v156, v156, v157
	v_cvt_pk_bf16_f32 v157, v158, v159
	v_cvt_pk_bf16_f32 v158, v160, v161
	v_cvt_pk_bf16_f32 v159, v162, v163
	s_mov_b64 exec, 0xffffffff
	global_store_dwordx4 v4, v[156:159], s[28:29]
	s_mov_b64 exec, s[66:67]
	global_store_dwordx4 v4, v[156:159], s[30:31]
	s_mov_b64 exec, -1
	v_lshlrev_b32_e32 v148, 16, v48
	v_and_b32_e32 v149, 0xffff0000, v48
	v_lshlrev_b32_e32 v150, 16, v49
	v_and_b32_e32 v151, 0xffff0000, v49
	v_lshlrev_b32_e32 v152, 16, v50
	v_and_b32_e32 v153, 0xffff0000, v50
	v_lshlrev_b32_e32 v154, 16, v51
	v_and_b32_e32 v155, 0xffff0000, v51
	v_mul_f32_e32 v164, v148, v148
	v_fmac_f32_e32 v164, v149, v149
	v_fmac_f32_e32 v164, v150, v150
	v_fmac_f32_e32 v164, v151, v151
	v_fmac_f32_e32 v164, v152, v152
	v_fmac_f32_e32 v164, v153, v153
	v_fmac_f32_e32 v164, v154, v154
	v_fmac_f32_e32 v164, v155, v155
	v_mul_f32_e32 v148, v148, v28
	v_mul_f32_e32 v149, v149, v29
	v_add_f32_dpp v164, v164, v164 quad_perm:[1,0,3,2] row_mask:0xf bank_mask:0xf
	v_mul_f32_e32 v150, v150, v30
	v_mul_f32_e32 v151, v151, v31
	v_add_f32_dpp v164, v164, v164 quad_perm:[2,3,0,1] row_mask:0xf bank_mask:0xf
	v_mul_f32_e32 v152, v152, v32
	v_mul_f32_e32 v153, v153, v33
	v_add_f32_dpp v164, v164, v164 row_half_mirror row_mask:0xf bank_mask:0xf
	v_mul_f32_e32 v154, v154, v34
	v_mul_f32_e32 v155, v155, v35
	v_add_f32_dpp v164, v164, v164 row_mirror row_mask:0xf bank_mask:0xf
	s_nop 0
	v_readlane_b32 s0, v164, 0
	v_readlane_b32 s1, v164, 16
	v_readlane_b32 s2, v164, 32
	v_readlane_b32 s3, v164, 48
	s_nop 1
	v_mov_b32_e32 v166, s0
	v_add_f32_e32 v166, s1, v166
	v_add_f32_e32 v166, s2, v166
	v_add_f32_e32 v166, s3, v166
	v_add_f32_e32 v166, 0x3a0637bd, v166
	v_rsq_f32_e32 v165, v166
	s_nop 0
	v_mul_f32_e32 v148, v148, v165
	v_mul_f32_e32 v149, v149, v165
	v_mul_f32_e32 v150, v150, v165
	v_mul_f32_e32 v151, v151, v165
	v_mul_f32_e32 v152, v152, v165
	v_mul_f32_e32 v153, v153, v165
	v_mul_f32_e32 v154, v154, v165
	v_mul_f32_e32 v155, v155, v165
	v_cvt_pk_bf16_f32 v156, v148, v149
	v_cvt_pk_bf16_f32 v157, v150, v151
	v_cvt_pk_bf16_f32 v158, v152, v153
	v_cvt_pk_bf16_f32 v159, v154, v155
	global_store_dwordx4 v4, v[156:159], s[34:35]
	v_add_f32_e32 v176, v68, v11
	v_mul_f32_e64 v177, |v176|, s47
	v_exp_f32_e32 v177, v177
	s_nop 0
	v_add_f32_e32 v178, 1.0, v177
	v_add_f32_e32 v179, -1.0, v178
	v_log_f32_e32 v180, v178
	v_rcp_f32_e32 v181, v179
	v_cmp_eq_f32_e32 vcc, 0, v179
	s_nop 0
	v_mul_f32_e32 v181, v177, v181
	s_nop 0
	v_cndmask_b32_e64 v181, v181, 1.0, vcc
	v_mul_f32_e32 v180, 0x3f317218, v180
	v_mul_f32_e32 v180, v180, v181
	v_min_f32_e32 v177, 0, v176
	v_sub_f32_e32 v177, v177, v180
	v_cndmask_b32_e64 v177, v176, v177, s[68:69]
	s_mov_b64 exec, 0xffff
	global_store_dword v8, v177, s[44:45]
	s_mov_b64 exec, -1
	s_add_i32 s11, s10, 0x1800
	s_lshr_b32 s0, s11, 8
	s_mul_i32 s0, s0, 57
	s_lshr_b32 s0, s0, 9
	s_mul_i32 s1, s0, 0x900
	s_sub_i32 s43, s11, s1
	s_sub_i32 s0, s43, 0x100
	s_max_i32 s0, s0, 0
	s_mul_i32 s1, s11, 0x2400
	s_add_u32 s12, s48, s1
	s_addc_u32 s13, s49, 0
	s_lshl_b32 s1, s11, 9
	s_add_u32 s14, s50, s1
	s_addc_u32 s15, s51, 0
	s_lshl_b32 s1, s0, 8
	s_add_u32 s16, s52, s1
	s_addc_u32 s17, s53, 0
	s_add_u32 s18, s54, s1
	s_addc_u32 s19, s55, 0
	global_load_dwordx4 v[36:39], v4, s[12:13]
	global_load_dwordx4 v[40:43], v4, s[12:13] offset:1024
	global_load_dwordx4 v[44:47], v5, s[12:13]
	global_load_dwordx4 v[48:51], v4, s[12:13] offset:3072
	global_load_dword v68, v6, s[14:15]
	global_load_dwordx4 v[52:55], v7, s[16:17]
	global_load_dwordx4 v[56:59], v7, s[16:17] offset:16
	global_load_dwordx4 v[60:63], v7, s[18:19]
	global_load_dwordx4 v[64:67], v7, s[18:19] offset:16
	s_waitcnt vmcnt(24)
	s_add_i32 s11, s10, 0x800
	s_lshr_b32 s0, s11, 8
	s_mul_i32 s0, s0, 57
	s_lshr_b32 s0, s0, 9
	s_mul_i32 s1, s0, 0x900
	s_sub_i32 s43, s11, s1
	s_mul_i32 s1, s0, 0x9000
	s_lshl_b32 s2, s43, 2
	s_add_i32 s1, s1, s2
	s_add_u32 s44, s4, s1
	s_addc_u32 s45, s5, 0
	s_lshl_b32 s1, s11, 11
	s_add_u32 s22, s56, s1
	s_addc_u32 s23, s57, 0
	s_lshl_b32 s1, s11, 9
	s_add_u32 s28, s58, s1
	s_addc_u32 s29, s59, 0
	s_add_u32 s30, s62, s1
	s_addc_u32 s31, s63, 0
	s_lshl_b32 s1, s11, 10
	s_add_u32 s34, s64, s1
	s_addc_u32 s35, s65, 0
	v_xor_b32_e32 v168, v9, v94
	v_xor_b32_e32 v169, v9, v95
	v_xor_b32_e32 v170, v9, v96
	v_xor_b32_e32 v171, v9, v97
	v_xor_b32_e32 v172, v9, v98
	v_xor_b32_e32 v173, v9, v99
	v_xor_b32_e32 v174, v9, v100
	v_xor_b32_e32 v175, v9, v101
	s_cmpk_ge_u32 s43, 0x100
	v_lshlrev_b32_e32 v148, 16, v70
	v_and_b32_e32 v149, 0xffff0000, v70
	v_lshlrev_b32_e32 v150, 16, v71
	v_and_b32_e32 v151, 0xffff0000, v71
	v_lshlrev_b32_e32 v152, 16, v72
	v_and_b32_e32 v153, 0xffff0000, v72
	v_lshlrev_b32_e32 v154, 16, v73
	v_and_b32_e32 v155, 0xffff0000, v73
	v_mul_f32_e32 v164, v148, v148
	v_fmac_f32_e32 v164, v149, v149
	v_fmac_f32_e32 v164, v150, v150
	v_fmac_f32_e32 v164, v151, v151
	v_fmac_f32_e32 v164, v152, v152
	v_fmac_f32_e32 v164, v153, v153
	v_fmac_f32_e32 v164, v154, v154
	v_fmac_f32_e32 v164, v155, v155
	v_mul_f32_e32 v148, v148, v12
	v_mul_f32_e32 v149, v149, v13
	v_add_f32_dpp v164, v164, v164 quad_perm:[1,0,3,2] row_mask:0xf bank_mask:0xf
	v_mul_f32_e32 v150, v150, v14
	v_mul_f32_e32 v151, v151, v15
	v_add_f32_dpp v164, v164, v164 quad_perm:[2,3,0,1] row_mask:0xf bank_mask:0xf
	v_mul_f32_e32 v152, v152, v16
	v_mul_f32_e32 v153, v153, v17
	v_add_f32_dpp v164, v164, v164 row_half_mirror row_mask:0xf bank_mask:0xf
	v_mul_f32_e32 v154, v154, v18
	v_mul_f32_e32 v155, v155, v19
	v_add_f32_dpp v164, v164, v164 row_mirror row_mask:0xf bank_mask:0xf
	v_add_f32_e32 v164, 0x390637bd, v164
	v_rsq_f32_e32 v165, v164
	s_nop 0
	v_mul_f32_e32 v148, v148, v165
	v_mul_f32_e32 v149, v149, v165
	v_mul_f32_e32 v150, v150, v165
	v_mul_f32_e32 v151, v151, v165
	v_mul_f32_e32 v152, v152, v165
	v_mul_f32_e32 v153, v153, v165
	v_mul_f32_e32 v154, v154, v165
	v_mul_f32_e32 v155, v155, v165
	s_cbranch_scc0 .Lpp_norope_q0_1
	v_mul_f32_dpp v156, v148, v168 row_ror:8 row_mask:0xf bank_mask:0xf
	v_mul_f32_dpp v157, v149, v169 row_ror:8 row_mask:0xf bank_mask:0xf
	v_mul_f32_dpp v158, v150, v170 row_ror:8 row_mask:0xf bank_mask:0xf
	v_mul_f32_dpp v159, v151, v171 row_ror:8 row_mask:0xf bank_mask:0xf
	v_mul_f32_dpp v160, v152, v172 row_ror:8 row_mask:0xf bank_mask:0xf
	v_mul_f32_dpp v161, v153, v173 row_ror:8 row_mask:0xf bank_mask:0xf
	v_mul_f32_dpp v162, v154, v174 row_ror:8 row_mask:0xf bank_mask:0xf
	v_mul_f32_dpp v163, v155, v175 row_ror:8 row_mask:0xf bank_mask:0xf
	v_fmac_f32_e32 v156, v148, v86
	v_fmac_f32_e32 v157, v149, v87
	v_fmac_f32_e32 v158, v150, v88
	v_fmac_f32_e32 v159, v151, v89
	v_fmac_f32_e32 v160, v152, v90
	v_fmac_f32_e32 v161, v153, v91
	v_fmac_f32_e32 v162, v154, v92
	v_fmac_f32_e32 v163, v155, v93
	s_branch .Lpp_ropedone_q0_1

.Lpp_ropedone_q0_1:
	v_cvt_pk_bf16_f32 v156, v156, v157
	v_cvt_pk_bf16_f32 v157, v158, v159
	v_cvt_pk_bf16_f32 v158, v160, v161
	v_cvt_pk_bf16_f32 v159, v162, v163
	global_store_dwordx4 v4, v[156:159], s[22:23]
	s_nop 1
	v_lshlrev_b32_e32 v148, 16, v74
	v_and_b32_e32 v149, 0xffff0000, v74
	v_lshlrev_b32_e32 v150, 16, v75
	v_and_b32_e32 v151, 0xffff0000, v75
	v_lshlrev_b32_e32 v152, 16, v76
	v_and_b32_e32 v153, 0xffff0000, v76
	v_lshlrev_b32_e32 v154, 16, v77
	v_and_b32_e32 v155, 0xffff0000, v77
	v_mul_f32_e32 v164, v148, v148
	v_fmac_f32_e32 v164, v149, v149
	v_fmac_f32_e32 v164, v150, v150
	v_fmac_f32_e32 v164, v151, v151
	v_fmac_f32_e32 v164, v152, v152
	v_fmac_f32_e32 v164, v153, v153
	v_fmac_f32_e32 v164, v154, v154
	v_fmac_f32_e32 v164, v155, v155
	v_mul_f32_e32 v148, v148, v12
	v_mul_f32_e32 v149, v149, v13
	v_add_f32_dpp v164, v164, v164 quad_perm:[1,0,3,2] row_mask:0xf bank_mask:0xf
	v_mul_f32_e32 v150, v150, v14
	v_mul_f32_e32 v151, v151, v15
	v_add_f32_dpp v164, v164, v164 quad_perm:[2,3,0,1] row_mask:0xf bank_mask:0xf
	v_mul_f32_e32 v152, v152, v16
	v_mul_f32_e32 v153, v153, v17
	v_add_f32_dpp v164, v164, v164 row_half_mirror row_mask:0xf bank_mask:0xf
	v_mul_f32_e32 v154, v154, v18
	v_mul_f32_e32 v155, v155, v19
	v_add_f32_dpp v164, v164, v164 row_mirror row_mask:0xf bank_mask:0xf
	v_add_f32_e32 v164, 0x390637bd, v164
	v_rsq_f32_e32 v165, v164
	s_nop 0
	v_mul_f32_e32 v148, v148, v165
	v_mul_f32_e32 v149, v149, v165
	v_mul_f32_e32 v150, v150, v165
	v_mul_f32_e32 v151, v151, v165
	v_mul_f32_e32 v152, v152, v165
	v_mul_f32_e32 v153, v153, v165
	v_mul_f32_e32 v154, v154, v165
	v_mul_f32_e32 v155, v155, v165
	s_cbranch_scc0 .Lpp_norope_q1_1
	v_mul_f32_dpp v156, v148, v168 row_ror:8 row_mask:0xf bank_mask:0xf
	v_mul_f32_dpp v157, v149, v169 row_ror:8 row_mask:0xf bank_mask:0xf
	v_mul_f32_dpp v158, v150, v170 row_ror:8 row_mask:0xf bank_mask:0xf
	v_mul_f32_dpp v159, v151, v171 row_ror:8 row_mask:0xf bank_mask:0xf
	v_mul_f32_dpp v160, v152, v172 row_ror:8 row_mask:0xf bank_mask:0xf
	v_mul_f32_dpp v161, v153, v173 row_ror:8 row_mask:0xf bank_mask:0xf
	v_mul_f32_dpp v162, v154, v174 row_ror:8 row_mask:0xf bank_mask:0xf
	v_mul_f32_dpp v163, v155, v175 row_ror:8 row_mask:0xf bank_mask:0xf
	v_fmac_f32_e32 v156, v148, v86
	v_fmac_f32_e32 v157, v149, v87
	v_fmac_f32_e32 v158, v150, v88
	v_fmac_f32_e32 v159, v151, v89
	v_fmac_f32_e32 v160, v152, v90
	v_fmac_f32_e32 v161, v153, v91
	v_fmac_f32_e32 v162, v154, v92
	v_fmac_f32_e32 v163, v155, v93
	s_branch .Lpp_ropedone_q1_1

.Lpp_ropedone_q1_1:
	v_cvt_pk_bf16_f32 v156, v156, v157
	v_cvt_pk_bf16_f32 v157, v158, v159
	v_cvt_pk_bf16_f32 v158, v160, v161
	v_cvt_pk_bf16_f32 v159, v162, v163
	global_store_dwordx4 v4, v[156:159], s[22:23] offset:1024
	s_nop 1
	v_lshlrev_b32_e32 v148, 16, v78
	v_and_b32_e32 v149, 0xffff0000, v78
	v_lshlrev_b32_e32 v150, 16, v79
	v_and_b32_e32 v151, 0xffff0000, v79
	v_lshlrev_b32_e32 v152, 16, v80
	v_and_b32_e32 v153, 0xffff0000, v80
	v_lshlrev_b32_e32 v154, 16, v81
	v_and_b32_e32 v155, 0xffff0000, v81
	v_mul_f32_e32 v164, v148, v148
	v_fmac_f32_e32 v164, v149, v149
	v_fmac_f32_e32 v164, v150, v150
	v_fmac_f32_e32 v164, v151, v151
	v_fmac_f32_e32 v164, v152, v152
	v_fmac_f32_e32 v164, v153, v153
	v_fmac_f32_e32 v164, v154, v154
	v_fmac_f32_e32 v164, v155, v155
	v_mul_f32_e32 v148, v148, v20
	v_mul_f32_e32 v149, v149, v21
	v_add_f32_dpp v164, v164, v164 quad_perm:[1,0,3,2] row_mask:0xf bank_mask:0xf
	v_mul_f32_e32 v150, v150, v22
	v_mul_f32_e32 v151, v151, v23
	v_add_f32_dpp v164, v164, v164 quad_perm:[2,3,0,1] row_mask:0xf bank_mask:0xf
	v_mul_f32_e32 v152, v152, v24
	v_mul_f32_e32 v153, v153, v25
	v_add_f32_dpp v164, v164, v164 row_half_mirror row_mask:0xf bank_mask:0xf
	v_mul_f32_e32 v154, v154, v26
	v_mul_f32_e32 v155, v155, v27
	v_add_f32_dpp v164, v164, v164 row_mirror row_mask:0xf bank_mask:0xf
	s_nop 0
	v_readlane_b32 s0, v164, 32
	v_readlane_b32 s1, v164, 48
	v_add_f32_e32 v176, 0x390637bd, v164
	s_nop 1
	v_mov_b32_e32 v166, s0
	v_add_f32_e32 v166, s1, v166
	v_add_f32_e32 v166, 0x398637bd, v166
	v_cndmask_b32_e64 v176, v176, v166, s[66:67]
	v_rsq_f32_e32 v165, v176
	s_nop 0
	v_mul_f32_e32 v148, v148, v165
	v_mul_f32_e32 v149, v149, v165
	v_mul_f32_e32 v150, v150, v165
	v_mul_f32_e32 v151, v151, v165
	v_mul_f32_e32 v152, v152, v165
	v_mul_f32_e32 v153, v153, v165
	v_mul_f32_e32 v154, v154, v165
	v_mul_f32_e32 v155, v155, v165
	s_cbranch_scc0 .Lpp_norope_kk_1
	v_mov_b32_e32 v156, v148
	v_mov_b32_e32 v157, v149
	v_mov_b32_e32 v158, v150
	v_mov_b32_e32 v159, v151
	v_mov_b32_e32 v160, v152
	v_mov_b32_e32 v161, v153
	v_mov_b32_e32 v162, v154
	v_mov_b32_e32 v163, v155
	s_mov_b64 exec, 0xffffffff
	s_nop 4
	v_mul_f32_dpp v156, v148, v168 row_ror:8 row_mask:0xf bank_mask:0xf
	v_mul_f32_dpp v157, v149, v169 row_ror:8 row_mask:0xf bank_mask:0xf
	v_mul_f32_dpp v158, v150, v170 row_ror:8 row_mask:0xf bank_mask:0xf
	v_mul_f32_dpp v159, v151, v171 row_ror:8 row_mask:0xf bank_mask:0xf
	v_mul_f32_dpp v160, v152, v172 row_ror:8 row_mask:0xf bank_mask:0xf
	v_mul_f32_dpp v161, v153, v173 row_ror:8 row_mask:0xf bank_mask:0xf
	v_mul_f32_dpp v162, v154, v174 row_ror:8 row_mask:0xf bank_mask:0xf
	v_mul_f32_dpp v163, v155, v175 row_ror:8 row_mask:0xf bank_mask:0xf
	v_fmac_f32_e32 v156, v148, v86
	v_fmac_f32_e32 v157, v149, v87
	v_fmac_f32_e32 v158, v150, v88
	v_fmac_f32_e32 v159, v151, v89
	v_fmac_f32_e32 v160, v152, v90
	v_fmac_f32_e32 v161, v153, v91
	v_fmac_f32_e32 v162, v154, v92
	v_fmac_f32_e32 v163, v155, v93
	s_mov_b64 exec, -1
	s_branch .Lpp_ropedone_kk_1

.Lpp_ropedone_kk_1:
	v_cvt_pk_bf16_f32 v156, v156, v157
	v_cvt_pk_bf16_f32 v157, v158, v159
	v_cvt_pk_bf16_f32 v158, v160, v161
	v_cvt_pk_bf16_f32 v159, v162, v163
	s_mov_b64 exec, 0xffffffff
	global_store_dwordx4 v4, v[156:159], s[28:29]
	s_mov_b64 exec, s[66:67]
	global_store_dwordx4 v4, v[156:159], s[30:31]
	s_mov_b64 exec, -1
	v_lshlrev_b32_e32 v148, 16, v82
	v_and_b32_e32 v149, 0xffff0000, v82
	v_lshlrev_b32_e32 v150, 16, v83
	v_and_b32_e32 v151, 0xffff0000, v83
	v_lshlrev_b32_e32 v152, 16, v84
	v_and_b32_e32 v153, 0xffff0000, v84
	v_lshlrev_b32_e32 v154, 16, v85
	v_and_b32_e32 v155, 0xffff0000, v85
	v_mul_f32_e32 v164, v148, v148
	v_fmac_f32_e32 v164, v149, v149
	v_fmac_f32_e32 v164, v150, v150
	v_fmac_f32_e32 v164, v151, v151
	v_fmac_f32_e32 v164, v152, v152
	v_fmac_f32_e32 v164, v153, v153
	v_fmac_f32_e32 v164, v154, v154
	v_fmac_f32_e32 v164, v155, v155
	v_mul_f32_e32 v148, v148, v28
	v_mul_f32_e32 v149, v149, v29
	v_add_f32_dpp v164, v164, v164 quad_perm:[1,0,3,2] row_mask:0xf bank_mask:0xf
	v_mul_f32_e32 v150, v150, v30
	v_mul_f32_e32 v151, v151, v31
	v_add_f32_dpp v164, v164, v164 quad_perm:[2,3,0,1] row_mask:0xf bank_mask:0xf
	v_mul_f32_e32 v152, v152, v32
	v_mul_f32_e32 v153, v153, v33
	v_add_f32_dpp v164, v164, v164 row_half_mirror row_mask:0xf bank_mask:0xf
	v_mul_f32_e32 v154, v154, v34
	v_mul_f32_e32 v155, v155, v35
	v_add_f32_dpp v164, v164, v164 row_mirror row_mask:0xf bank_mask:0xf
	s_nop 0
	v_readlane_b32 s0, v164, 0
	v_readlane_b32 s1, v164, 16
	v_readlane_b32 s2, v164, 32
	v_readlane_b32 s3, v164, 48
	s_nop 1
	v_mov_b32_e32 v166, s0
	v_add_f32_e32 v166, s1, v166
	v_add_f32_e32 v166, s2, v166
	v_add_f32_e32 v166, s3, v166
	v_add_f32_e32 v166, 0x3a0637bd, v166
	v_rsq_f32_e32 v165, v166
	s_nop 0
	v_mul_f32_e32 v148, v148, v165
	v_mul_f32_e32 v149, v149, v165
	v_mul_f32_e32 v150, v150, v165
	v_mul_f32_e32 v151, v151, v165
	v_mul_f32_e32 v152, v152, v165
	v_mul_f32_e32 v153, v153, v165
	v_mul_f32_e32 v154, v154, v165
	v_mul_f32_e32 v155, v155, v165
	v_cvt_pk_bf16_f32 v156, v148, v149
	v_cvt_pk_bf16_f32 v157, v150, v151
	v_cvt_pk_bf16_f32 v158, v152, v153
	v_cvt_pk_bf16_f32 v159, v154, v155
	global_store_dwordx4 v4, v[156:159], s[34:35]
	v_add_f32_e32 v176, v102, v11
	v_mul_f32_e64 v177, |v176|, s47
	v_exp_f32_e32 v177, v177
	s_nop 0
	v_add_f32_e32 v178, 1.0, v177
	v_add_f32_e32 v179, -1.0, v178
	v_log_f32_e32 v180, v178
	v_rcp_f32_e32 v181, v179
	v_cmp_eq_f32_e32 vcc, 0, v179
	s_nop 0
	v_mul_f32_e32 v181, v177, v181
	s_nop 0
	v_cndmask_b32_e64 v181, v181, 1.0, vcc
	v_mul_f32_e32 v180, 0x3f317218, v180
	v_mul_f32_e32 v180, v180, v181
	v_min_f32_e32 v177, 0, v176
	v_sub_f32_e32 v177, v177, v180
	v_cndmask_b32_e64 v177, v176, v177, s[68:69]
	s_mov_b64 exec, 0xffff
	global_store_dword v8, v177, s[44:45]
	s_mov_b64 exec, -1
	s_add_i32 s11, s10, 0x2000
	s_lshr_b32 s0, s11, 8
	s_mul_i32 s0, s0, 57
	s_lshr_b32 s0, s0, 9
	s_mul_i32 s1, s0, 0x900
	s_sub_i32 s43, s11, s1
	s_sub_i32 s0, s43, 0x100
	s_max_i32 s0, s0, 0
	s_mul_i32 s1, s11, 0x2400
	s_add_u32 s12, s48, s1
	s_addc_u32 s13, s49, 0
	s_lshl_b32 s1, s11, 9
	s_add_u32 s14, s50, s1
	s_addc_u32 s15, s51, 0
	s_lshl_b32 s1, s0, 8
	s_add_u32 s16, s52, s1
	s_addc_u32 s17, s53, 0
	s_add_u32 s18, s54, s1
	s_addc_u32 s19, s55, 0
	global_load_dwordx4 v[70:73], v4, s[12:13]
	global_load_dwordx4 v[74:77], v4, s[12:13] offset:1024
	global_load_dwordx4 v[78:81], v5, s[12:13]
	global_load_dwordx4 v[82:85], v4, s[12:13] offset:3072
	global_load_dword v102, v6, s[14:15]
	global_load_dwordx4 v[86:89], v7, s[16:17]
	global_load_dwordx4 v[90:93], v7, s[16:17] offset:16
	global_load_dwordx4 v[94:97], v7, s[18:19]
	global_load_dwordx4 v[98:101], v7, s[18:19] offset:16
	s_waitcnt vmcnt(30)
	s_add_i32 s11, s10, 0x1000
	s_lshr_b32 s0, s11, 8
	s_mul_i32 s0, s0, 57
	s_lshr_b32 s0, s0, 9
	s_mul_i32 s1, s0, 0x900
	s_sub_i32 s43, s11, s1
	s_mul_i32 s1, s0, 0x9000
	s_lshl_b32 s2, s43, 2
	s_add_i32 s1, s1, s2
	s_add_u32 s44, s4, s1
	s_addc_u32 s45, s5, 0
	s_lshl_b32 s1, s11, 11
	s_add_u32 s22, s56, s1
	s_addc_u32 s23, s57, 0
	s_lshl_b32 s1, s11, 9
	s_add_u32 s28, s58, s1
	s_addc_u32 s29, s59, 0
	s_add_u32 s30, s62, s1
	s_addc_u32 s31, s63, 0
	s_lshl_b32 s1, s11, 10
	s_add_u32 s34, s64, s1
	s_addc_u32 s35, s65, 0
	v_xor_b32_e32 v168, v9, v128
	v_xor_b32_e32 v169, v9, v129
	v_xor_b32_e32 v170, v9, v130
	v_xor_b32_e32 v171, v9, v131
	v_xor_b32_e32 v172, v9, v132
	v_xor_b32_e32 v173, v9, v133
	v_xor_b32_e32 v174, v9, v134
	v_xor_b32_e32 v175, v9, v135
	s_cmpk_ge_u32 s43, 0x100
	v_lshlrev_b32_e32 v148, 16, v104
	v_and_b32_e32 v149, 0xffff0000, v104
	v_lshlrev_b32_e32 v150, 16, v105
	v_and_b32_e32 v151, 0xffff0000, v105
	v_lshlrev_b32_e32 v152, 16, v106
	v_and_b32_e32 v153, 0xffff0000, v106
	v_lshlrev_b32_e32 v154, 16, v107
	v_and_b32_e32 v155, 0xffff0000, v107
	v_mul_f32_e32 v164, v148, v148
	v_fmac_f32_e32 v164, v149, v149
	v_fmac_f32_e32 v164, v150, v150
	v_fmac_f32_e32 v164, v151, v151
	v_fmac_f32_e32 v164, v152, v152
	v_fmac_f32_e32 v164, v153, v153
	v_fmac_f32_e32 v164, v154, v154
	v_fmac_f32_e32 v164, v155, v155
	v_mul_f32_e32 v148, v148, v12
	v_mul_f32_e32 v149, v149, v13
	v_add_f32_dpp v164, v164, v164 quad_perm:[1,0,3,2] row_mask:0xf bank_mask:0xf
	v_mul_f32_e32 v150, v150, v14
	v_mul_f32_e32 v151, v151, v15
	v_add_f32_dpp v164, v164, v164 quad_perm:[2,3,0,1] row_mask:0xf bank_mask:0xf
	v_mul_f32_e32 v152, v152, v16
	v_mul_f32_e32 v153, v153, v17
	v_add_f32_dpp v164, v164, v164 row_half_mirror row_mask:0xf bank_mask:0xf
	v_mul_f32_e32 v154, v154, v18
	v_mul_f32_e32 v155, v155, v19
	v_add_f32_dpp v164, v164, v164 row_mirror row_mask:0xf bank_mask:0xf
	v_add_f32_e32 v164, 0x390637bd, v164
	v_rsq_f32_e32 v165, v164
	s_nop 0
	v_mul_f32_e32 v148, v148, v165
	v_mul_f32_e32 v149, v149, v165
	v_mul_f32_e32 v150, v150, v165
	v_mul_f32_e32 v151, v151, v165
	v_mul_f32_e32 v152, v152, v165
	v_mul_f32_e32 v153, v153, v165
	v_mul_f32_e32 v154, v154, v165
	v_mul_f32_e32 v155, v155, v165
	s_cbranch_scc0 .Lpp_norope_q0_2
	v_mul_f32_dpp v156, v148, v168 row_ror:8 row_mask:0xf bank_mask:0xf
	v_mul_f32_dpp v157, v149, v169 row_ror:8 row_mask:0xf bank_mask:0xf
	v_mul_f32_dpp v158, v150, v170 row_ror:8 row_mask:0xf bank_mask:0xf
	v_mul_f32_dpp v159, v151, v171 row_ror:8 row_mask:0xf bank_mask:0xf
	v_mul_f32_dpp v160, v152, v172 row_ror:8 row_mask:0xf bank_mask:0xf
	v_mul_f32_dpp v161, v153, v173 row_ror:8 row_mask:0xf bank_mask:0xf
	v_mul_f32_dpp v162, v154, v174 row_ror:8 row_mask:0xf bank_mask:0xf
	v_mul_f32_dpp v163, v155, v175 row_ror:8 row_mask:0xf bank_mask:0xf
	v_fmac_f32_e32 v156, v148, v120
	v_fmac_f32_e32 v157, v149, v121
	v_fmac_f32_e32 v158, v150, v122
	v_fmac_f32_e32 v159, v151, v123
	v_fmac_f32_e32 v160, v152, v124
	v_fmac_f32_e32 v161, v153, v125
	v_fmac_f32_e32 v162, v154, v126
	v_fmac_f32_e32 v163, v155, v127
	s_branch .Lpp_ropedone_q0_2

.Lpp_ropedone_q0_2:
	v_cvt_pk_bf16_f32 v156, v156, v157
	v_cvt_pk_bf16_f32 v157, v158, v159
	v_cvt_pk_bf16_f32 v158, v160, v161
	v_cvt_pk_bf16_f32 v159, v162, v163
	global_store_dwordx4 v4, v[156:159], s[22:23]
	s_nop 1
	v_lshlrev_b32_e32 v148, 16, v108
	v_and_b32_e32 v149, 0xffff0000, v108
	v_lshlrev_b32_e32 v150, 16, v109
	v_and_b32_e32 v151, 0xffff0000, v109
	v_lshlrev_b32_e32 v152, 16, v110
	v_and_b32_e32 v153, 0xffff0000, v110
	v_lshlrev_b32_e32 v154, 16, v111
	v_and_b32_e32 v155, 0xffff0000, v111
	v_mul_f32_e32 v164, v148, v148
	v_fmac_f32_e32 v164, v149, v149
	v_fmac_f32_e32 v164, v150, v150
	v_fmac_f32_e32 v164, v151, v151
	v_fmac_f32_e32 v164, v152, v152
	v_fmac_f32_e32 v164, v153, v153
	v_fmac_f32_e32 v164, v154, v154
	v_fmac_f32_e32 v164, v155, v155
	v_mul_f32_e32 v148, v148, v12
	v_mul_f32_e32 v149, v149, v13
	v_add_f32_dpp v164, v164, v164 quad_perm:[1,0,3,2] row_mask:0xf bank_mask:0xf
	v_mul_f32_e32 v150, v150, v14
	v_mul_f32_e32 v151, v151, v15
	v_add_f32_dpp v164, v164, v164 quad_perm:[2,3,0,1] row_mask:0xf bank_mask:0xf
	v_mul_f32_e32 v152, v152, v16
	v_mul_f32_e32 v153, v153, v17
	v_add_f32_dpp v164, v164, v164 row_half_mirror row_mask:0xf bank_mask:0xf
	v_mul_f32_e32 v154, v154, v18
	v_mul_f32_e32 v155, v155, v19
	v_add_f32_dpp v164, v164, v164 row_mirror row_mask:0xf bank_mask:0xf
	v_add_f32_e32 v164, 0x390637bd, v164
	v_rsq_f32_e32 v165, v164
	s_nop 0
	v_mul_f32_e32 v148, v148, v165
	v_mul_f32_e32 v149, v149, v165
	v_mul_f32_e32 v150, v150, v165
	v_mul_f32_e32 v151, v151, v165
	v_mul_f32_e32 v152, v152, v165
	v_mul_f32_e32 v153, v153, v165
	v_mul_f32_e32 v154, v154, v165
	v_mul_f32_e32 v155, v155, v165
	s_cbranch_scc0 .Lpp_norope_q1_2
	v_mul_f32_dpp v156, v148, v168 row_ror:8 row_mask:0xf bank_mask:0xf
	v_mul_f32_dpp v157, v149, v169 row_ror:8 row_mask:0xf bank_mask:0xf
	v_mul_f32_dpp v158, v150, v170 row_ror:8 row_mask:0xf bank_mask:0xf
	v_mul_f32_dpp v159, v151, v171 row_ror:8 row_mask:0xf bank_mask:0xf
	v_mul_f32_dpp v160, v152, v172 row_ror:8 row_mask:0xf bank_mask:0xf
	v_mul_f32_dpp v161, v153, v173 row_ror:8 row_mask:0xf bank_mask:0xf
	v_mul_f32_dpp v162, v154, v174 row_ror:8 row_mask:0xf bank_mask:0xf
	v_mul_f32_dpp v163, v155, v175 row_ror:8 row_mask:0xf bank_mask:0xf
	v_fmac_f32_e32 v156, v148, v120
	v_fmac_f32_e32 v157, v149, v121
	v_fmac_f32_e32 v158, v150, v122
	v_fmac_f32_e32 v159, v151, v123
	v_fmac_f32_e32 v160, v152, v124
	v_fmac_f32_e32 v161, v153, v125
	v_fmac_f32_e32 v162, v154, v126
	v_fmac_f32_e32 v163, v155, v127
	s_branch .Lpp_ropedone_q1_2

.Lpp_ropedone_q1_2:
	v_cvt_pk_bf16_f32 v156, v156, v157
	v_cvt_pk_bf16_f32 v157, v158, v159
	v_cvt_pk_bf16_f32 v158, v160, v161
	v_cvt_pk_bf16_f32 v159, v162, v163
	global_store_dwordx4 v4, v[156:159], s[22:23] offset:1024
	s_nop 1
	v_lshlrev_b32_e32 v148, 16, v112
	v_and_b32_e32 v149, 0xffff0000, v112
	v_lshlrev_b32_e32 v150, 16, v113
	v_and_b32_e32 v151, 0xffff0000, v113
	v_lshlrev_b32_e32 v152, 16, v114
	v_and_b32_e32 v153, 0xffff0000, v114
	v_lshlrev_b32_e32 v154, 16, v115
	v_and_b32_e32 v155, 0xffff0000, v115
	v_mul_f32_e32 v164, v148, v148
	v_fmac_f32_e32 v164, v149, v149
	v_fmac_f32_e32 v164, v150, v150
	v_fmac_f32_e32 v164, v151, v151
	v_fmac_f32_e32 v164, v152, v152
	v_fmac_f32_e32 v164, v153, v153
	v_fmac_f32_e32 v164, v154, v154
	v_fmac_f32_e32 v164, v155, v155
	v_mul_f32_e32 v148, v148, v20
	v_mul_f32_e32 v149, v149, v21
	v_add_f32_dpp v164, v164, v164 quad_perm:[1,0,3,2] row_mask:0xf bank_mask:0xf
	v_mul_f32_e32 v150, v150, v22
	v_mul_f32_e32 v151, v151, v23
	v_add_f32_dpp v164, v164, v164 quad_perm:[2,3,0,1] row_mask:0xf bank_mask:0xf
	v_mul_f32_e32 v152, v152, v24
	v_mul_f32_e32 v153, v153, v25
	v_add_f32_dpp v164, v164, v164 row_half_mirror row_mask:0xf bank_mask:0xf
	v_mul_f32_e32 v154, v154, v26
	v_mul_f32_e32 v155, v155, v27
	v_add_f32_dpp v164, v164, v164 row_mirror row_mask:0xf bank_mask:0xf
	s_nop 0
	v_readlane_b32 s0, v164, 32
	v_readlane_b32 s1, v164, 48
	v_add_f32_e32 v176, 0x390637bd, v164
	s_nop 1
	v_mov_b32_e32 v166, s0
	v_add_f32_e32 v166, s1, v166
	v_add_f32_e32 v166, 0x398637bd, v166
	v_cndmask_b32_e64 v176, v176, v166, s[66:67]
	v_rsq_f32_e32 v165, v176
	s_nop 0
	v_mul_f32_e32 v148, v148, v165
	v_mul_f32_e32 v149, v149, v165
	v_mul_f32_e32 v150, v150, v165
	v_mul_f32_e32 v151, v151, v165
	v_mul_f32_e32 v152, v152, v165
	v_mul_f32_e32 v153, v153, v165
	v_mul_f32_e32 v154, v154, v165
	v_mul_f32_e32 v155, v155, v165
	s_cbranch_scc0 .Lpp_norope_kk_2
	v_mov_b32_e32 v156, v148
	v_mov_b32_e32 v157, v149
	v_mov_b32_e32 v158, v150
	v_mov_b32_e32 v159, v151
	v_mov_b32_e32 v160, v152
	v_mov_b32_e32 v161, v153
	v_mov_b32_e32 v162, v154
	v_mov_b32_e32 v163, v155
	s_mov_b64 exec, 0xffffffff
	s_nop 4
	v_mul_f32_dpp v156, v148, v168 row_ror:8 row_mask:0xf bank_mask:0xf
	v_mul_f32_dpp v157, v149, v169 row_ror:8 row_mask:0xf bank_mask:0xf
	v_mul_f32_dpp v158, v150, v170 row_ror:8 row_mask:0xf bank_mask:0xf
	v_mul_f32_dpp v159, v151, v171 row_ror:8 row_mask:0xf bank_mask:0xf
	v_mul_f32_dpp v160, v152, v172 row_ror:8 row_mask:0xf bank_mask:0xf
	v_mul_f32_dpp v161, v153, v173 row_ror:8 row_mask:0xf bank_mask:0xf
	v_mul_f32_dpp v162, v154, v174 row_ror:8 row_mask:0xf bank_mask:0xf
	v_mul_f32_dpp v163, v155, v175 row_ror:8 row_mask:0xf bank_mask:0xf
	v_fmac_f32_e32 v156, v148, v120
	v_fmac_f32_e32 v157, v149, v121
	v_fmac_f32_e32 v158, v150, v122
	v_fmac_f32_e32 v159, v151, v123
	v_fmac_f32_e32 v160, v152, v124
	v_fmac_f32_e32 v161, v153, v125
	v_fmac_f32_e32 v162, v154, v126
	v_fmac_f32_e32 v163, v155, v127
	s_mov_b64 exec, -1
	s_branch .Lpp_ropedone_kk_2

.Lpp_ropedone_kk_2:
	v_cvt_pk_bf16_f32 v156, v156, v157
	v_cvt_pk_bf16_f32 v157, v158, v159
	v_cvt_pk_bf16_f32 v158, v160, v161
	v_cvt_pk_bf16_f32 v159, v162, v163
	s_mov_b64 exec, 0xffffffff
	global_store_dwordx4 v4, v[156:159], s[28:29]
	s_mov_b64 exec, s[66:67]
	global_store_dwordx4 v4, v[156:159], s[30:31]
	s_mov_b64 exec, -1
	v_lshlrev_b32_e32 v148, 16, v116
	v_and_b32_e32 v149, 0xffff0000, v116
	v_lshlrev_b32_e32 v150, 16, v117
	v_and_b32_e32 v151, 0xffff0000, v117
	v_lshlrev_b32_e32 v152, 16, v118
	v_and_b32_e32 v153, 0xffff0000, v118
	v_lshlrev_b32_e32 v154, 16, v119
	v_and_b32_e32 v155, 0xffff0000, v119
	v_mul_f32_e32 v164, v148, v148
	v_fmac_f32_e32 v164, v149, v149
	v_fmac_f32_e32 v164, v150, v150
	v_fmac_f32_e32 v164, v151, v151
	v_fmac_f32_e32 v164, v152, v152
	v_fmac_f32_e32 v164, v153, v153
	v_fmac_f32_e32 v164, v154, v154
	v_fmac_f32_e32 v164, v155, v155
	v_mul_f32_e32 v148, v148, v28
	v_mul_f32_e32 v149, v149, v29
	v_add_f32_dpp v164, v164, v164 quad_perm:[1,0,3,2] row_mask:0xf bank_mask:0xf
	v_mul_f32_e32 v150, v150, v30
	v_mul_f32_e32 v151, v151, v31
	v_add_f32_dpp v164, v164, v164 quad_perm:[2,3,0,1] row_mask:0xf bank_mask:0xf
	v_mul_f32_e32 v152, v152, v32
	v_mul_f32_e32 v153, v153, v33
	v_add_f32_dpp v164, v164, v164 row_half_mirror row_mask:0xf bank_mask:0xf
	v_mul_f32_e32 v154, v154, v34
	v_mul_f32_e32 v155, v155, v35
	v_add_f32_dpp v164, v164, v164 row_mirror row_mask:0xf bank_mask:0xf
	s_nop 0
	v_readlane_b32 s0, v164, 0
	v_readlane_b32 s1, v164, 16
	v_readlane_b32 s2, v164, 32
	v_readlane_b32 s3, v164, 48
	s_nop 1
	v_mov_b32_e32 v166, s0
	v_add_f32_e32 v166, s1, v166
	v_add_f32_e32 v166, s2, v166
	v_add_f32_e32 v166, s3, v166
	v_add_f32_e32 v166, 0x3a0637bd, v166
	v_rsq_f32_e32 v165, v166
	s_nop 0
	v_mul_f32_e32 v148, v148, v165
	v_mul_f32_e32 v149, v149, v165
	v_mul_f32_e32 v150, v150, v165
	v_mul_f32_e32 v151, v151, v165
	v_mul_f32_e32 v152, v152, v165
	v_mul_f32_e32 v153, v153, v165
	v_mul_f32_e32 v154, v154, v165
	v_mul_f32_e32 v155, v155, v165
	v_cvt_pk_bf16_f32 v156, v148, v149
	v_cvt_pk_bf16_f32 v157, v150, v151
	v_cvt_pk_bf16_f32 v158, v152, v153
	v_cvt_pk_bf16_f32 v159, v154, v155
	global_store_dwordx4 v4, v[156:159], s[34:35]
	v_add_f32_e32 v176, v136, v11
	v_mul_f32_e64 v177, |v176|, s47
	v_exp_f32_e32 v177, v177
	s_nop 0
	v_add_f32_e32 v178, 1.0, v177
	v_add_f32_e32 v179, -1.0, v178
	v_log_f32_e32 v180, v178
	v_rcp_f32_e32 v181, v179
	v_cmp_eq_f32_e32 vcc, 0, v179
	s_nop 0
	v_mul_f32_e32 v181, v177, v181
	s_nop 0
	v_cndmask_b32_e64 v181, v181, 1.0, vcc
	v_mul_f32_e32 v180, 0x3f317218, v180
	v_mul_f32_e32 v180, v180, v181
	v_min_f32_e32 v177, 0, v176
	v_sub_f32_e32 v177, v177, v180
	v_cndmask_b32_e64 v177, v176, v177, s[68:69]
	s_mov_b64 exec, 0xffff
	global_store_dword v8, v177, s[44:45]
	s_mov_b64 exec, -1
	s_add_i32 s11, s10, 0x2800
	s_lshr_b32 s0, s11, 8
	s_mul_i32 s0, s0, 57
	s_lshr_b32 s0, s0, 9
	s_mul_i32 s1, s0, 0x900
	s_sub_i32 s43, s11, s1
	s_sub_i32 s0, s43, 0x100
	s_max_i32 s0, s0, 0
	s_mul_i32 s1, s11, 0x2400
	s_add_u32 s12, s48, s1
	s_addc_u32 s13, s49, 0
	s_lshl_b32 s1, s11, 9
	s_add_u32 s14, s50, s1
	s_addc_u32 s15, s51, 0
	s_lshl_b32 s1, s0, 8
	s_add_u32 s16, s52, s1
	s_addc_u32 s17, s53, 0
	s_add_u32 s18, s54, s1
	s_addc_u32 s19, s55, 0
	global_load_dwordx4 v[104:107], v4, s[12:13]
	global_load_dwordx4 v[108:111], v4, s[12:13] offset:1024
	global_load_dwordx4 v[112:115], v5, s[12:13]
	global_load_dwordx4 v[116:119], v4, s[12:13] offset:3072
	global_load_dword v136, v6, s[14:15]
	global_load_dwordx4 v[120:123], v7, s[16:17]
	global_load_dwordx4 v[124:127], v7, s[16:17] offset:16
	global_load_dwordx4 v[128:131], v7, s[18:19]
	global_load_dwordx4 v[132:135], v7, s[18:19] offset:16
	s_waitcnt vmcnt(30)
	s_add_i32 s11, s10, 0x1800
	s_lshr_b32 s0, s11, 8
	s_mul_i32 s0, s0, 57
	s_lshr_b32 s0, s0, 9
	s_mul_i32 s1, s0, 0x900
	s_sub_i32 s43, s11, s1
	s_mul_i32 s1, s0, 0x9000
	s_lshl_b32 s2, s43, 2
	s_add_i32 s1, s1, s2
	s_add_u32 s44, s4, s1
	s_addc_u32 s45, s5, 0
	s_lshl_b32 s1, s11, 11
	s_add_u32 s22, s56, s1
	s_addc_u32 s23, s57, 0
	s_lshl_b32 s1, s11, 9
	s_add_u32 s28, s58, s1
	s_addc_u32 s29, s59, 0
	s_add_u32 s30, s62, s1
	s_addc_u32 s31, s63, 0
	s_lshl_b32 s1, s11, 10
	s_add_u32 s34, s64, s1
	s_addc_u32 s35, s65, 0
	v_xor_b32_e32 v168, v9, v60
	v_xor_b32_e32 v169, v9, v61
	v_xor_b32_e32 v170, v9, v62
	v_xor_b32_e32 v171, v9, v63
	v_xor_b32_e32 v172, v9, v64
	v_xor_b32_e32 v173, v9, v65
	v_xor_b32_e32 v174, v9, v66
	v_xor_b32_e32 v175, v9, v67
	s_cmpk_ge_u32 s43, 0x100
	v_lshlrev_b32_e32 v148, 16, v36
	v_and_b32_e32 v149, 0xffff0000, v36
	v_lshlrev_b32_e32 v150, 16, v37
	v_and_b32_e32 v151, 0xffff0000, v37
	v_lshlrev_b32_e32 v152, 16, v38
	v_and_b32_e32 v153, 0xffff0000, v38
	v_lshlrev_b32_e32 v154, 16, v39
	v_and_b32_e32 v155, 0xffff0000, v39
	v_mul_f32_e32 v164, v148, v148
	v_fmac_f32_e32 v164, v149, v149
	v_fmac_f32_e32 v164, v150, v150
	v_fmac_f32_e32 v164, v151, v151
	v_fmac_f32_e32 v164, v152, v152
	v_fmac_f32_e32 v164, v153, v153
	v_fmac_f32_e32 v164, v154, v154
	v_fmac_f32_e32 v164, v155, v155
	v_mul_f32_e32 v148, v148, v12
	v_mul_f32_e32 v149, v149, v13
	v_add_f32_dpp v164, v164, v164 quad_perm:[1,0,3,2] row_mask:0xf bank_mask:0xf
	v_mul_f32_e32 v150, v150, v14
	v_mul_f32_e32 v151, v151, v15
	v_add_f32_dpp v164, v164, v164 quad_perm:[2,3,0,1] row_mask:0xf bank_mask:0xf
	v_mul_f32_e32 v152, v152, v16
	v_mul_f32_e32 v153, v153, v17
	v_add_f32_dpp v164, v164, v164 row_half_mirror row_mask:0xf bank_mask:0xf
	v_mul_f32_e32 v154, v154, v18
	v_mul_f32_e32 v155, v155, v19
	v_add_f32_dpp v164, v164, v164 row_mirror row_mask:0xf bank_mask:0xf
	v_add_f32_e32 v164, 0x390637bd, v164
	v_rsq_f32_e32 v165, v164
	s_nop 0
	v_mul_f32_e32 v148, v148, v165
	v_mul_f32_e32 v149, v149, v165
	v_mul_f32_e32 v150, v150, v165
	v_mul_f32_e32 v151, v151, v165
	v_mul_f32_e32 v152, v152, v165
	v_mul_f32_e32 v153, v153, v165
	v_mul_f32_e32 v154, v154, v165
	v_mul_f32_e32 v155, v155, v165
	s_cbranch_scc0 .Lpp_norope_q0_3
	v_mul_f32_dpp v156, v148, v168 row_ror:8 row_mask:0xf bank_mask:0xf
	v_mul_f32_dpp v157, v149, v169 row_ror:8 row_mask:0xf bank_mask:0xf
	v_mul_f32_dpp v158, v150, v170 row_ror:8 row_mask:0xf bank_mask:0xf
	v_mul_f32_dpp v159, v151, v171 row_ror:8 row_mask:0xf bank_mask:0xf
	v_mul_f32_dpp v160, v152, v172 row_ror:8 row_mask:0xf bank_mask:0xf
	v_mul_f32_dpp v161, v153, v173 row_ror:8 row_mask:0xf bank_mask:0xf
	v_mul_f32_dpp v162, v154, v174 row_ror:8 row_mask:0xf bank_mask:0xf
	v_mul_f32_dpp v163, v155, v175 row_ror:8 row_mask:0xf bank_mask:0xf
	v_fmac_f32_e32 v156, v148, v52
	v_fmac_f32_e32 v157, v149, v53
	v_fmac_f32_e32 v158, v150, v54
	v_fmac_f32_e32 v159, v151, v55
	v_fmac_f32_e32 v160, v152, v56
	v_fmac_f32_e32 v161, v153, v57
	v_fmac_f32_e32 v162, v154, v58
	v_fmac_f32_e32 v163, v155, v59
	s_branch .Lpp_ropedone_q0_3

.Lpp_ropedone_kk_3:
	v_cvt_pk_bf16_f32 v156, v156, v157
	v_cvt_pk_bf16_f32 v157, v158, v159
	v_cvt_pk_bf16_f32 v158, v160, v161
	v_cvt_pk_bf16_f32 v159, v162, v163
	s_mov_b64 exec, 0xffffffff
	global_store_dwordx4 v4, v[156:159], s[28:29]
	s_mov_b64 exec, s[66:67]
	global_store_dwordx4 v4, v[156:159], s[30:31]
	s_mov_b64 exec, -1
	v_lshlrev_b32_e32 v148, 16, v48
	v_and_b32_e32 v149, 0xffff0000, v48
	v_lshlrev_b32_e32 v150, 16, v49
	v_and_b32_e32 v151, 0xffff0000, v49
	v_lshlrev_b32_e32 v152, 16, v50
	v_and_b32_e32 v153, 0xffff0000, v50
	v_lshlrev_b32_e32 v154, 16, v51
	v_and_b32_e32 v155, 0xffff0000, v51
	v_mul_f32_e32 v164, v148, v148
	v_fmac_f32_e32 v164, v149, v149
	v_fmac_f32_e32 v164, v150, v150
	v_fmac_f32_e32 v164, v151, v151
	v_fmac_f32_e32 v164, v152, v152
	v_fmac_f32_e32 v164, v153, v153
	v_fmac_f32_e32 v164, v154, v154
	v_fmac_f32_e32 v164, v155, v155
	v_mul_f32_e32 v148, v148, v28
	v_mul_f32_e32 v149, v149, v29
	v_add_f32_dpp v164, v164, v164 quad_perm:[1,0,3,2] row_mask:0xf bank_mask:0xf
	v_mul_f32_e32 v150, v150, v30
	v_mul_f32_e32 v151, v151, v31
	v_add_f32_dpp v164, v164, v164 quad_perm:[2,3,0,1] row_mask:0xf bank_mask:0xf
	v_mul_f32_e32 v152, v152, v32
	v_mul_f32_e32 v153, v153, v33
	v_add_f32_dpp v164, v164, v164 row_half_mirror row_mask:0xf bank_mask:0xf
	v_mul_f32_e32 v154, v154, v34
	v_mul_f32_e32 v155, v155, v35
	v_add_f32_dpp v164, v164, v164 row_mirror row_mask:0xf bank_mask:0xf
	s_nop 0
	v_readlane_b32 s0, v164, 0
	v_readlane_b32 s1, v164, 16
	v_readlane_b32 s2, v164, 32
	v_readlane_b32 s3, v164, 48
	s_nop 1
	v_mov_b32_e32 v166, s0
	v_add_f32_e32 v166, s1, v166
	v_add_f32_e32 v166, s2, v166
	v_add_f32_e32 v166, s3, v166
	v_add_f32_e32 v166, 0x3a0637bd, v166
	v_rsq_f32_e32 v165, v166
	s_nop 0
	v_mul_f32_e32 v148, v148, v165
	v_mul_f32_e32 v149, v149, v165
	v_mul_f32_e32 v150, v150, v165
	v_mul_f32_e32 v151, v151, v165
	v_mul_f32_e32 v152, v152, v165
	v_mul_f32_e32 v153, v153, v165
	v_mul_f32_e32 v154, v154, v165
	v_mul_f32_e32 v155, v155, v165
	v_cvt_pk_bf16_f32 v156, v148, v149
	v_cvt_pk_bf16_f32 v157, v150, v151
	v_cvt_pk_bf16_f32 v158, v152, v153
	v_cvt_pk_bf16_f32 v159, v154, v155
	global_store_dwordx4 v4, v[156:159], s[34:35]
	v_add_f32_e32 v176, v68, v11
	v_mul_f32_e64 v177, |v176|, s47
	v_exp_f32_e32 v177, v177
	s_nop 0
	v_add_f32_e32 v178, 1.0, v177
	v_add_f32_e32 v179, -1.0, v178
	v_log_f32_e32 v180, v178
	v_rcp_f32_e32 v181, v179
	v_cmp_eq_f32_e32 vcc, 0, v179
	s_nop 0
	v_mul_f32_e32 v181, v177, v181
	s_nop 0
	v_cndmask_b32_e64 v181, v181, 1.0, vcc
	v_mul_f32_e32 v180, 0x3f317218, v180
	v_mul_f32_e32 v180, v180, v181
	v_min_f32_e32 v177, 0, v176
	v_sub_f32_e32 v177, v177, v180
	v_cndmask_b32_e64 v177, v176, v177, s[68:69]
	s_mov_b64 exec, 0xffff
	global_store_dword v8, v177, s[44:45]
	s_mov_b64 exec, -1
	s_add_i32 s11, s10, 0x3000
	s_lshr_b32 s0, s11, 8
	s_mul_i32 s0, s0, 57
	s_lshr_b32 s0, s0, 9
	s_mul_i32 s1, s0, 0x900
	s_sub_i32 s43, s11, s1
	s_sub_i32 s0, s43, 0x100
	s_max_i32 s0, s0, 0
	s_mul_i32 s1, s11, 0x2400
	s_add_u32 s12, s48, s1
	s_addc_u32 s13, s49, 0
	s_lshl_b32 s1, s11, 9
	s_add_u32 s14, s50, s1
	s_addc_u32 s15, s51, 0
	s_lshl_b32 s1, s0, 8
	s_add_u32 s16, s52, s1
	s_addc_u32 s17, s53, 0
	s_add_u32 s18, s54, s1
	s_addc_u32 s19, s55, 0
	global_load_dwordx4 v[36:39], v4, s[12:13]
	global_load_dwordx4 v[40:43], v4, s[12:13] offset:1024
	global_load_dwordx4 v[44:47], v5, s[12:13]
	global_load_dwordx4 v[48:51], v4, s[12:13] offset:3072
	global_load_dword v68, v6, s[14:15]
	global_load_dwordx4 v[52:55], v7, s[16:17]
	global_load_dwordx4 v[56:59], v7, s[16:17] offset:16
	global_load_dwordx4 v[60:63], v7, s[18:19]
	global_load_dwordx4 v[64:67], v7, s[18:19] offset:16
	s_waitcnt vmcnt(30)
	s_add_i32 s11, s10, 0x2000
	s_lshr_b32 s0, s11, 8
	s_mul_i32 s0, s0, 57
	s_lshr_b32 s0, s0, 9
	s_mul_i32 s1, s0, 0x900
	s_sub_i32 s43, s11, s1
	s_mul_i32 s1, s0, 0x9000
	s_lshl_b32 s2, s43, 2
	s_add_i32 s1, s1, s2
	s_add_u32 s44, s4, s1
	s_addc_u32 s45, s5, 0
	s_lshl_b32 s1, s11, 11
	s_add_u32 s22, s56, s1
	s_addc_u32 s23, s57, 0
	s_lshl_b32 s1, s11, 9
	s_add_u32 s28, s58, s1
	s_addc_u32 s29, s59, 0
	s_add_u32 s30, s62, s1
	s_addc_u32 s31, s63, 0
	s_lshl_b32 s1, s11, 10
	s_add_u32 s34, s64, s1
	s_addc_u32 s35, s65, 0
	v_xor_b32_e32 v168, v9, v94
	v_xor_b32_e32 v169, v9, v95
	v_xor_b32_e32 v170, v9, v96
	v_xor_b32_e32 v171, v9, v97
	v_xor_b32_e32 v172, v9, v98
	v_xor_b32_e32 v173, v9, v99
	v_xor_b32_e32 v174, v9, v100
	v_xor_b32_e32 v175, v9, v101
	s_cmpk_ge_u32 s43, 0x100
	v_lshlrev_b32_e32 v148, 16, v70
	v_and_b32_e32 v149, 0xffff0000, v70
	v_lshlrev_b32_e32 v150, 16, v71
	v_and_b32_e32 v151, 0xffff0000, v71
	v_lshlrev_b32_e32 v152, 16, v72
	v_and_b32_e32 v153, 0xffff0000, v72
	v_lshlrev_b32_e32 v154, 16, v73
	v_and_b32_e32 v155, 0xffff0000, v73
	v_mul_f32_e32 v164, v148, v148
	v_fmac_f32_e32 v164, v149, v149
	v_fmac_f32_e32 v164, v150, v150
	v_fmac_f32_e32 v164, v151, v151
	v_fmac_f32_e32 v164, v152, v152
	v_fmac_f32_e32 v164, v153, v153
	v_fmac_f32_e32 v164, v154, v154
	v_fmac_f32_e32 v164, v155, v155
	v_mul_f32_e32 v148, v148, v12
	v_mul_f32_e32 v149, v149, v13
	v_add_f32_dpp v164, v164, v164 quad_perm:[1,0,3,2] row_mask:0xf bank_mask:0xf
	v_mul_f32_e32 v150, v150, v14
	v_mul_f32_e32 v151, v151, v15
	v_add_f32_dpp v164, v164, v164 quad_perm:[2,3,0,1] row_mask:0xf bank_mask:0xf
	v_mul_f32_e32 v152, v152, v16
	v_mul_f32_e32 v153, v153, v17
	v_add_f32_dpp v164, v164, v164 row_half_mirror row_mask:0xf bank_mask:0xf
	v_mul_f32_e32 v154, v154, v18
	v_mul_f32_e32 v155, v155, v19
	v_add_f32_dpp v164, v164, v164 row_mirror row_mask:0xf bank_mask:0xf
	v_add_f32_e32 v164, 0x390637bd, v164
	v_rsq_f32_e32 v165, v164
	s_nop 0
	v_mul_f32_e32 v148, v148, v165
	v_mul_f32_e32 v149, v149, v165
	v_mul_f32_e32 v150, v150, v165
	v_mul_f32_e32 v151, v151, v165
	v_mul_f32_e32 v152, v152, v165
	v_mul_f32_e32 v153, v153, v165
	v_mul_f32_e32 v154, v154, v165
	v_mul_f32_e32 v155, v155, v165
	s_cbranch_scc0 .Lpp_norope_q0_4
	v_mul_f32_dpp v156, v148, v168 row_ror:8 row_mask:0xf bank_mask:0xf
	v_mul_f32_dpp v157, v149, v169 row_ror:8 row_mask:0xf bank_mask:0xf
	v_mul_f32_dpp v158, v150, v170 row_ror:8 row_mask:0xf bank_mask:0xf
	v_mul_f32_dpp v159, v151, v171 row_ror:8 row_mask:0xf bank_mask:0xf
	v_mul_f32_dpp v160, v152, v172 row_ror:8 row_mask:0xf bank_mask:0xf
	v_mul_f32_dpp v161, v153, v173 row_ror:8 row_mask:0xf bank_mask:0xf
	v_mul_f32_dpp v162, v154, v174 row_ror:8 row_mask:0xf bank_mask:0xf
	v_mul_f32_dpp v163, v155, v175 row_ror:8 row_mask:0xf bank_mask:0xf
	v_fmac_f32_e32 v156, v148, v86
	v_fmac_f32_e32 v157, v149, v87
	v_fmac_f32_e32 v158, v150, v88
	v_fmac_f32_e32 v159, v151, v89
	v_fmac_f32_e32 v160, v152, v90
	v_fmac_f32_e32 v161, v153, v91
	v_fmac_f32_e32 v162, v154, v92
	v_fmac_f32_e32 v163, v155, v93
	s_branch .Lpp_ropedone_q0_4

.Lpp_ropedone_kk_4:
	v_cvt_pk_bf16_f32 v156, v156, v157
	v_cvt_pk_bf16_f32 v157, v158, v159
	v_cvt_pk_bf16_f32 v158, v160, v161
	v_cvt_pk_bf16_f32 v159, v162, v163
	s_mov_b64 exec, 0xffffffff
	global_store_dwordx4 v4, v[156:159], s[28:29]
	s_mov_b64 exec, s[66:67]
	global_store_dwordx4 v4, v[156:159], s[30:31]
	s_mov_b64 exec, -1
	v_lshlrev_b32_e32 v148, 16, v82
	v_and_b32_e32 v149, 0xffff0000, v82
	v_lshlrev_b32_e32 v150, 16, v83
	v_and_b32_e32 v151, 0xffff0000, v83
	v_lshlrev_b32_e32 v152, 16, v84
	v_and_b32_e32 v153, 0xffff0000, v84
	v_lshlrev_b32_e32 v154, 16, v85
	v_and_b32_e32 v155, 0xffff0000, v85
	v_mul_f32_e32 v164, v148, v148
	v_fmac_f32_e32 v164, v149, v149
	v_fmac_f32_e32 v164, v150, v150
	v_fmac_f32_e32 v164, v151, v151
	v_fmac_f32_e32 v164, v152, v152
	v_fmac_f32_e32 v164, v153, v153
	v_fmac_f32_e32 v164, v154, v154
	v_fmac_f32_e32 v164, v155, v155
	v_mul_f32_e32 v148, v148, v28
	v_mul_f32_e32 v149, v149, v29
	v_add_f32_dpp v164, v164, v164 quad_perm:[1,0,3,2] row_mask:0xf bank_mask:0xf
	v_mul_f32_e32 v150, v150, v30
	v_mul_f32_e32 v151, v151, v31
	v_add_f32_dpp v164, v164, v164 quad_perm:[2,3,0,1] row_mask:0xf bank_mask:0xf
	v_mul_f32_e32 v152, v152, v32
	v_mul_f32_e32 v153, v153, v33
	v_add_f32_dpp v164, v164, v164 row_half_mirror row_mask:0xf bank_mask:0xf
	v_mul_f32_e32 v154, v154, v34
	v_mul_f32_e32 v155, v155, v35
	v_add_f32_dpp v164, v164, v164 row_mirror row_mask:0xf bank_mask:0xf
	s_nop 0
	v_readlane_b32 s0, v164, 0
	v_readlane_b32 s1, v164, 16
	v_readlane_b32 s2, v164, 32
	v_readlane_b32 s3, v164, 48
	s_nop 1
	v_mov_b32_e32 v166, s0
	v_add_f32_e32 v166, s1, v166
	v_add_f32_e32 v166, s2, v166
	v_add_f32_e32 v166, s3, v166
	v_add_f32_e32 v166, 0x3a0637bd, v166
	v_rsq_f32_e32 v165, v166
	s_nop 0
	v_mul_f32_e32 v148, v148, v165
	v_mul_f32_e32 v149, v149, v165
	v_mul_f32_e32 v150, v150, v165
	v_mul_f32_e32 v151, v151, v165
	v_mul_f32_e32 v152, v152, v165
	v_mul_f32_e32 v153, v153, v165
	v_mul_f32_e32 v154, v154, v165
	v_mul_f32_e32 v155, v155, v165
	v_cvt_pk_bf16_f32 v156, v148, v149
	v_cvt_pk_bf16_f32 v157, v150, v151
	v_cvt_pk_bf16_f32 v158, v152, v153
	v_cvt_pk_bf16_f32 v159, v154, v155
	global_store_dwordx4 v4, v[156:159], s[34:35]
	v_add_f32_e32 v176, v102, v11
	v_mul_f32_e64 v177, |v176|, s47
	v_exp_f32_e32 v177, v177
	s_nop 0
	v_add_f32_e32 v178, 1.0, v177
	v_add_f32_e32 v179, -1.0, v178
	v_log_f32_e32 v180, v178
	v_rcp_f32_e32 v181, v179
	v_cmp_eq_f32_e32 vcc, 0, v179
	s_nop 0
	v_mul_f32_e32 v181, v177, v181
	s_nop 0
	v_cndmask_b32_e64 v181, v181, 1.0, vcc
	v_mul_f32_e32 v180, 0x3f317218, v180
	v_mul_f32_e32 v180, v180, v181
	v_min_f32_e32 v177, 0, v176
	v_sub_f32_e32 v177, v177, v180
	v_cndmask_b32_e64 v177, v176, v177, s[68:69]
	s_mov_b64 exec, 0xffff
	global_store_dword v8, v177, s[44:45]
	s_mov_b64 exec, -1
	s_add_i32 s11, s10, 0x3800
	s_lshr_b32 s0, s11, 8
	s_mul_i32 s0, s0, 57
	s_lshr_b32 s0, s0, 9
	s_mul_i32 s1, s0, 0x900
	s_sub_i32 s43, s11, s1
	s_sub_i32 s0, s43, 0x100
	s_max_i32 s0, s0, 0
	s_mul_i32 s1, s11, 0x2400
	s_add_u32 s12, s48, s1
	s_addc_u32 s13, s49, 0
	s_lshl_b32 s1, s11, 9
	s_add_u32 s14, s50, s1
	s_addc_u32 s15, s51, 0
	s_lshl_b32 s1, s0, 8
	s_add_u32 s16, s52, s1
	s_addc_u32 s17, s53, 0
	s_add_u32 s18, s54, s1
	s_addc_u32 s19, s55, 0
	global_load_dwordx4 v[70:73], v4, s[12:13]
	global_load_dwordx4 v[74:77], v4, s[12:13] offset:1024
	global_load_dwordx4 v[78:81], v5, s[12:13]
	global_load_dwordx4 v[82:85], v4, s[12:13] offset:3072
	global_load_dword v102, v6, s[14:15]
	global_load_dwordx4 v[86:89], v7, s[16:17]
	global_load_dwordx4 v[90:93], v7, s[16:17] offset:16
	global_load_dwordx4 v[94:97], v7, s[18:19]
	global_load_dwordx4 v[98:101], v7, s[18:19] offset:16
	s_waitcnt vmcnt(30)
	s_add_i32 s11, s10, 0x2800
	s_lshr_b32 s0, s11, 8
	s_mul_i32 s0, s0, 57
	s_lshr_b32 s0, s0, 9
	s_mul_i32 s1, s0, 0x900
	s_sub_i32 s43, s11, s1
	s_mul_i32 s1, s0, 0x9000
	s_lshl_b32 s2, s43, 2
	s_add_i32 s1, s1, s2
	s_add_u32 s44, s4, s1
	s_addc_u32 s45, s5, 0
	s_lshl_b32 s1, s11, 11
	s_add_u32 s22, s56, s1
	s_addc_u32 s23, s57, 0
	s_lshl_b32 s1, s11, 9
	s_add_u32 s28, s58, s1
	s_addc_u32 s29, s59, 0
	s_add_u32 s30, s62, s1
	s_addc_u32 s31, s63, 0
	s_lshl_b32 s1, s11, 10
	s_add_u32 s34, s64, s1
	s_addc_u32 s35, s65, 0
	v_xor_b32_e32 v168, v9, v128
	v_xor_b32_e32 v169, v9, v129
	v_xor_b32_e32 v170, v9, v130
	v_xor_b32_e32 v171, v9, v131
	v_xor_b32_e32 v172, v9, v132
	v_xor_b32_e32 v173, v9, v133
	v_xor_b32_e32 v174, v9, v134
	v_xor_b32_e32 v175, v9, v135
	s_cmpk_ge_u32 s43, 0x100
	v_lshlrev_b32_e32 v148, 16, v104
	v_and_b32_e32 v149, 0xffff0000, v104
	v_lshlrev_b32_e32 v150, 16, v105
	v_and_b32_e32 v151, 0xffff0000, v105
	v_lshlrev_b32_e32 v152, 16, v106
	v_and_b32_e32 v153, 0xffff0000, v106
	v_lshlrev_b32_e32 v154, 16, v107
	v_and_b32_e32 v155, 0xffff0000, v107
	v_mul_f32_e32 v164, v148, v148
	v_fmac_f32_e32 v164, v149, v149
	v_fmac_f32_e32 v164, v150, v150
	v_fmac_f32_e32 v164, v151, v151
	v_fmac_f32_e32 v164, v152, v152
	v_fmac_f32_e32 v164, v153, v153
	v_fmac_f32_e32 v164, v154, v154
	v_fmac_f32_e32 v164, v155, v155
	v_mul_f32_e32 v148, v148, v12
	v_mul_f32_e32 v149, v149, v13
	v_add_f32_dpp v164, v164, v164 quad_perm:[1,0,3,2] row_mask:0xf bank_mask:0xf
	v_mul_f32_e32 v150, v150, v14
	v_mul_f32_e32 v151, v151, v15
	v_add_f32_dpp v164, v164, v164 quad_perm:[2,3,0,1] row_mask:0xf bank_mask:0xf
	v_mul_f32_e32 v152, v152, v16
	v_mul_f32_e32 v153, v153, v17
	v_add_f32_dpp v164, v164, v164 row_half_mirror row_mask:0xf bank_mask:0xf
	v_mul_f32_e32 v154, v154, v18
	v_mul_f32_e32 v155, v155, v19
	v_add_f32_dpp v164, v164, v164 row_mirror row_mask:0xf bank_mask:0xf
	v_add_f32_e32 v164, 0x390637bd, v164
	v_rsq_f32_e32 v165, v164
	s_nop 0
	v_mul_f32_e32 v148, v148, v165
	v_mul_f32_e32 v149, v149, v165
	v_mul_f32_e32 v150, v150, v165
	v_mul_f32_e32 v151, v151, v165
	v_mul_f32_e32 v152, v152, v165
	v_mul_f32_e32 v153, v153, v165
	v_mul_f32_e32 v154, v154, v165
	v_mul_f32_e32 v155, v155, v165
	s_cbranch_scc0 .Lpp_norope_q0_5
	v_mul_f32_dpp v156, v148, v168 row_ror:8 row_mask:0xf bank_mask:0xf
	v_mul_f32_dpp v157, v149, v169 row_ror:8 row_mask:0xf bank_mask:0xf
	v_mul_f32_dpp v158, v150, v170 row_ror:8 row_mask:0xf bank_mask:0xf
	v_mul_f32_dpp v159, v151, v171 row_ror:8 row_mask:0xf bank_mask:0xf
	v_mul_f32_dpp v160, v152, v172 row_ror:8 row_mask:0xf bank_mask:0xf
	v_mul_f32_dpp v161, v153, v173 row_ror:8 row_mask:0xf bank_mask:0xf
	v_mul_f32_dpp v162, v154, v174 row_ror:8 row_mask:0xf bank_mask:0xf
	v_mul_f32_dpp v163, v155, v175 row_ror:8 row_mask:0xf bank_mask:0xf
	v_fmac_f32_e32 v156, v148, v120
	v_fmac_f32_e32 v157, v149, v121
	v_fmac_f32_e32 v158, v150, v122
	v_fmac_f32_e32 v159, v151, v123
	v_fmac_f32_e32 v160, v152, v124
	v_fmac_f32_e32 v161, v153, v125
	v_fmac_f32_e32 v162, v154, v126
	v_fmac_f32_e32 v163, v155, v127
	s_branch .Lpp_ropedone_q0_5

.Lpp_ropedone_kk_5:
	v_cvt_pk_bf16_f32 v156, v156, v157
	v_cvt_pk_bf16_f32 v157, v158, v159
	v_cvt_pk_bf16_f32 v158, v160, v161
	v_cvt_pk_bf16_f32 v159, v162, v163
	s_mov_b64 exec, 0xffffffff
	global_store_dwordx4 v4, v[156:159], s[28:29]
	s_mov_b64 exec, s[66:67]
	global_store_dwordx4 v4, v[156:159], s[30:31]
	s_mov_b64 exec, -1
	v_lshlrev_b32_e32 v148, 16, v116
	v_and_b32_e32 v149, 0xffff0000, v116
	v_lshlrev_b32_e32 v150, 16, v117
	v_and_b32_e32 v151, 0xffff0000, v117
	v_lshlrev_b32_e32 v152, 16, v118
	v_and_b32_e32 v153, 0xffff0000, v118
	v_lshlrev_b32_e32 v154, 16, v119
	v_and_b32_e32 v155, 0xffff0000, v119
	v_mul_f32_e32 v164, v148, v148
	v_fmac_f32_e32 v164, v149, v149
	v_fmac_f32_e32 v164, v150, v150
	v_fmac_f32_e32 v164, v151, v151
	v_fmac_f32_e32 v164, v152, v152
	v_fmac_f32_e32 v164, v153, v153
	v_fmac_f32_e32 v164, v154, v154
	v_fmac_f32_e32 v164, v155, v155
	v_mul_f32_e32 v148, v148, v28
	v_mul_f32_e32 v149, v149, v29
	v_add_f32_dpp v164, v164, v164 quad_perm:[1,0,3,2] row_mask:0xf bank_mask:0xf
	v_mul_f32_e32 v150, v150, v30
	v_mul_f32_e32 v151, v151, v31
	v_add_f32_dpp v164, v164, v164 quad_perm:[2,3,0,1] row_mask:0xf bank_mask:0xf
	v_mul_f32_e32 v152, v152, v32
	v_mul_f32_e32 v153, v153, v33
	v_add_f32_dpp v164, v164, v164 row_half_mirror row_mask:0xf bank_mask:0xf
	v_mul_f32_e32 v154, v154, v34
	v_mul_f32_e32 v155, v155, v35
	v_add_f32_dpp v164, v164, v164 row_mirror row_mask:0xf bank_mask:0xf
	s_nop 0
	v_readlane_b32 s0, v164, 0
	v_readlane_b32 s1, v164, 16
	v_readlane_b32 s2, v164, 32
	v_readlane_b32 s3, v164, 48
	s_nop 1
	v_mov_b32_e32 v166, s0
	v_add_f32_e32 v166, s1, v166
	v_add_f32_e32 v166, s2, v166
	v_add_f32_e32 v166, s3, v166
	v_add_f32_e32 v166, 0x3a0637bd, v166
	v_rsq_f32_e32 v165, v166
	s_nop 0
	v_mul_f32_e32 v148, v148, v165
	v_mul_f32_e32 v149, v149, v165
	v_mul_f32_e32 v150, v150, v165
	v_mul_f32_e32 v151, v151, v165
	v_mul_f32_e32 v152, v152, v165
	v_mul_f32_e32 v153, v153, v165
	v_mul_f32_e32 v154, v154, v165
	v_mul_f32_e32 v155, v155, v165
	v_cvt_pk_bf16_f32 v156, v148, v149
	v_cvt_pk_bf16_f32 v157, v150, v151
	v_cvt_pk_bf16_f32 v158, v152, v153
	v_cvt_pk_bf16_f32 v159, v154, v155
	global_store_dwordx4 v4, v[156:159], s[34:35]
	v_add_f32_e32 v176, v136, v11
	v_mul_f32_e64 v177, |v176|, s47
	v_exp_f32_e32 v177, v177
	s_nop 0
	v_add_f32_e32 v178, 1.0, v177
	v_add_f32_e32 v179, -1.0, v178
	v_log_f32_e32 v180, v178
	v_rcp_f32_e32 v181, v179
	v_cmp_eq_f32_e32 vcc, 0, v179
	s_nop 0
	v_mul_f32_e32 v181, v177, v181
	s_nop 0
	v_cndmask_b32_e64 v181, v181, 1.0, vcc
	v_mul_f32_e32 v180, 0x3f317218, v180
	v_mul_f32_e32 v180, v180, v181
	v_min_f32_e32 v177, 0, v176
	v_sub_f32_e32 v177, v177, v180
	v_cndmask_b32_e64 v177, v176, v177, s[68:69]
	s_mov_b64 exec, 0xffff
	global_store_dword v8, v177, s[44:45]
	s_mov_b64 exec, -1
	s_add_i32 s11, s10, 0x4000
	s_lshr_b32 s0, s11, 8
	s_mul_i32 s0, s0, 57
	s_lshr_b32 s0, s0, 9
	s_mul_i32 s1, s0, 0x900
	s_sub_i32 s43, s11, s1
	s_sub_i32 s0, s43, 0x100
	s_max_i32 s0, s0, 0
	s_mul_i32 s1, s11, 0x2400
	s_add_u32 s12, s48, s1
	s_addc_u32 s13, s49, 0
	s_lshl_b32 s1, s11, 9
	s_add_u32 s14, s50, s1
	s_addc_u32 s15, s51, 0
	s_lshl_b32 s1, s0, 8
	s_add_u32 s16, s52, s1
	s_addc_u32 s17, s53, 0
	s_add_u32 s18, s54, s1
	s_addc_u32 s19, s55, 0
	global_load_dwordx4 v[104:107], v4, s[12:13]
	global_load_dwordx4 v[108:111], v4, s[12:13] offset:1024
	global_load_dwordx4 v[112:115], v5, s[12:13]
	global_load_dwordx4 v[116:119], v4, s[12:13] offset:3072
	global_load_dword v136, v6, s[14:15]
	global_load_dwordx4 v[120:123], v7, s[16:17]
	global_load_dwordx4 v[124:127], v7, s[16:17] offset:16
	global_load_dwordx4 v[128:131], v7, s[18:19]
	global_load_dwordx4 v[132:135], v7, s[18:19] offset:16
	s_waitcnt vmcnt(30)
	s_add_i32 s11, s10, 0x3000
	s_lshr_b32 s0, s11, 8
	s_mul_i32 s0, s0, 57
	s_lshr_b32 s0, s0, 9
	s_mul_i32 s1, s0, 0x900
	s_sub_i32 s43, s11, s1
	s_mul_i32 s1, s0, 0x9000
	s_lshl_b32 s2, s43, 2
	s_add_i32 s1, s1, s2
	s_add_u32 s44, s4, s1
	s_addc_u32 s45, s5, 0
	s_lshl_b32 s1, s11, 11
	s_add_u32 s22, s56, s1
	s_addc_u32 s23, s57, 0
	s_lshl_b32 s1, s11, 9
	s_add_u32 s28, s58, s1
	s_addc_u32 s29, s59, 0
	s_add_u32 s30, s62, s1
	s_addc_u32 s31, s63, 0
	s_lshl_b32 s1, s11, 10
	s_add_u32 s34, s64, s1
	s_addc_u32 s35, s65, 0
	v_xor_b32_e32 v168, v9, v60
	v_xor_b32_e32 v169, v9, v61
	v_xor_b32_e32 v170, v9, v62
	v_xor_b32_e32 v171, v9, v63
	v_xor_b32_e32 v172, v9, v64
	v_xor_b32_e32 v173, v9, v65
	v_xor_b32_e32 v174, v9, v66
	v_xor_b32_e32 v175, v9, v67
	s_cmpk_ge_u32 s43, 0x100
	v_lshlrev_b32_e32 v148, 16, v36
	v_and_b32_e32 v149, 0xffff0000, v36
	v_lshlrev_b32_e32 v150, 16, v37
	v_and_b32_e32 v151, 0xffff0000, v37
	v_lshlrev_b32_e32 v152, 16, v38
	v_and_b32_e32 v153, 0xffff0000, v38
	v_lshlrev_b32_e32 v154, 16, v39
	v_and_b32_e32 v155, 0xffff0000, v39
	v_mul_f32_e32 v164, v148, v148
	v_fmac_f32_e32 v164, v149, v149
	v_fmac_f32_e32 v164, v150, v150
	v_fmac_f32_e32 v164, v151, v151
	v_fmac_f32_e32 v164, v152, v152
	v_fmac_f32_e32 v164, v153, v153
	v_fmac_f32_e32 v164, v154, v154
	v_fmac_f32_e32 v164, v155, v155
	v_mul_f32_e32 v148, v148, v12
	v_mul_f32_e32 v149, v149, v13
	v_add_f32_dpp v164, v164, v164 quad_perm:[1,0,3,2] row_mask:0xf bank_mask:0xf
	v_mul_f32_e32 v150, v150, v14
	v_mul_f32_e32 v151, v151, v15
	v_add_f32_dpp v164, v164, v164 quad_perm:[2,3,0,1] row_mask:0xf bank_mask:0xf
	v_mul_f32_e32 v152, v152, v16
	v_mul_f32_e32 v153, v153, v17
	v_add_f32_dpp v164, v164, v164 row_half_mirror row_mask:0xf bank_mask:0xf
	v_mul_f32_e32 v154, v154, v18
	v_mul_f32_e32 v155, v155, v19
	v_add_f32_dpp v164, v164, v164 row_mirror row_mask:0xf bank_mask:0xf
	v_add_f32_e32 v164, 0x390637bd, v164
	v_rsq_f32_e32 v165, v164
	s_nop 0
	v_mul_f32_e32 v148, v148, v165
	v_mul_f32_e32 v149, v149, v165
	v_mul_f32_e32 v150, v150, v165
	v_mul_f32_e32 v151, v151, v165
	v_mul_f32_e32 v152, v152, v165
	v_mul_f32_e32 v153, v153, v165
	v_mul_f32_e32 v154, v154, v165
	v_mul_f32_e32 v155, v155, v165
	s_cbranch_scc0 .Lpp_norope_q0_6
	v_mul_f32_dpp v156, v148, v168 row_ror:8 row_mask:0xf bank_mask:0xf
	v_mul_f32_dpp v157, v149, v169 row_ror:8 row_mask:0xf bank_mask:0xf
	v_mul_f32_dpp v158, v150, v170 row_ror:8 row_mask:0xf bank_mask:0xf
	v_mul_f32_dpp v159, v151, v171 row_ror:8 row_mask:0xf bank_mask:0xf
	v_mul_f32_dpp v160, v152, v172 row_ror:8 row_mask:0xf bank_mask:0xf
	v_mul_f32_dpp v161, v153, v173 row_ror:8 row_mask:0xf bank_mask:0xf
	v_mul_f32_dpp v162, v154, v174 row_ror:8 row_mask:0xf bank_mask:0xf
	v_mul_f32_dpp v163, v155, v175 row_ror:8 row_mask:0xf bank_mask:0xf
	v_fmac_f32_e32 v156, v148, v52
	v_fmac_f32_e32 v157, v149, v53
	v_fmac_f32_e32 v158, v150, v54
	v_fmac_f32_e32 v159, v151, v55
	v_fmac_f32_e32 v160, v152, v56
	v_fmac_f32_e32 v161, v153, v57
	v_fmac_f32_e32 v162, v154, v58
	v_fmac_f32_e32 v163, v155, v59
	s_branch .Lpp_ropedone_q0_6

.Lpp_ropedone_kk_6:
	v_cvt_pk_bf16_f32 v156, v156, v157
	v_cvt_pk_bf16_f32 v157, v158, v159
	v_cvt_pk_bf16_f32 v158, v160, v161
	v_cvt_pk_bf16_f32 v159, v162, v163
	s_mov_b64 exec, 0xffffffff
	global_store_dwordx4 v4, v[156:159], s[28:29]
	s_mov_b64 exec, s[66:67]
	global_store_dwordx4 v4, v[156:159], s[30:31]
	s_mov_b64 exec, -1
	v_lshlrev_b32_e32 v148, 16, v48
	v_and_b32_e32 v149, 0xffff0000, v48
	v_lshlrev_b32_e32 v150, 16, v49
	v_and_b32_e32 v151, 0xffff0000, v49
	v_lshlrev_b32_e32 v152, 16, v50
	v_and_b32_e32 v153, 0xffff0000, v50
	v_lshlrev_b32_e32 v154, 16, v51
	v_and_b32_e32 v155, 0xffff0000, v51
	v_mul_f32_e32 v164, v148, v148
	v_fmac_f32_e32 v164, v149, v149
	v_fmac_f32_e32 v164, v150, v150
	v_fmac_f32_e32 v164, v151, v151
	v_fmac_f32_e32 v164, v152, v152
	v_fmac_f32_e32 v164, v153, v153
	v_fmac_f32_e32 v164, v154, v154
	v_fmac_f32_e32 v164, v155, v155
	v_mul_f32_e32 v148, v148, v28
	v_mul_f32_e32 v149, v149, v29
	v_add_f32_dpp v164, v164, v164 quad_perm:[1,0,3,2] row_mask:0xf bank_mask:0xf
	v_mul_f32_e32 v150, v150, v30
	v_mul_f32_e32 v151, v151, v31
	v_add_f32_dpp v164, v164, v164 quad_perm:[2,3,0,1] row_mask:0xf bank_mask:0xf
	v_mul_f32_e32 v152, v152, v32
	v_mul_f32_e32 v153, v153, v33
	v_add_f32_dpp v164, v164, v164 row_half_mirror row_mask:0xf bank_mask:0xf
	v_mul_f32_e32 v154, v154, v34
	v_mul_f32_e32 v155, v155, v35
	v_add_f32_dpp v164, v164, v164 row_mirror row_mask:0xf bank_mask:0xf
	s_nop 0
	v_readlane_b32 s0, v164, 0
	v_readlane_b32 s1, v164, 16
	v_readlane_b32 s2, v164, 32
	v_readlane_b32 s3, v164, 48
	s_nop 1
	v_mov_b32_e32 v166, s0
	v_add_f32_e32 v166, s1, v166
	v_add_f32_e32 v166, s2, v166
	v_add_f32_e32 v166, s3, v166
	v_add_f32_e32 v166, 0x3a0637bd, v166
	v_rsq_f32_e32 v165, v166
	s_nop 0
	v_mul_f32_e32 v148, v148, v165
	v_mul_f32_e32 v149, v149, v165
	v_mul_f32_e32 v150, v150, v165
	v_mul_f32_e32 v151, v151, v165
	v_mul_f32_e32 v152, v152, v165
	v_mul_f32_e32 v153, v153, v165
	v_mul_f32_e32 v154, v154, v165
	v_mul_f32_e32 v155, v155, v165
	v_cvt_pk_bf16_f32 v156, v148, v149
	v_cvt_pk_bf16_f32 v157, v150, v151
	v_cvt_pk_bf16_f32 v158, v152, v153
	v_cvt_pk_bf16_f32 v159, v154, v155
	global_store_dwordx4 v4, v[156:159], s[34:35]
	v_add_f32_e32 v176, v68, v11
	v_mul_f32_e64 v177, |v176|, s47
	v_exp_f32_e32 v177, v177
	s_nop 0
	v_add_f32_e32 v178, 1.0, v177
	v_add_f32_e32 v179, -1.0, v178
	v_log_f32_e32 v180, v178
	v_rcp_f32_e32 v181, v179
	v_cmp_eq_f32_e32 vcc, 0, v179
	s_nop 0
	v_mul_f32_e32 v181, v177, v181
	s_nop 0
	v_cndmask_b32_e64 v181, v181, 1.0, vcc
	v_mul_f32_e32 v180, 0x3f317218, v180
	v_mul_f32_e32 v180, v180, v181
	v_min_f32_e32 v177, 0, v176
	v_sub_f32_e32 v177, v177, v180
	v_cndmask_b32_e64 v177, v176, v177, s[68:69]
	s_mov_b64 exec, 0xffff
	global_store_dword v8, v177, s[44:45]
	s_mov_b64 exec, -1
	s_waitcnt vmcnt(21)
	s_add_i32 s11, s10, 0x3800
	s_lshr_b32 s0, s11, 8
	s_mul_i32 s0, s0, 57
	s_lshr_b32 s0, s0, 9
	s_mul_i32 s1, s0, 0x900
	s_sub_i32 s43, s11, s1
	s_mul_i32 s1, s0, 0x9000
	s_lshl_b32 s2, s43, 2
	s_add_i32 s1, s1, s2
	s_add_u32 s44, s4, s1
	s_addc_u32 s45, s5, 0
	s_lshl_b32 s1, s11, 11
	s_add_u32 s22, s56, s1
	s_addc_u32 s23, s57, 0
	s_lshl_b32 s1, s11, 9
	s_add_u32 s28, s58, s1
	s_addc_u32 s29, s59, 0
	s_add_u32 s30, s62, s1
	s_addc_u32 s31, s63, 0
	s_lshl_b32 s1, s11, 10
	s_add_u32 s34, s64, s1
	s_addc_u32 s35, s65, 0
	v_xor_b32_e32 v168, v9, v94
	v_xor_b32_e32 v169, v9, v95
	v_xor_b32_e32 v170, v9, v96
	v_xor_b32_e32 v171, v9, v97
	v_xor_b32_e32 v172, v9, v98
	v_xor_b32_e32 v173, v9, v99
	v_xor_b32_e32 v174, v9, v100
	v_xor_b32_e32 v175, v9, v101
	s_cmpk_ge_u32 s43, 0x100
	v_lshlrev_b32_e32 v148, 16, v70
	v_and_b32_e32 v149, 0xffff0000, v70
	v_lshlrev_b32_e32 v150, 16, v71
	v_and_b32_e32 v151, 0xffff0000, v71
	v_lshlrev_b32_e32 v152, 16, v72
	v_and_b32_e32 v153, 0xffff0000, v72
	v_lshlrev_b32_e32 v154, 16, v73
	v_and_b32_e32 v155, 0xffff0000, v73
	v_mul_f32_e32 v164, v148, v148
	v_fmac_f32_e32 v164, v149, v149
	v_fmac_f32_e32 v164, v150, v150
	v_fmac_f32_e32 v164, v151, v151
	v_fmac_f32_e32 v164, v152, v152
	v_fmac_f32_e32 v164, v153, v153
	v_fmac_f32_e32 v164, v154, v154
	v_fmac_f32_e32 v164, v155, v155
	v_mul_f32_e32 v148, v148, v12
	v_mul_f32_e32 v149, v149, v13
	v_add_f32_dpp v164, v164, v164 quad_perm:[1,0,3,2] row_mask:0xf bank_mask:0xf
	v_mul_f32_e32 v150, v150, v14
	v_mul_f32_e32 v151, v151, v15
	v_add_f32_dpp v164, v164, v164 quad_perm:[2,3,0,1] row_mask:0xf bank_mask:0xf
	v_mul_f32_e32 v152, v152, v16
	v_mul_f32_e32 v153, v153, v17
	v_add_f32_dpp v164, v164, v164 row_half_mirror row_mask:0xf bank_mask:0xf
	v_mul_f32_e32 v154, v154, v18
	v_mul_f32_e32 v155, v155, v19
	v_add_f32_dpp v164, v164, v164 row_mirror row_mask:0xf bank_mask:0xf
	v_add_f32_e32 v164, 0x390637bd, v164
	v_rsq_f32_e32 v165, v164
	s_nop 0
	v_mul_f32_e32 v148, v148, v165
	v_mul_f32_e32 v149, v149, v165
	v_mul_f32_e32 v150, v150, v165
	v_mul_f32_e32 v151, v151, v165
	v_mul_f32_e32 v152, v152, v165
	v_mul_f32_e32 v153, v153, v165
	v_mul_f32_e32 v154, v154, v165
	v_mul_f32_e32 v155, v155, v165
	s_cbranch_scc0 .Lpp_norope_q0_7
	v_mul_f32_dpp v156, v148, v168 row_ror:8 row_mask:0xf bank_mask:0xf
	v_mul_f32_dpp v157, v149, v169 row_ror:8 row_mask:0xf bank_mask:0xf
	v_mul_f32_dpp v158, v150, v170 row_ror:8 row_mask:0xf bank_mask:0xf
	v_mul_f32_dpp v159, v151, v171 row_ror:8 row_mask:0xf bank_mask:0xf
	v_mul_f32_dpp v160, v152, v172 row_ror:8 row_mask:0xf bank_mask:0xf
	v_mul_f32_dpp v161, v153, v173 row_ror:8 row_mask:0xf bank_mask:0xf
	v_mul_f32_dpp v162, v154, v174 row_ror:8 row_mask:0xf bank_mask:0xf
	v_mul_f32_dpp v163, v155, v175 row_ror:8 row_mask:0xf bank_mask:0xf
	v_fmac_f32_e32 v156, v148, v86
	v_fmac_f32_e32 v157, v149, v87
	v_fmac_f32_e32 v158, v150, v88
	v_fmac_f32_e32 v159, v151, v89
	v_fmac_f32_e32 v160, v152, v90
	v_fmac_f32_e32 v161, v153, v91
	v_fmac_f32_e32 v162, v154, v92
	v_fmac_f32_e32 v163, v155, v93
	s_branch .Lpp_ropedone_q0_7

.Lpp_ropedone_kk_7:
	v_cvt_pk_bf16_f32 v156, v156, v157
	v_cvt_pk_bf16_f32 v157, v158, v159
	v_cvt_pk_bf16_f32 v158, v160, v161
	v_cvt_pk_bf16_f32 v159, v162, v163
	s_mov_b64 exec, 0xffffffff
	global_store_dwordx4 v4, v[156:159], s[28:29]
	s_mov_b64 exec, s[66:67]
	global_store_dwordx4 v4, v[156:159], s[30:31]
	s_mov_b64 exec, -1
	v_lshlrev_b32_e32 v148, 16, v82
	v_and_b32_e32 v149, 0xffff0000, v82
	v_lshlrev_b32_e32 v150, 16, v83
	v_and_b32_e32 v151, 0xffff0000, v83
	v_lshlrev_b32_e32 v152, 16, v84
	v_and_b32_e32 v153, 0xffff0000, v84
	v_lshlrev_b32_e32 v154, 16, v85
	v_and_b32_e32 v155, 0xffff0000, v85
	v_mul_f32_e32 v164, v148, v148
	v_fmac_f32_e32 v164, v149, v149
	v_fmac_f32_e32 v164, v150, v150
	v_fmac_f32_e32 v164, v151, v151
	v_fmac_f32_e32 v164, v152, v152
	v_fmac_f32_e32 v164, v153, v153
	v_fmac_f32_e32 v164, v154, v154
	v_fmac_f32_e32 v164, v155, v155
	v_mul_f32_e32 v148, v148, v28
	v_mul_f32_e32 v149, v149, v29
	v_add_f32_dpp v164, v164, v164 quad_perm:[1,0,3,2] row_mask:0xf bank_mask:0xf
	v_mul_f32_e32 v150, v150, v30
	v_mul_f32_e32 v151, v151, v31
	v_add_f32_dpp v164, v164, v164 quad_perm:[2,3,0,1] row_mask:0xf bank_mask:0xf
	v_mul_f32_e32 v152, v152, v32
	v_mul_f32_e32 v153, v153, v33
	v_add_f32_dpp v164, v164, v164 row_half_mirror row_mask:0xf bank_mask:0xf
	v_mul_f32_e32 v154, v154, v34
	v_mul_f32_e32 v155, v155, v35
	v_add_f32_dpp v164, v164, v164 row_mirror row_mask:0xf bank_mask:0xf
	s_nop 0
	v_readlane_b32 s0, v164, 0
	v_readlane_b32 s1, v164, 16
	v_readlane_b32 s2, v164, 32
	v_readlane_b32 s3, v164, 48
	s_nop 1
	v_mov_b32_e32 v166, s0
	v_add_f32_e32 v166, s1, v166
	v_add_f32_e32 v166, s2, v166
	v_add_f32_e32 v166, s3, v166
	v_add_f32_e32 v166, 0x3a0637bd, v166
	v_rsq_f32_e32 v165, v166
	s_nop 0
	v_mul_f32_e32 v148, v148, v165
	v_mul_f32_e32 v149, v149, v165
	v_mul_f32_e32 v150, v150, v165
	v_mul_f32_e32 v151, v151, v165
	v_mul_f32_e32 v152, v152, v165
	v_mul_f32_e32 v153, v153, v165
	v_mul_f32_e32 v154, v154, v165
	v_mul_f32_e32 v155, v155, v165
	v_cvt_pk_bf16_f32 v156, v148, v149
	v_cvt_pk_bf16_f32 v157, v150, v151
	v_cvt_pk_bf16_f32 v158, v152, v153
	v_cvt_pk_bf16_f32 v159, v154, v155
	global_store_dwordx4 v4, v[156:159], s[34:35]
	v_add_f32_e32 v176, v102, v11
	v_mul_f32_e64 v177, |v176|, s47
	v_exp_f32_e32 v177, v177
	s_nop 0
	v_add_f32_e32 v178, 1.0, v177
	v_add_f32_e32 v179, -1.0, v178
	v_log_f32_e32 v180, v178
	v_rcp_f32_e32 v181, v179
	v_cmp_eq_f32_e32 vcc, 0, v179
	s_nop 0
	v_mul_f32_e32 v181, v177, v181
	s_nop 0
	v_cndmask_b32_e64 v181, v181, 1.0, vcc
	v_mul_f32_e32 v180, 0x3f317218, v180
	v_mul_f32_e32 v180, v180, v181
	v_min_f32_e32 v177, 0, v176
	v_sub_f32_e32 v177, v177, v180
	v_cndmask_b32_e64 v177, v176, v177, s[68:69]
	s_mov_b64 exec, 0xffff
	global_store_dword v8, v177, s[44:45]
	s_mov_b64 exec, -1
	s_waitcnt vmcnt(12)
	s_add_i32 s11, s10, 0x4000
	s_lshr_b32 s0, s11, 8
	s_mul_i32 s0, s0, 57
	s_lshr_b32 s0, s0, 9
	s_mul_i32 s1, s0, 0x900
	s_sub_i32 s43, s11, s1
	s_mul_i32 s1, s0, 0x9000
	s_lshl_b32 s2, s43, 2
	s_add_i32 s1, s1, s2
	s_add_u32 s44, s4, s1
	s_addc_u32 s45, s5, 0
	s_lshl_b32 s1, s11, 11
	s_add_u32 s22, s56, s1
	s_addc_u32 s23, s57, 0
	s_lshl_b32 s1, s11, 9
	s_add_u32 s28, s58, s1
	s_addc_u32 s29, s59, 0
	s_add_u32 s30, s62, s1
	s_addc_u32 s31, s63, 0
	s_lshl_b32 s1, s11, 10
	s_add_u32 s34, s64, s1
	s_addc_u32 s35, s65, 0
	v_xor_b32_e32 v168, v9, v128
	v_xor_b32_e32 v169, v9, v129
	v_xor_b32_e32 v170, v9, v130
	v_xor_b32_e32 v171, v9, v131
	v_xor_b32_e32 v172, v9, v132
	v_xor_b32_e32 v173, v9, v133
	v_xor_b32_e32 v174, v9, v134
	v_xor_b32_e32 v175, v9, v135
	s_cmpk_ge_u32 s43, 0x100
	v_lshlrev_b32_e32 v148, 16, v104
	v_and_b32_e32 v149, 0xffff0000, v104
	v_lshlrev_b32_e32 v150, 16, v105
	v_and_b32_e32 v151, 0xffff0000, v105
	v_lshlrev_b32_e32 v152, 16, v106
	v_and_b32_e32 v153, 0xffff0000, v106
	v_lshlrev_b32_e32 v154, 16, v107
	v_and_b32_e32 v155, 0xffff0000, v107
	v_mul_f32_e32 v164, v148, v148
	v_fmac_f32_e32 v164, v149, v149
	v_fmac_f32_e32 v164, v150, v150
	v_fmac_f32_e32 v164, v151, v151
	v_fmac_f32_e32 v164, v152, v152
	v_fmac_f32_e32 v164, v153, v153
	v_fmac_f32_e32 v164, v154, v154
	v_fmac_f32_e32 v164, v155, v155
	v_mul_f32_e32 v148, v148, v12
	v_mul_f32_e32 v149, v149, v13
	v_add_f32_dpp v164, v164, v164 quad_perm:[1,0,3,2] row_mask:0xf bank_mask:0xf
	v_mul_f32_e32 v150, v150, v14
	v_mul_f32_e32 v151, v151, v15
	v_add_f32_dpp v164, v164, v164 quad_perm:[2,3,0,1] row_mask:0xf bank_mask:0xf
	v_mul_f32_e32 v152, v152, v16
	v_mul_f32_e32 v153, v153, v17
	v_add_f32_dpp v164, v164, v164 row_half_mirror row_mask:0xf bank_mask:0xf
	v_mul_f32_e32 v154, v154, v18
	v_mul_f32_e32 v155, v155, v19
	v_add_f32_dpp v164, v164, v164 row_mirror row_mask:0xf bank_mask:0xf
	v_add_f32_e32 v164, 0x390637bd, v164
	v_rsq_f32_e32 v165, v164
	s_nop 0
	v_mul_f32_e32 v148, v148, v165
	v_mul_f32_e32 v149, v149, v165
	v_mul_f32_e32 v150, v150, v165
	v_mul_f32_e32 v151, v151, v165
	v_mul_f32_e32 v152, v152, v165
	v_mul_f32_e32 v153, v153, v165
	v_mul_f32_e32 v154, v154, v165
	v_mul_f32_e32 v155, v155, v165
	s_cbranch_scc0 .Lpp_norope_q0_8
	v_mul_f32_dpp v156, v148, v168 row_ror:8 row_mask:0xf bank_mask:0xf
	v_mul_f32_dpp v157, v149, v169 row_ror:8 row_mask:0xf bank_mask:0xf
	v_mul_f32_dpp v158, v150, v170 row_ror:8 row_mask:0xf bank_mask:0xf
	v_mul_f32_dpp v159, v151, v171 row_ror:8 row_mask:0xf bank_mask:0xf
	v_mul_f32_dpp v160, v152, v172 row_ror:8 row_mask:0xf bank_mask:0xf
	v_mul_f32_dpp v161, v153, v173 row_ror:8 row_mask:0xf bank_mask:0xf
	v_mul_f32_dpp v162, v154, v174 row_ror:8 row_mask:0xf bank_mask:0xf
	v_mul_f32_dpp v163, v155, v175 row_ror:8 row_mask:0xf bank_mask:0xf
	v_fmac_f32_e32 v156, v148, v120
	v_fmac_f32_e32 v157, v149, v121
	v_fmac_f32_e32 v158, v150, v122
	v_fmac_f32_e32 v159, v151, v123
	v_fmac_f32_e32 v160, v152, v124
	v_fmac_f32_e32 v161, v153, v125
	v_fmac_f32_e32 v162, v154, v126
	v_fmac_f32_e32 v163, v155, v127
	s_branch .Lpp_ropedone_q0_8

.Lpp_ropedone_kk_8:
	v_cvt_pk_bf16_f32 v156, v156, v157
	v_cvt_pk_bf16_f32 v157, v158, v159
	v_cvt_pk_bf16_f32 v158, v160, v161
	v_cvt_pk_bf16_f32 v159, v162, v163
	s_mov_b64 exec, 0xffffffff
	global_store_dwordx4 v4, v[156:159], s[28:29]
	s_mov_b64 exec, s[66:67]
	global_store_dwordx4 v4, v[156:159], s[30:31]
	s_mov_b64 exec, -1
	v_lshlrev_b32_e32 v148, 16, v116
	v_and_b32_e32 v149, 0xffff0000, v116
	v_lshlrev_b32_e32 v150, 16, v117
	v_and_b32_e32 v151, 0xffff0000, v117
	v_lshlrev_b32_e32 v152, 16, v118
	v_and_b32_e32 v153, 0xffff0000, v118
	v_lshlrev_b32_e32 v154, 16, v119
	v_and_b32_e32 v155, 0xffff0000, v119
	v_mul_f32_e32 v164, v148, v148
	v_fmac_f32_e32 v164, v149, v149
	v_fmac_f32_e32 v164, v150, v150
	v_fmac_f32_e32 v164, v151, v151
	v_fmac_f32_e32 v164, v152, v152
	v_fmac_f32_e32 v164, v153, v153
	v_fmac_f32_e32 v164, v154, v154
	v_fmac_f32_e32 v164, v155, v155
	v_mul_f32_e32 v148, v148, v28
	v_mul_f32_e32 v149, v149, v29
	v_add_f32_dpp v164, v164, v164 quad_perm:[1,0,3,2] row_mask:0xf bank_mask:0xf
	v_mul_f32_e32 v150, v150, v30
	v_mul_f32_e32 v151, v151, v31
	v_add_f32_dpp v164, v164, v164 quad_perm:[2,3,0,1] row_mask:0xf bank_mask:0xf
	v_mul_f32_e32 v152, v152, v32
	v_mul_f32_e32 v153, v153, v33
	v_add_f32_dpp v164, v164, v164 row_half_mirror row_mask:0xf bank_mask:0xf
	v_mul_f32_e32 v154, v154, v34
	v_mul_f32_e32 v155, v155, v35
	v_add_f32_dpp v164, v164, v164 row_mirror row_mask:0xf bank_mask:0xf
	s_nop 0
	v_readlane_b32 s0, v164, 0
	v_readlane_b32 s1, v164, 16
	v_readlane_b32 s2, v164, 32
	v_readlane_b32 s3, v164, 48
	s_nop 1
	v_mov_b32_e32 v166, s0
	v_add_f32_e32 v166, s1, v166
	v_add_f32_e32 v166, s2, v166
	v_add_f32_e32 v166, s3, v166
	v_add_f32_e32 v166, 0x3a0637bd, v166
	v_rsq_f32_e32 v165, v166
	s_nop 0
	v_mul_f32_e32 v148, v148, v165
	v_mul_f32_e32 v149, v149, v165
	v_mul_f32_e32 v150, v150, v165
	v_mul_f32_e32 v151, v151, v165
	v_mul_f32_e32 v152, v152, v165
	v_mul_f32_e32 v153, v153, v165
	v_mul_f32_e32 v154, v154, v165
	v_mul_f32_e32 v155, v155, v165
	v_cvt_pk_bf16_f32 v156, v148, v149
	v_cvt_pk_bf16_f32 v157, v150, v151
	v_cvt_pk_bf16_f32 v158, v152, v153
	v_cvt_pk_bf16_f32 v159, v154, v155
	global_store_dwordx4 v4, v[156:159], s[34:35]
	v_add_f32_e32 v176, v136, v11
	v_mul_f32_e64 v177, |v176|, s47
	v_exp_f32_e32 v177, v177
	s_nop 0
	v_add_f32_e32 v178, 1.0, v177
	v_add_f32_e32 v179, -1.0, v178
	v_log_f32_e32 v180, v178
	v_rcp_f32_e32 v181, v179
	v_cmp_eq_f32_e32 vcc, 0, v179
	s_nop 0
	v_mul_f32_e32 v181, v177, v181
	s_nop 0
	v_cndmask_b32_e64 v181, v181, 1.0, vcc
	v_mul_f32_e32 v180, 0x3f317218, v180
	v_mul_f32_e32 v180, v180, v181
	v_min_f32_e32 v177, 0, v176
	v_sub_f32_e32 v177, v177, v180
	v_cndmask_b32_e64 v177, v176, v177, s[68:69]
	s_mov_b64 exec, 0xffff
	global_store_dword v8, v177, s[44:45]
	s_mov_b64 exec, -1
	s_branch .LBB0_6309
.Lpp_orig:
	s_waitcnt vmcnt(0)
	v_mov_b32_e32 v20, v0
	v_readlane_b32 s8, v251, 57
	v_readfirstlane_b32 s0, v20
	s_ashr_i32 s0, s0, 6
	v_readlane_b32 s1, v251, 61
	v_readlane_b32 s10, v251, 59
	v_readlane_b32 s11, v251, 60
	s_add_i32 s24, s0, s1
	s_mov_b64 s[20:21], s[10:11]
	s_cmpk_gt_i32 s24, 0x47ff
	v_readlane_b32 s9, v251, 58
	s_cbranch_scc1 .LBB0_6309
	s_add_u32 s28, s20, 0x41490000
	s_addc_u32 s29, s21, 0
	s_add_u32 s2, s20, 0x4b690000
	v_readlane_b32 s8, v255, 20
	s_addc_u32 s3, s21, 0
	s_lshl_b32 s6, s8, 7
	v_readlane_b32 s48, v251, 5
	s_lshl_b64 s[30:31], s[6:7], 2
	v_readlane_b32 s56, v251, 13
	v_readlane_b32 s57, v251, 14
	s_add_u32 s0, s56, s30
	s_addc_u32 s1, s57, s31
	s_lshl_b32 s6, s8, 8
	v_readlane_b32 s60, v251, 17
	s_lshl_b64 s[4:5], s[6:7], 2
	v_readlane_b32 s61, v251, 18
	s_add_u32 s4, s60, s4
	s_addc_u32 s5, s61, s5
	s_lshl_b32 s6, s8, 9
	v_readlane_b32 s58, v251, 15
	s_lshl_b64 s[26:27], s[6:7], 2
	v_readlane_b32 s59, v251, 16
	s_add_u32 s26, s58, s26
	v_readlane_b32 s54, v251, 11
	s_addc_u32 s27, s59, s27
	v_readlane_b32 s55, v251, 12
	s_add_u32 s46, s54, s30
	s_addc_u32 s47, s55, s31
	s_add_i32 s6, s24, s33
	s_cmpk_lt_i32 s6, 0x4800
	s_cselect_b32 s30, s6, 0
	s_ashr_i32 s31, s30, 31
	s_lshl_b64 s[34:35], s[30:31], 9
	s_add_u32 s34, s2, s34
	s_addc_u32 s35, s3, s35
	s_mul_i32 s25, s30, 0x2400
	v_and_b32_e32 v21, 63, v20
	s_mul_hi_i32 s6, s30, 0x2400
	s_add_u32 s30, s28, s25
	v_cmp_gt_u32_e64 s[38:39], 32, v21
	v_mov_b32_e32 v1, 0xf00
	v_mov_b32_e32 v2, 0xc00
	s_addc_u32 s31, s29, s6
	v_lshlrev_b32_e32 v26, 4, v21
	s_waitcnt lgkmcnt(1)
	v_mov_b32_e32 v27, v3
	v_lshlrev_b32_e32 v22, 3, v21
	v_cndmask_b32_e64 v1, v1, v2, s[38:39]
	v_lshl_add_u64 v[4:5], s[30:31], 0, v[26:27]
	s_movk_i32 s6, 0x1000
	s_waitcnt lgkmcnt(0)
	v_add_u32_e32 v24, v1, v22
	v_and_b32_e32 v1, 15, v20
	v_add_co_u32_e32 v4, vcc, s6, v4
	v_lshlrev_b32_e32 v2, 2, v1
	s_nop 0
	v_addc_co_u32_e32 v5, vcc, 0, v5, vcc
	v_lshlrev_b32_e32 v1, 1, v24
	s_ashr_i32 s25, s24, 31
	global_load_dword v118, v2, s[34:35]
	global_load_dwordx4 v[36:39], v[4:5], off offset:3072
	global_load_dwordx4 v[40:43], v1, s[30:31]
	global_load_dwordx4 v[44:47], v[4:5], off offset:1024
	global_load_dwordx4 v[48:51], v[4:5], off
	s_lshl_b64 s[30:31], s[24:25], 9
	v_lshl_add_u64 v[80:81], s[2:3], 0, v[2:3]
	s_add_u32 s2, s2, s30
	s_addc_u32 s3, s3, s31
	global_load_dword v121, v2, s[2:3]
	s_mul_i32 s2, s24, 0x2400
	s_mul_hi_i32 s3, s24, 0x2400
	s_add_u32 s2, s28, s2
	s_addc_u32 s3, s29, s3
	v_lshl_add_u64 v[4:5], s[2:3], 0, v[26:27]
	v_add_co_u32_e32 v16, vcc, s6, v4
	v_lshlrev_b32_e32 v28, 5, v21
	s_nop 0
	v_addc_co_u32_e32 v17, vcc, 0, v5, vcc
	global_load_dwordx4 v[4:7], v[16:17], off offset:3072
	global_load_dwordx4 v[8:11], v1, s[2:3]
	global_load_dwordx4 v[12:15], v[16:17], off offset:1024
	s_nop 0
	global_load_dwordx4 v[16:19], v[16:17], off
	v_and_b32_e32 v2, 0xe0, v28
	v_and_b32_e32 v1, 8, v20
	v_lshl_add_u64 v[30:31], s[20:21], 0, v[2:3]
	v_and_b32_e32 v2, 64, v224
	v_cmp_eq_u32_e64 s[40:41], 0, v1
	v_xor_b32_e32 v1, 8, v224
	v_add_u32_e32 v2, 64, v2
	v_cmp_lt_i32_e32 vcc, v1, v2
	v_xor_b32_e32 v23, 4, v224
	s_mov_b64 s[2:3], 0xe8000
	v_cndmask_b32_e32 v1, v224, v1, vcc
	v_cmp_lt_i32_e32 vcc, v23, v2
	v_lshl_add_u64 v[82:83], v[30:31], 0, s[2:3]
	v_lshl_add_u64 v[84:85], s[20:21], 0, v[26:27]
	v_cndmask_b32_e32 v23, v224, v23, vcc
	v_lshlrev_b32_e32 v93, 2, v23
	v_xor_b32_e32 v23, 2, v224
	v_cmp_lt_i32_e32 vcc, v23, v2
	s_mov_b64 s[2:3], 0x4bf90000
	v_lshl_add_u64 v[86:87], v[84:85], 0, s[2:3]
	v_cndmask_b32_e32 v23, v224, v23, vcc
	v_lshlrev_b32_e32 v112, 2, v23
	v_xor_b32_e32 v23, 1, v224
	v_cmp_lt_i32_e32 vcc, v23, v2
	s_mov_b64 s[2:3], 0x4e390000
	v_lshl_add_u64 v[88:89], v[84:85], 0, s[2:3]
	v_cndmask_b32_e32 v23, v224, v23, vcc
	v_lshlrev_b32_e32 v113, 2, v23
	v_xor_b32_e32 v23, 16, v224
	v_cmp_lt_i32_e32 vcc, v23, v2
	s_mov_b64 s[2:3], 0x4ec90000
	v_lshl_add_u64 v[90:91], v[84:85], 0, s[2:3]
	v_cndmask_b32_e32 v23, v224, v23, vcc
	v_lshlrev_b32_e32 v114, 2, v23
	v_xor_b32_e32 v23, 32, v224
	v_cmp_lt_i32_e32 vcc, v23, v2
	v_cmp_gt_u32_e64 s[42:43], 16, v21
	v_mov_b32_e32 v29, v3
	v_cndmask_b32_e32 v2, v224, v23, vcc
	v_lshlrev_b32_e32 v115, 2, v2
	v_lshl_add_u32 v2, s8, 4, v21
	v_and_b32_e32 v21, 4, v20
	s_movk_i32 s2, 0xfc00
	v_and_b32_e32 v92, 3, v20
	v_cmp_ne_u32_e64 s[44:45], 0, v21
	v_and_b32_e32 v116, 56, v20
	v_and_b32_e32 v20, 0x1e0, v28
	v_mov_b32_e32 v21, v3
	v_lshl_add_u64 v[26:27], s[4:5], 0, v[28:29]
	s_mov_b32 s3, -1
	v_readlane_b32 s50, v251, 7
	v_readlane_b32 s51, v251, 8
	v_lshl_add_u64 v[94:95], s[46:47], 0, v[20:21]
	v_lshl_add_u64 v[26:27], v[26:27], 0, s[2:3]
	v_lshl_add_u64 v[20:21], s[0:1], 0, v[20:21]
	v_lshlrev_b32_e32 v1, 2, v1
	v_lshl_add_u64 v[96:97], s[26:27], 0, v[28:29]
	v_lshl_add_u64 v[98:99], v[2:3], 2, s[50:51]
	v_cndmask_b32_e64 v101, v27, v21, s[38:39]
	v_cndmask_b32_e64 v100, v26, v20, s[38:39]
	v_lshlrev_b32_e32 v2, 1, v22
	v_lshlrev_b32_e32 v117, 1, v24
	v_readlane_b32 s9, v255, 21
	v_readlane_b32 s49, v251, 6
	v_readlane_b32 s52, v251, 9
	v_readlane_b32 s53, v251, 10
	v_readlane_b32 s62, v251, 19
	v_readlane_b32 s63, v251, 20
	s_branch .LBB0_6301

.LBB0_6454:
	s_andn2_b64 vcc, exec, s[0:1]
	s_cbranch_vccnz .LBB0_6626
	v_readlane_b32 s0, v251, 2
	s_nop 3
	s_cmpk_lg_u32 s0, 0x100
	s_cbranch_scc1 .Lmp_orig
	v_readlane_b32 s4, v251, 59
	v_readlane_b32 s5, v251, 60
	v_readlane_b32 s8, v255, 20
	v_readlane_b32 s10, v251, 61
	v_readfirstlane_b32 s0, v0
	v_readlane_b32 s62, v251, 23
	v_readlane_b32 s63, v251, 24
	v_readlane_b32 s64, v251, 25
	v_readlane_b32 s65, v251, 26
	s_nop 3
	s_lshr_b32 s0, s0, 6
	s_add_i32 s10, s10, s0
	s_mul_i32 s1, s8, 0x300
	s_add_u32 s62, s62, s1
	s_addc_u32 s63, s63, 0
	s_add_u32 s64, s64, s1
	s_addc_u32 s65, s65, 0
	s_add_u32 s48, s4, 0x50790000
	s_addc_u32 s49, s5, 0
	s_add_u32 s50, s4, 0x52290000
	s_addc_u32 s51, s5, 0
	s_add_u32 s52, s4, 0x4b690000
	s_addc_u32 s53, s5, 0
	s_add_u32 s54, s4, 0x1e8000
	s_addc_u32 s55, s5, 0
	s_add_u32 s56, s4, 0x228000
	s_addc_u32 s57, s5, 0
	s_add_u32 s58, s4, 0x54690000
	s_addc_u32 s59, s5, 0
	s_add_u32 s44, s4, 0x56190000
	s_addc_u32 s45, s5, 0
	v_and_b32_e32 v1, 63, v0
	v_and_b32_e32 v2, 15, v1
	v_lshrrev_b32_e32 v100, 4, v1
	s_movk_i32 s0, 0x180
	v_lshlrev_b32_e32 v4, 4, v2
	v_mad_u32_u24 v4, v100, s0, v4
	v_lshlrev_b32_e32 v5, 3, v2
	v_mad_u32_u24 v5, v100, s0, v5
	v_add_u32_e32 v5, 0x100, v5
	v_lshlrev_b32_e32 v6, 9, v100
	v_lshl_add_u32 v6, v2, 4, v6
	v_lshlrev_b32_e32 v7, 4, v2
	v_add_u32_e32 v7, 64, v7
	v_and_b32_e32 v8, 7, v2
	v_lshlrev_b32_e32 v8, 4, v8
	v_and_b32_e32 v9, 8, v2
	v_lshlrev_b32_e32 v9, 28, v9
	v_xor_b32_e32 v9, 0x80000000, v9
	v_lshlrev_b32_e32 v101, 5, v2
	v_lshlrev_b32_e32 v102, 4, v2
	global_load_dwordx4 v[10:13], v101, s[62:63]
	global_load_dwordx4 v[14:17], v101, s[62:63] offset:16
	global_load_dwordx4 v[18:21], v102, s[62:63] offset:512
	global_load_dwordx4 v[22:25], v101, s[64:65]
	global_load_dwordx4 v[26:29], v101, s[64:65] offset:16
	global_load_dwordx4 v[30:33], v102, s[64:65] offset:512
	s_add_i32 s11, s10, 0x0
	s_lshr_b32 s0, s11, 8
	s_mul_i32 s0, s0, 57
	s_lshr_b32 s0, s0, 9
	s_mul_i32 s0, s0, 0x900
	s_sub_i32 s0, s11, s0
	s_sub_i32 s0, s0, 0x100
	s_max_i32 s0, s0, 0
	s_mul_i32 s1, s11, 0x600
	s_add_u32 s12, s48, s1
	s_addc_u32 s13, s49, 0
	s_lshl_b32 s1, s11, 11
	s_add_u32 s14, s50, s1
	s_addc_u32 s15, s51, 0
	s_lshl_b32 s1, s11, 9
	s_add_u32 s16, s52, s1
	s_addc_u32 s17, s53, 0
	s_lshl_b32 s1, s0, 7
	s_add_u32 s18, s54, s1
	s_addc_u32 s19, s55, 0
	s_add_u32 s22, s56, s1
	s_addc_u32 s23, s57, 0
	global_load_dwordx4 v[34:37], v4, s[12:13]
	global_load_dwordx2 v[38:39], v5, s[12:13]
	global_load_dwordx4 v[40:43], v6, s[14:15]
	global_load_dwordx4 v[44:47], v7, s[16:17]
	global_load_dwordx4 v[48:51], v8, s[18:19]
	global_load_dwordx4 v[52:55], v8, s[22:23]
	s_add_i32 s11, s10, 0x800
	s_lshr_b32 s0, s11, 8
	s_mul_i32 s0, s0, 57
	s_lshr_b32 s0, s0, 9
	s_mul_i32 s0, s0, 0x900
	s_sub_i32 s0, s11, s0
	s_sub_i32 s0, s0, 0x100
	s_max_i32 s0, s0, 0
	s_mul_i32 s1, s11, 0x600
	s_add_u32 s12, s48, s1
	s_addc_u32 s13, s49, 0
	s_lshl_b32 s1, s11, 11
	s_add_u32 s14, s50, s1
	s_addc_u32 s15, s51, 0
	s_lshl_b32 s1, s11, 9
	s_add_u32 s16, s52, s1
	s_addc_u32 s17, s53, 0
	s_lshl_b32 s1, s0, 7
	s_add_u32 s18, s54, s1
	s_addc_u32 s19, s55, 0
	s_add_u32 s22, s56, s1
	s_addc_u32 s23, s57, 0
	global_load_dwordx4 v[56:59], v4, s[12:13]
	global_load_dwordx2 v[60:61], v5, s[12:13]
	global_load_dwordx4 v[62:65], v6, s[14:15]
	global_load_dwordx4 v[66:69], v7, s[16:17]
	global_load_dwordx4 v[70:73], v8, s[18:19]
	global_load_dwordx4 v[74:77], v8, s[22:23]
	s_add_i32 s11, s10, 0x1000
	s_lshr_b32 s0, s11, 8
	s_mul_i32 s0, s0, 57
	s_lshr_b32 s0, s0, 9
	s_mul_i32 s0, s0, 0x900
	s_sub_i32 s0, s11, s0
	s_sub_i32 s0, s0, 0x100
	s_max_i32 s0, s0, 0
	s_mul_i32 s1, s11, 0x600
	s_add_u32 s12, s48, s1
	s_addc_u32 s13, s49, 0
	s_lshl_b32 s1, s11, 11
	s_add_u32 s14, s50, s1
	s_addc_u32 s15, s51, 0
	s_lshl_b32 s1, s11, 9
	s_add_u32 s16, s52, s1
	s_addc_u32 s17, s53, 0
	s_lshl_b32 s1, s0, 7
	s_add_u32 s18, s54, s1
	s_addc_u32 s19, s55, 0
	s_add_u32 s22, s56, s1
	s_addc_u32 s23, s57, 0
	global_load_dwordx4 v[78:81], v4, s[12:13]
	global_load_dwordx2 v[82:83], v5, s[12:13]
	global_load_dwordx4 v[84:87], v6, s[14:15]
	global_load_dwordx4 v[88:91], v7, s[16:17]
	global_load_dwordx4 v[92:95], v8, s[18:19]
	global_load_dwordx4 v[96:99], v8, s[22:23]
	s_waitcnt vmcnt(18)
	v_mul_f32_e32 v10, 0x3fb8aa3b, v10
	v_mul_f32_e32 v11, 0x3fb8aa3b, v11
	v_mul_f32_e32 v12, 0x3fb8aa3b, v12
	v_mul_f32_e32 v13, 0x3fb8aa3b, v13
	v_mul_f32_e32 v14, 0x3fb8aa3b, v14
	v_mul_f32_e32 v15, 0x3fb8aa3b, v15
	v_mul_f32_e32 v16, 0x3fb8aa3b, v16
	v_mul_f32_e32 v17, 0x3fb8aa3b, v17
	v_mul_f32_e32 v18, 0x3fb8aa3b, v18
	v_mul_f32_e32 v19, 0x3fb8aa3b, v19
	v_mul_f32_e32 v20, 0x3fb8aa3b, v20
	v_mul_f32_e32 v21, 0x3fb8aa3b, v21
	v_mul_f32_e32 v22, 0x415db3d7, v22
	v_mul_f32_e32 v23, 0x415db3d7, v23
	v_mul_f32_e32 v24, 0x415db3d7, v24
	v_mul_f32_e32 v25, 0x415db3d7, v25
	v_mul_f32_e32 v26, 0x415db3d7, v26
	v_mul_f32_e32 v27, 0x415db3d7, v27
	v_mul_f32_e32 v28, 0x415db3d7, v28
	v_mul_f32_e32 v29, 0x415db3d7, v29
	v_mul_f32_e32 v30, 0x415db3d7, v30
	v_mul_f32_e32 v31, 0x415db3d7, v31
	v_mul_f32_e32 v32, 0x415db3d7, v32
	v_mul_f32_e32 v33, 0x415db3d7, v33
	s_waitcnt vmcnt(12)
	s_add_i32 s11, s10, 0x0
	s_lshr_b32 s0, s11, 8
	s_mul_i32 s0, s0, 57
	s_lshr_b32 s0, s0, 9
	s_mul_i32 s0, s0, 0x900
	s_sub_i32 s0, s11, s0
	s_mul_i32 s1, s11, 0x600
	s_add_u32 s28, s58, s1
	s_addc_u32 s29, s59, 0
	s_add_u32 s30, s44, s1
	s_addc_u32 s31, s45, 0
	v_xor_b32_e32 v114, v9, v52
	v_xor_b32_e32 v115, v9, v53
	v_xor_b32_e32 v116, v9, v54
	v_xor_b32_e32 v117, v9, v55
	s_cmpk_ge_u32 s0, 0x100
	v_lshlrev_b32_e32 v100, 16, v34
	v_and_b32_e32 v101, 0xffff0000, v34
	v_lshlrev_b32_e32 v102, 16, v35
	v_and_b32_e32 v103, 0xffff0000, v35
	v_lshlrev_b32_e32 v104, 16, v36
	v_and_b32_e32 v105, 0xffff0000, v36
	v_lshlrev_b32_e32 v106, 16, v37
	v_and_b32_e32 v107, 0xffff0000, v37
	v_lshlrev_b32_e32 v108, 16, v38
	v_and_b32_e32 v109, 0xffff0000, v38
	v_lshlrev_b32_e32 v110, 16, v39
	v_and_b32_e32 v111, 0xffff0000, v39
	v_mul_f32_e32 v112, v100, v100
	v_fmac_f32_e32 v112, v101, v101
	v_fmac_f32_e32 v112, v102, v102
	v_fmac_f32_e32 v112, v103, v103
	v_fmac_f32_e32 v112, v104, v104
	v_fmac_f32_e32 v112, v105, v105
	v_fmac_f32_e32 v112, v106, v106
	v_fmac_f32_e32 v112, v107, v107
	v_fmac_f32_e32 v112, v108, v108
	v_fmac_f32_e32 v112, v109, v109
	v_fmac_f32_e32 v112, v110, v110
	v_fmac_f32_e32 v112, v111, v111
	v_mul_f32_e32 v100, v100, v10
	v_mul_f32_e32 v101, v101, v11
	v_add_f32_dpp v112, v112, v112 quad_perm:[1,0,3,2] row_mask:0xf bank_mask:0xf
	v_mul_f32_e32 v102, v102, v12
	v_mul_f32_e32 v103, v103, v13
	v_add_f32_dpp v112, v112, v112 quad_perm:[2,3,0,1] row_mask:0xf bank_mask:0xf
	v_mul_f32_e32 v104, v104, v14
	v_mul_f32_e32 v105, v105, v15
	v_add_f32_dpp v112, v112, v112 row_half_mirror row_mask:0xf bank_mask:0xf
	v_mul_f32_e32 v106, v106, v16
	v_mul_f32_e32 v107, v107, v17
	v_add_f32_dpp v112, v112, v112 row_mirror row_mask:0xf bank_mask:0xf
	v_mul_f32_e32 v108, v108, v18
	v_mul_f32_e32 v109, v109, v19
	v_mul_f32_e32 v110, v110, v20
	v_mul_f32_e32 v111, v111, v21
	v_add_f32_e32 v112, 0x3949539c, v112
	v_rsq_f32_e32 v113, v112
	s_nop 0
	v_mul_f32_e32 v108, v108, v113
	v_mul_f32_e32 v109, v109, v113
	v_mul_f32_e32 v110, v110, v113
	v_mul_f32_e32 v111, v111, v113
	v_mul_f32_e32 v100, v100, v113
	v_mul_f32_e32 v101, v101, v113
	v_mul_f32_e32 v102, v102, v113
	v_mul_f32_e32 v103, v103, v113
	v_mul_f32_e32 v104, v104, v113
	v_mul_f32_e32 v105, v105, v113
	v_mul_f32_e32 v106, v106, v113
	v_mul_f32_e32 v107, v107, v113
	s_cbranch_scc0 .Lmp_norope_q0
	v_mul_f32_dpp v118, v108, v114 row_ror:8 row_mask:0xf bank_mask:0xf
	v_mul_f32_dpp v119, v109, v115 row_ror:8 row_mask:0xf bank_mask:0xf
	v_mul_f32_dpp v120, v110, v116 row_ror:8 row_mask:0xf bank_mask:0xf
	v_mul_f32_dpp v121, v111, v117 row_ror:8 row_mask:0xf bank_mask:0xf
	v_fmac_f32_e32 v118, v108, v48
	v_fmac_f32_e32 v119, v109, v49
	v_fmac_f32_e32 v120, v110, v50
	v_fmac_f32_e32 v121, v111, v51
	s_branch .Lmp_ropedone_q0
.Lmp_norope_q0:
	v_mov_b32_e32 v118, v108
	v_mov_b32_e32 v119, v109
	v_mov_b32_e32 v120, v110
	v_mov_b32_e32 v121, v111
.Lmp_ropedone_q0:
	v_cvt_pk_bf16_f32 v100, v100, v101
	v_cvt_pk_bf16_f32 v101, v102, v103
	v_cvt_pk_bf16_f32 v102, v104, v105
	v_cvt_pk_bf16_f32 v103, v106, v107
	v_cvt_pk_bf16_f32 v118, v118, v119
	v_cvt_pk_bf16_f32 v119, v120, v121
	global_store_dwordx4 v4, v[100:103], s[28:29]
	global_store_dwordx2 v5, v[118:119], s[28:29]
	s_nop 1
	v_lshlrev_b32_e32 v100, 16, v40
	v_and_b32_e32 v101, 0xffff0000, v40
	v_lshlrev_b32_e32 v102, 16, v41
	v_and_b32_e32 v103, 0xffff0000, v41
	v_lshlrev_b32_e32 v104, 16, v42
	v_and_b32_e32 v105, 0xffff0000, v42
	v_lshlrev_b32_e32 v106, 16, v43
	v_and_b32_e32 v107, 0xffff0000, v43
	v_mul_f32_e32 v112, v100, v100
	v_fmac_f32_e32 v112, v101, v101
	v_fmac_f32_e32 v112, v102, v102
	v_fmac_f32_e32 v112, v103, v103
	v_fmac_f32_e32 v112, v104, v104
	v_fmac_f32_e32 v112, v105, v105
	v_fmac_f32_e32 v112, v106, v106
	v_fmac_f32_e32 v112, v107, v107
	v_fmac_f32_e32 v112, v44, v44
	v_fmac_f32_e32 v112, v45, v45
	v_fmac_f32_e32 v112, v46, v46
	v_fmac_f32_e32 v112, v47, v47
	v_mul_f32_e32 v100, v100, v22
	v_mul_f32_e32 v101, v101, v23
	v_add_f32_dpp v112, v112, v112 quad_perm:[1,0,3,2] row_mask:0xf bank_mask:0xf
	v_mul_f32_e32 v102, v102, v24
	v_mul_f32_e32 v103, v103, v25
	v_add_f32_dpp v112, v112, v112 quad_perm:[2,3,0,1] row_mask:0xf bank_mask:0xf
	v_mul_f32_e32 v104, v104, v26
	v_mul_f32_e32 v105, v105, v27
	v_add_f32_dpp v112, v112, v112 row_half_mirror row_mask:0xf bank_mask:0xf
	v_mul_f32_e32 v106, v106, v28
	v_mul_f32_e32 v107, v107, v29
	v_add_f32_dpp v112, v112, v112 row_mirror row_mask:0xf bank_mask:0xf
	v_mul_f32_e32 v108, v44, v30
	v_mul_f32_e32 v109, v45, v31
	v_mul_f32_e32 v110, v46, v32
	v_mul_f32_e32 v111, v47, v33
	v_add_f32_e32 v112, 0x3949539c, v112
	v_rsq_f32_e32 v113, v112
	s_nop 0
	v_mul_f32_e32 v108, v108, v113
	v_mul_f32_e32 v109, v109, v113
	v_mul_f32_e32 v110, v110, v113
	v_mul_f32_e32 v111, v111, v113
	v_mul_f32_e32 v100, v100, v113
	v_mul_f32_e32 v101, v101, v113
	v_mul_f32_e32 v102, v102, v113
	v_mul_f32_e32 v103, v103, v113
	v_mul_f32_e32 v104, v104, v113
	v_mul_f32_e32 v105, v105, v113
	v_mul_f32_e32 v106, v106, v113
	v_mul_f32_e32 v107, v107, v113
	s_cbranch_scc0 .Lmp_norope_k0
	v_mul_f32_dpp v118, v108, v114 row_ror:8 row_mask:0xf bank_mask:0xf
	v_mul_f32_dpp v119, v109, v115 row_ror:8 row_mask:0xf bank_mask:0xf
	v_mul_f32_dpp v120, v110, v116 row_ror:8 row_mask:0xf bank_mask:0xf
	v_mul_f32_dpp v121, v111, v117 row_ror:8 row_mask:0xf bank_mask:0xf
	v_fmac_f32_e32 v118, v108, v48
	v_fmac_f32_e32 v119, v109, v49
	v_fmac_f32_e32 v120, v110, v50
	v_fmac_f32_e32 v121, v111, v51
	s_branch .Lmp_ropedone_k0

.Lmp_ropedone_k0:
	v_cvt_pk_bf16_f32 v100, v100, v101
	v_cvt_pk_bf16_f32 v101, v102, v103
	v_cvt_pk_bf16_f32 v102, v104, v105
	v_cvt_pk_bf16_f32 v103, v106, v107
	v_cvt_pk_bf16_f32 v118, v118, v119
	v_cvt_pk_bf16_f32 v119, v120, v121
	global_store_dwordx4 v4, v[100:103], s[30:31]
	global_store_dwordx2 v5, v[118:119], s[30:31]
	s_nop 1
	s_add_i32 s11, s10, 0x1800
	s_lshr_b32 s0, s11, 8
	s_mul_i32 s0, s0, 57
	s_lshr_b32 s0, s0, 9
	s_mul_i32 s0, s0, 0x900
	s_sub_i32 s0, s11, s0
	s_sub_i32 s0, s0, 0x100
	s_max_i32 s0, s0, 0
	s_mul_i32 s1, s11, 0x600
	s_add_u32 s12, s48, s1
	s_addc_u32 s13, s49, 0
	s_lshl_b32 s1, s11, 11
	s_add_u32 s14, s50, s1
	s_addc_u32 s15, s51, 0
	s_lshl_b32 s1, s11, 9
	s_add_u32 s16, s52, s1
	s_addc_u32 s17, s53, 0
	s_lshl_b32 s1, s0, 7
	s_add_u32 s18, s54, s1
	s_addc_u32 s19, s55, 0
	s_add_u32 s22, s56, s1
	s_addc_u32 s23, s57, 0
	global_load_dwordx4 v[34:37], v4, s[12:13]
	global_load_dwordx2 v[38:39], v5, s[12:13]
	global_load_dwordx4 v[40:43], v6, s[14:15]
	global_load_dwordx4 v[44:47], v7, s[16:17]
	global_load_dwordx4 v[48:51], v8, s[18:19]
	global_load_dwordx4 v[52:55], v8, s[22:23]
	s_waitcnt vmcnt(16)
	s_add_i32 s11, s10, 0x800
	s_lshr_b32 s0, s11, 8
	s_mul_i32 s0, s0, 57
	s_lshr_b32 s0, s0, 9
	s_mul_i32 s0, s0, 0x900
	s_sub_i32 s0, s11, s0
	s_mul_i32 s1, s11, 0x600
	s_add_u32 s28, s58, s1
	s_addc_u32 s29, s59, 0
	s_add_u32 s30, s44, s1
	s_addc_u32 s31, s45, 0
	v_xor_b32_e32 v114, v9, v74
	v_xor_b32_e32 v115, v9, v75
	v_xor_b32_e32 v116, v9, v76
	v_xor_b32_e32 v117, v9, v77
	s_cmpk_ge_u32 s0, 0x100
	v_lshlrev_b32_e32 v100, 16, v56
	v_and_b32_e32 v101, 0xffff0000, v56
	v_lshlrev_b32_e32 v102, 16, v57
	v_and_b32_e32 v103, 0xffff0000, v57
	v_lshlrev_b32_e32 v104, 16, v58
	v_and_b32_e32 v105, 0xffff0000, v58
	v_lshlrev_b32_e32 v106, 16, v59
	v_and_b32_e32 v107, 0xffff0000, v59
	v_lshlrev_b32_e32 v108, 16, v60
	v_and_b32_e32 v109, 0xffff0000, v60
	v_lshlrev_b32_e32 v110, 16, v61
	v_and_b32_e32 v111, 0xffff0000, v61
	v_mul_f32_e32 v112, v100, v100
	v_fmac_f32_e32 v112, v101, v101
	v_fmac_f32_e32 v112, v102, v102
	v_fmac_f32_e32 v112, v103, v103
	v_fmac_f32_e32 v112, v104, v104
	v_fmac_f32_e32 v112, v105, v105
	v_fmac_f32_e32 v112, v106, v106
	v_fmac_f32_e32 v112, v107, v107
	v_fmac_f32_e32 v112, v108, v108
	v_fmac_f32_e32 v112, v109, v109
	v_fmac_f32_e32 v112, v110, v110
	v_fmac_f32_e32 v112, v111, v111
	v_mul_f32_e32 v100, v100, v10
	v_mul_f32_e32 v101, v101, v11
	v_add_f32_dpp v112, v112, v112 quad_perm:[1,0,3,2] row_mask:0xf bank_mask:0xf
	v_mul_f32_e32 v102, v102, v12
	v_mul_f32_e32 v103, v103, v13
	v_add_f32_dpp v112, v112, v112 quad_perm:[2,3,0,1] row_mask:0xf bank_mask:0xf
	v_mul_f32_e32 v104, v104, v14
	v_mul_f32_e32 v105, v105, v15
	v_add_f32_dpp v112, v112, v112 row_half_mirror row_mask:0xf bank_mask:0xf
	v_mul_f32_e32 v106, v106, v16
	v_mul_f32_e32 v107, v107, v17
	v_add_f32_dpp v112, v112, v112 row_mirror row_mask:0xf bank_mask:0xf
	v_mul_f32_e32 v108, v108, v18
	v_mul_f32_e32 v109, v109, v19
	v_mul_f32_e32 v110, v110, v20
	v_mul_f32_e32 v111, v111, v21
	v_add_f32_e32 v112, 0x3949539c, v112
	v_rsq_f32_e32 v113, v112
	s_nop 0
	v_mul_f32_e32 v108, v108, v113
	v_mul_f32_e32 v109, v109, v113
	v_mul_f32_e32 v110, v110, v113
	v_mul_f32_e32 v111, v111, v113
	v_mul_f32_e32 v100, v100, v113
	v_mul_f32_e32 v101, v101, v113
	v_mul_f32_e32 v102, v102, v113
	v_mul_f32_e32 v103, v103, v113
	v_mul_f32_e32 v104, v104, v113
	v_mul_f32_e32 v105, v105, v113
	v_mul_f32_e32 v106, v106, v113
	v_mul_f32_e32 v107, v107, v113
	s_cbranch_scc0 .Lmp_norope_q1
	v_mul_f32_dpp v118, v108, v114 row_ror:8 row_mask:0xf bank_mask:0xf
	v_mul_f32_dpp v119, v109, v115 row_ror:8 row_mask:0xf bank_mask:0xf
	v_mul_f32_dpp v120, v110, v116 row_ror:8 row_mask:0xf bank_mask:0xf
	v_mul_f32_dpp v121, v111, v117 row_ror:8 row_mask:0xf bank_mask:0xf
	v_fmac_f32_e32 v118, v108, v70
	v_fmac_f32_e32 v119, v109, v71
	v_fmac_f32_e32 v120, v110, v72
	v_fmac_f32_e32 v121, v111, v73
	s_branch .Lmp_ropedone_q1

.Lmp_ropedone_q1:
	v_cvt_pk_bf16_f32 v100, v100, v101
	v_cvt_pk_bf16_f32 v101, v102, v103
	v_cvt_pk_bf16_f32 v102, v104, v105
	v_cvt_pk_bf16_f32 v103, v106, v107
	v_cvt_pk_bf16_f32 v118, v118, v119
	v_cvt_pk_bf16_f32 v119, v120, v121
	global_store_dwordx4 v4, v[100:103], s[28:29]
	global_store_dwordx2 v5, v[118:119], s[28:29]
	s_nop 1
	v_lshlrev_b32_e32 v100, 16, v62
	v_and_b32_e32 v101, 0xffff0000, v62
	v_lshlrev_b32_e32 v102, 16, v63
	v_and_b32_e32 v103, 0xffff0000, v63
	v_lshlrev_b32_e32 v104, 16, v64
	v_and_b32_e32 v105, 0xffff0000, v64
	v_lshlrev_b32_e32 v106, 16, v65
	v_and_b32_e32 v107, 0xffff0000, v65
	v_mul_f32_e32 v112, v100, v100
	v_fmac_f32_e32 v112, v101, v101
	v_fmac_f32_e32 v112, v102, v102
	v_fmac_f32_e32 v112, v103, v103
	v_fmac_f32_e32 v112, v104, v104
	v_fmac_f32_e32 v112, v105, v105
	v_fmac_f32_e32 v112, v106, v106
	v_fmac_f32_e32 v112, v107, v107
	v_fmac_f32_e32 v112, v66, v66
	v_fmac_f32_e32 v112, v67, v67
	v_fmac_f32_e32 v112, v68, v68
	v_fmac_f32_e32 v112, v69, v69
	v_mul_f32_e32 v100, v100, v22
	v_mul_f32_e32 v101, v101, v23
	v_add_f32_dpp v112, v112, v112 quad_perm:[1,0,3,2] row_mask:0xf bank_mask:0xf
	v_mul_f32_e32 v102, v102, v24
	v_mul_f32_e32 v103, v103, v25
	v_add_f32_dpp v112, v112, v112 quad_perm:[2,3,0,1] row_mask:0xf bank_mask:0xf
	v_mul_f32_e32 v104, v104, v26
	v_mul_f32_e32 v105, v105, v27
	v_add_f32_dpp v112, v112, v112 row_half_mirror row_mask:0xf bank_mask:0xf
	v_mul_f32_e32 v106, v106, v28
	v_mul_f32_e32 v107, v107, v29
	v_add_f32_dpp v112, v112, v112 row_mirror row_mask:0xf bank_mask:0xf
	v_mul_f32_e32 v108, v66, v30
	v_mul_f32_e32 v109, v67, v31
	v_mul_f32_e32 v110, v68, v32
	v_mul_f32_e32 v111, v69, v33
	v_add_f32_e32 v112, 0x3949539c, v112
	v_rsq_f32_e32 v113, v112
	s_nop 0
	v_mul_f32_e32 v108, v108, v113
	v_mul_f32_e32 v109, v109, v113
	v_mul_f32_e32 v110, v110, v113
	v_mul_f32_e32 v111, v111, v113
	v_mul_f32_e32 v100, v100, v113
	v_mul_f32_e32 v101, v101, v113
	v_mul_f32_e32 v102, v102, v113
	v_mul_f32_e32 v103, v103, v113
	v_mul_f32_e32 v104, v104, v113
	v_mul_f32_e32 v105, v105, v113
	v_mul_f32_e32 v106, v106, v113
	v_mul_f32_e32 v107, v107, v113
	s_cbranch_scc0 .Lmp_norope_k1
	v_mul_f32_dpp v118, v108, v114 row_ror:8 row_mask:0xf bank_mask:0xf
	v_mul_f32_dpp v119, v109, v115 row_ror:8 row_mask:0xf bank_mask:0xf
	v_mul_f32_dpp v120, v110, v116 row_ror:8 row_mask:0xf bank_mask:0xf
	v_mul_f32_dpp v121, v111, v117 row_ror:8 row_mask:0xf bank_mask:0xf
	v_fmac_f32_e32 v118, v108, v70
	v_fmac_f32_e32 v119, v109, v71
	v_fmac_f32_e32 v120, v110, v72
	v_fmac_f32_e32 v121, v111, v73
	s_branch .Lmp_ropedone_k1

.Lmp_ropedone_k1:
	v_cvt_pk_bf16_f32 v100, v100, v101
	v_cvt_pk_bf16_f32 v101, v102, v103
	v_cvt_pk_bf16_f32 v102, v104, v105
	v_cvt_pk_bf16_f32 v103, v106, v107
	v_cvt_pk_bf16_f32 v118, v118, v119
	v_cvt_pk_bf16_f32 v119, v120, v121
	global_store_dwordx4 v4, v[100:103], s[30:31]
	global_store_dwordx2 v5, v[118:119], s[30:31]
	s_nop 1
	s_add_i32 s11, s10, 0x2000
	s_lshr_b32 s0, s11, 8
	s_mul_i32 s0, s0, 57
	s_lshr_b32 s0, s0, 9
	s_mul_i32 s0, s0, 0x900
	s_sub_i32 s0, s11, s0
	s_sub_i32 s0, s0, 0x100
	s_max_i32 s0, s0, 0
	s_mul_i32 s1, s11, 0x600
	s_add_u32 s12, s48, s1
	s_addc_u32 s13, s49, 0
	s_lshl_b32 s1, s11, 11
	s_add_u32 s14, s50, s1
	s_addc_u32 s15, s51, 0
	s_lshl_b32 s1, s11, 9
	s_add_u32 s16, s52, s1
	s_addc_u32 s17, s53, 0
	s_lshl_b32 s1, s0, 7
	s_add_u32 s18, s54, s1
	s_addc_u32 s19, s55, 0
	s_add_u32 s22, s56, s1
	s_addc_u32 s23, s57, 0
	global_load_dwordx4 v[56:59], v4, s[12:13]
	global_load_dwordx2 v[60:61], v5, s[12:13]
	global_load_dwordx4 v[62:65], v6, s[14:15]
	global_load_dwordx4 v[66:69], v7, s[16:17]
	global_load_dwordx4 v[70:73], v8, s[18:19]
	global_load_dwordx4 v[74:77], v8, s[22:23]
	s_waitcnt vmcnt(20)
	s_add_i32 s11, s10, 0x1000
	s_lshr_b32 s0, s11, 8
	s_mul_i32 s0, s0, 57
	s_lshr_b32 s0, s0, 9
	s_mul_i32 s0, s0, 0x900
	s_sub_i32 s0, s11, s0
	s_mul_i32 s1, s11, 0x600
	s_add_u32 s28, s58, s1
	s_addc_u32 s29, s59, 0
	s_add_u32 s30, s44, s1
	s_addc_u32 s31, s45, 0
	v_xor_b32_e32 v114, v9, v96
	v_xor_b32_e32 v115, v9, v97
	v_xor_b32_e32 v116, v9, v98
	v_xor_b32_e32 v117, v9, v99
	s_cmpk_ge_u32 s0, 0x100
	v_lshlrev_b32_e32 v100, 16, v78
	v_and_b32_e32 v101, 0xffff0000, v78
	v_lshlrev_b32_e32 v102, 16, v79
	v_and_b32_e32 v103, 0xffff0000, v79
	v_lshlrev_b32_e32 v104, 16, v80
	v_and_b32_e32 v105, 0xffff0000, v80
	v_lshlrev_b32_e32 v106, 16, v81
	v_and_b32_e32 v107, 0xffff0000, v81
	v_lshlrev_b32_e32 v108, 16, v82
	v_and_b32_e32 v109, 0xffff0000, v82
	v_lshlrev_b32_e32 v110, 16, v83
	v_and_b32_e32 v111, 0xffff0000, v83
	v_mul_f32_e32 v112, v100, v100
	v_fmac_f32_e32 v112, v101, v101
	v_fmac_f32_e32 v112, v102, v102
	v_fmac_f32_e32 v112, v103, v103
	v_fmac_f32_e32 v112, v104, v104
	v_fmac_f32_e32 v112, v105, v105
	v_fmac_f32_e32 v112, v106, v106
	v_fmac_f32_e32 v112, v107, v107
	v_fmac_f32_e32 v112, v108, v108
	v_fmac_f32_e32 v112, v109, v109
	v_fmac_f32_e32 v112, v110, v110
	v_fmac_f32_e32 v112, v111, v111
	v_mul_f32_e32 v100, v100, v10
	v_mul_f32_e32 v101, v101, v11
	v_add_f32_dpp v112, v112, v112 quad_perm:[1,0,3,2] row_mask:0xf bank_mask:0xf
	v_mul_f32_e32 v102, v102, v12
	v_mul_f32_e32 v103, v103, v13
	v_add_f32_dpp v112, v112, v112 quad_perm:[2,3,0,1] row_mask:0xf bank_mask:0xf
	v_mul_f32_e32 v104, v104, v14
	v_mul_f32_e32 v105, v105, v15
	v_add_f32_dpp v112, v112, v112 row_half_mirror row_mask:0xf bank_mask:0xf
	v_mul_f32_e32 v106, v106, v16
	v_mul_f32_e32 v107, v107, v17
	v_add_f32_dpp v112, v112, v112 row_mirror row_mask:0xf bank_mask:0xf
	v_mul_f32_e32 v108, v108, v18
	v_mul_f32_e32 v109, v109, v19
	v_mul_f32_e32 v110, v110, v20
	v_mul_f32_e32 v111, v111, v21
	v_add_f32_e32 v112, 0x3949539c, v112
	v_rsq_f32_e32 v113, v112
	s_nop 0
	v_mul_f32_e32 v108, v108, v113
	v_mul_f32_e32 v109, v109, v113
	v_mul_f32_e32 v110, v110, v113
	v_mul_f32_e32 v111, v111, v113
	v_mul_f32_e32 v100, v100, v113
	v_mul_f32_e32 v101, v101, v113
	v_mul_f32_e32 v102, v102, v113
	v_mul_f32_e32 v103, v103, v113
	v_mul_f32_e32 v104, v104, v113
	v_mul_f32_e32 v105, v105, v113
	v_mul_f32_e32 v106, v106, v113
	v_mul_f32_e32 v107, v107, v113
	s_cbranch_scc0 .Lmp_norope_q2
	v_mul_f32_dpp v118, v108, v114 row_ror:8 row_mask:0xf bank_mask:0xf
	v_mul_f32_dpp v119, v109, v115 row_ror:8 row_mask:0xf bank_mask:0xf
	v_mul_f32_dpp v120, v110, v116 row_ror:8 row_mask:0xf bank_mask:0xf
	v_mul_f32_dpp v121, v111, v117 row_ror:8 row_mask:0xf bank_mask:0xf
	v_fmac_f32_e32 v118, v108, v92
	v_fmac_f32_e32 v119, v109, v93
	v_fmac_f32_e32 v120, v110, v94
	v_fmac_f32_e32 v121, v111, v95
	s_branch .Lmp_ropedone_q2

.Lmp_ropedone_q2:
	v_cvt_pk_bf16_f32 v100, v100, v101
	v_cvt_pk_bf16_f32 v101, v102, v103
	v_cvt_pk_bf16_f32 v102, v104, v105
	v_cvt_pk_bf16_f32 v103, v106, v107
	v_cvt_pk_bf16_f32 v118, v118, v119
	v_cvt_pk_bf16_f32 v119, v120, v121
	global_store_dwordx4 v4, v[100:103], s[28:29]
	global_store_dwordx2 v5, v[118:119], s[28:29]
	s_nop 1
	v_lshlrev_b32_e32 v100, 16, v84
	v_and_b32_e32 v101, 0xffff0000, v84
	v_lshlrev_b32_e32 v102, 16, v85
	v_and_b32_e32 v103, 0xffff0000, v85
	v_lshlrev_b32_e32 v104, 16, v86
	v_and_b32_e32 v105, 0xffff0000, v86
	v_lshlrev_b32_e32 v106, 16, v87
	v_and_b32_e32 v107, 0xffff0000, v87
	v_mul_f32_e32 v112, v100, v100
	v_fmac_f32_e32 v112, v101, v101
	v_fmac_f32_e32 v112, v102, v102
	v_fmac_f32_e32 v112, v103, v103
	v_fmac_f32_e32 v112, v104, v104
	v_fmac_f32_e32 v112, v105, v105
	v_fmac_f32_e32 v112, v106, v106
	v_fmac_f32_e32 v112, v107, v107
	v_fmac_f32_e32 v112, v88, v88
	v_fmac_f32_e32 v112, v89, v89
	v_fmac_f32_e32 v112, v90, v90
	v_fmac_f32_e32 v112, v91, v91
	v_mul_f32_e32 v100, v100, v22
	v_mul_f32_e32 v101, v101, v23
	v_add_f32_dpp v112, v112, v112 quad_perm:[1,0,3,2] row_mask:0xf bank_mask:0xf
	v_mul_f32_e32 v102, v102, v24
	v_mul_f32_e32 v103, v103, v25
	v_add_f32_dpp v112, v112, v112 quad_perm:[2,3,0,1] row_mask:0xf bank_mask:0xf
	v_mul_f32_e32 v104, v104, v26
	v_mul_f32_e32 v105, v105, v27
	v_add_f32_dpp v112, v112, v112 row_half_mirror row_mask:0xf bank_mask:0xf
	v_mul_f32_e32 v106, v106, v28
	v_mul_f32_e32 v107, v107, v29
	v_add_f32_dpp v112, v112, v112 row_mirror row_mask:0xf bank_mask:0xf
	v_mul_f32_e32 v108, v88, v30
	v_mul_f32_e32 v109, v89, v31
	v_mul_f32_e32 v110, v90, v32
	v_mul_f32_e32 v111, v91, v33
	v_add_f32_e32 v112, 0x3949539c, v112
	v_rsq_f32_e32 v113, v112
	s_nop 0
	v_mul_f32_e32 v108, v108, v113
	v_mul_f32_e32 v109, v109, v113
	v_mul_f32_e32 v110, v110, v113
	v_mul_f32_e32 v111, v111, v113
	v_mul_f32_e32 v100, v100, v113
	v_mul_f32_e32 v101, v101, v113
	v_mul_f32_e32 v102, v102, v113
	v_mul_f32_e32 v103, v103, v113
	v_mul_f32_e32 v104, v104, v113
	v_mul_f32_e32 v105, v105, v113
	v_mul_f32_e32 v106, v106, v113
	v_mul_f32_e32 v107, v107, v113
	s_cbranch_scc0 .Lmp_norope_k2
	v_mul_f32_dpp v118, v108, v114 row_ror:8 row_mask:0xf bank_mask:0xf
	v_mul_f32_dpp v119, v109, v115 row_ror:8 row_mask:0xf bank_mask:0xf
	v_mul_f32_dpp v120, v110, v116 row_ror:8 row_mask:0xf bank_mask:0xf
	v_mul_f32_dpp v121, v111, v117 row_ror:8 row_mask:0xf bank_mask:0xf
	v_fmac_f32_e32 v118, v108, v92
	v_fmac_f32_e32 v119, v109, v93
	v_fmac_f32_e32 v120, v110, v94
	v_fmac_f32_e32 v121, v111, v95
	s_branch .Lmp_ropedone_k2

.Lmp_ropedone_k2:
	v_cvt_pk_bf16_f32 v100, v100, v101
	v_cvt_pk_bf16_f32 v101, v102, v103
	v_cvt_pk_bf16_f32 v102, v104, v105
	v_cvt_pk_bf16_f32 v103, v106, v107
	v_cvt_pk_bf16_f32 v118, v118, v119
	v_cvt_pk_bf16_f32 v119, v120, v121
	global_store_dwordx4 v4, v[100:103], s[30:31]
	global_store_dwordx2 v5, v[118:119], s[30:31]
	s_nop 1
	s_add_i32 s11, s10, 0x2800
	s_lshr_b32 s0, s11, 8
	s_mul_i32 s0, s0, 57
	s_lshr_b32 s0, s0, 9
	s_mul_i32 s0, s0, 0x900
	s_sub_i32 s0, s11, s0
	s_sub_i32 s0, s0, 0x100
	s_max_i32 s0, s0, 0
	s_mul_i32 s1, s11, 0x600
	s_add_u32 s12, s48, s1
	s_addc_u32 s13, s49, 0
	s_lshl_b32 s1, s11, 11
	s_add_u32 s14, s50, s1
	s_addc_u32 s15, s51, 0
	s_lshl_b32 s1, s11, 9
	s_add_u32 s16, s52, s1
	s_addc_u32 s17, s53, 0
	s_lshl_b32 s1, s0, 7
	s_add_u32 s18, s54, s1
	s_addc_u32 s19, s55, 0
	s_add_u32 s22, s56, s1
	s_addc_u32 s23, s57, 0
	global_load_dwordx4 v[78:81], v4, s[12:13]
	global_load_dwordx2 v[82:83], v5, s[12:13]
	global_load_dwordx4 v[84:87], v6, s[14:15]
	global_load_dwordx4 v[88:91], v7, s[16:17]
	global_load_dwordx4 v[92:95], v8, s[18:19]
	global_load_dwordx4 v[96:99], v8, s[22:23]
	s_waitcnt vmcnt(20)
	s_add_i32 s11, s10, 0x1800
	s_lshr_b32 s0, s11, 8
	s_mul_i32 s0, s0, 57
	s_lshr_b32 s0, s0, 9
	s_mul_i32 s0, s0, 0x900
	s_sub_i32 s0, s11, s0
	s_mul_i32 s1, s11, 0x600
	s_add_u32 s28, s58, s1
	s_addc_u32 s29, s59, 0
	s_add_u32 s30, s44, s1
	s_addc_u32 s31, s45, 0
	v_xor_b32_e32 v114, v9, v52
	v_xor_b32_e32 v115, v9, v53
	v_xor_b32_e32 v116, v9, v54
	v_xor_b32_e32 v117, v9, v55
	s_cmpk_ge_u32 s0, 0x100
	v_lshlrev_b32_e32 v100, 16, v34
	v_and_b32_e32 v101, 0xffff0000, v34
	v_lshlrev_b32_e32 v102, 16, v35
	v_and_b32_e32 v103, 0xffff0000, v35
	v_lshlrev_b32_e32 v104, 16, v36
	v_and_b32_e32 v105, 0xffff0000, v36
	v_lshlrev_b32_e32 v106, 16, v37
	v_and_b32_e32 v107, 0xffff0000, v37
	v_lshlrev_b32_e32 v108, 16, v38
	v_and_b32_e32 v109, 0xffff0000, v38
	v_lshlrev_b32_e32 v110, 16, v39
	v_and_b32_e32 v111, 0xffff0000, v39
	v_mul_f32_e32 v112, v100, v100
	v_fmac_f32_e32 v112, v101, v101
	v_fmac_f32_e32 v112, v102, v102
	v_fmac_f32_e32 v112, v103, v103
	v_fmac_f32_e32 v112, v104, v104
	v_fmac_f32_e32 v112, v105, v105
	v_fmac_f32_e32 v112, v106, v106
	v_fmac_f32_e32 v112, v107, v107
	v_fmac_f32_e32 v112, v108, v108
	v_fmac_f32_e32 v112, v109, v109
	v_fmac_f32_e32 v112, v110, v110
	v_fmac_f32_e32 v112, v111, v111
	v_mul_f32_e32 v100, v100, v10
	v_mul_f32_e32 v101, v101, v11
	v_add_f32_dpp v112, v112, v112 quad_perm:[1,0,3,2] row_mask:0xf bank_mask:0xf
	v_mul_f32_e32 v102, v102, v12
	v_mul_f32_e32 v103, v103, v13
	v_add_f32_dpp v112, v112, v112 quad_perm:[2,3,0,1] row_mask:0xf bank_mask:0xf
	v_mul_f32_e32 v104, v104, v14
	v_mul_f32_e32 v105, v105, v15
	v_add_f32_dpp v112, v112, v112 row_half_mirror row_mask:0xf bank_mask:0xf
	v_mul_f32_e32 v106, v106, v16
	v_mul_f32_e32 v107, v107, v17
	v_add_f32_dpp v112, v112, v112 row_mirror row_mask:0xf bank_mask:0xf
	v_mul_f32_e32 v108, v108, v18
	v_mul_f32_e32 v109, v109, v19
	v_mul_f32_e32 v110, v110, v20
	v_mul_f32_e32 v111, v111, v21
	v_add_f32_e32 v112, 0x3949539c, v112
	v_rsq_f32_e32 v113, v112
	s_nop 0
	v_mul_f32_e32 v108, v108, v113
	v_mul_f32_e32 v109, v109, v113
	v_mul_f32_e32 v110, v110, v113
	v_mul_f32_e32 v111, v111, v113
	v_mul_f32_e32 v100, v100, v113
	v_mul_f32_e32 v101, v101, v113
	v_mul_f32_e32 v102, v102, v113
	v_mul_f32_e32 v103, v103, v113
	v_mul_f32_e32 v104, v104, v113
	v_mul_f32_e32 v105, v105, v113
	v_mul_f32_e32 v106, v106, v113
	v_mul_f32_e32 v107, v107, v113
	s_cbranch_scc0 .Lmp_norope_q3
	v_mul_f32_dpp v118, v108, v114 row_ror:8 row_mask:0xf bank_mask:0xf
	v_mul_f32_dpp v119, v109, v115 row_ror:8 row_mask:0xf bank_mask:0xf
	v_mul_f32_dpp v120, v110, v116 row_ror:8 row_mask:0xf bank_mask:0xf
	v_mul_f32_dpp v121, v111, v117 row_ror:8 row_mask:0xf bank_mask:0xf
	v_fmac_f32_e32 v118, v108, v48
	v_fmac_f32_e32 v119, v109, v49
	v_fmac_f32_e32 v120, v110, v50
	v_fmac_f32_e32 v121, v111, v51
	s_branch .Lmp_ropedone_q3

.Lmp_ropedone_k3:
	v_cvt_pk_bf16_f32 v100, v100, v101
	v_cvt_pk_bf16_f32 v101, v102, v103
	v_cvt_pk_bf16_f32 v102, v104, v105
	v_cvt_pk_bf16_f32 v103, v106, v107
	v_cvt_pk_bf16_f32 v118, v118, v119
	v_cvt_pk_bf16_f32 v119, v120, v121
	global_store_dwordx4 v4, v[100:103], s[30:31]
	global_store_dwordx2 v5, v[118:119], s[30:31]
	s_nop 1
	s_add_i32 s11, s10, 0x3000
	s_lshr_b32 s0, s11, 8
	s_mul_i32 s0, s0, 57
	s_lshr_b32 s0, s0, 9
	s_mul_i32 s0, s0, 0x900
	s_sub_i32 s0, s11, s0
	s_sub_i32 s0, s0, 0x100
	s_max_i32 s0, s0, 0
	s_mul_i32 s1, s11, 0x600
	s_add_u32 s12, s48, s1
	s_addc_u32 s13, s49, 0
	s_lshl_b32 s1, s11, 11
	s_add_u32 s14, s50, s1
	s_addc_u32 s15, s51, 0
	s_lshl_b32 s1, s11, 9
	s_add_u32 s16, s52, s1
	s_addc_u32 s17, s53, 0
	s_lshl_b32 s1, s0, 7
	s_add_u32 s18, s54, s1
	s_addc_u32 s19, s55, 0
	s_add_u32 s22, s56, s1
	s_addc_u32 s23, s57, 0
	global_load_dwordx4 v[34:37], v4, s[12:13]
	global_load_dwordx2 v[38:39], v5, s[12:13]
	global_load_dwordx4 v[40:43], v6, s[14:15]
	global_load_dwordx4 v[44:47], v7, s[16:17]
	global_load_dwordx4 v[48:51], v8, s[18:19]
	global_load_dwordx4 v[52:55], v8, s[22:23]
	s_waitcnt vmcnt(20)
	s_add_i32 s11, s10, 0x2000
	s_lshr_b32 s0, s11, 8
	s_mul_i32 s0, s0, 57
	s_lshr_b32 s0, s0, 9
	s_mul_i32 s0, s0, 0x900
	s_sub_i32 s0, s11, s0
	s_mul_i32 s1, s11, 0x600
	s_add_u32 s28, s58, s1
	s_addc_u32 s29, s59, 0
	s_add_u32 s30, s44, s1
	s_addc_u32 s31, s45, 0
	v_xor_b32_e32 v114, v9, v74
	v_xor_b32_e32 v115, v9, v75
	v_xor_b32_e32 v116, v9, v76
	v_xor_b32_e32 v117, v9, v77
	s_cmpk_ge_u32 s0, 0x100
	v_lshlrev_b32_e32 v100, 16, v56
	v_and_b32_e32 v101, 0xffff0000, v56
	v_lshlrev_b32_e32 v102, 16, v57
	v_and_b32_e32 v103, 0xffff0000, v57
	v_lshlrev_b32_e32 v104, 16, v58
	v_and_b32_e32 v105, 0xffff0000, v58
	v_lshlrev_b32_e32 v106, 16, v59
	v_and_b32_e32 v107, 0xffff0000, v59
	v_lshlrev_b32_e32 v108, 16, v60
	v_and_b32_e32 v109, 0xffff0000, v60
	v_lshlrev_b32_e32 v110, 16, v61
	v_and_b32_e32 v111, 0xffff0000, v61
	v_mul_f32_e32 v112, v100, v100
	v_fmac_f32_e32 v112, v101, v101
	v_fmac_f32_e32 v112, v102, v102
	v_fmac_f32_e32 v112, v103, v103
	v_fmac_f32_e32 v112, v104, v104
	v_fmac_f32_e32 v112, v105, v105
	v_fmac_f32_e32 v112, v106, v106
	v_fmac_f32_e32 v112, v107, v107
	v_fmac_f32_e32 v112, v108, v108
	v_fmac_f32_e32 v112, v109, v109
	v_fmac_f32_e32 v112, v110, v110
	v_fmac_f32_e32 v112, v111, v111
	v_mul_f32_e32 v100, v100, v10
	v_mul_f32_e32 v101, v101, v11
	v_add_f32_dpp v112, v112, v112 quad_perm:[1,0,3,2] row_mask:0xf bank_mask:0xf
	v_mul_f32_e32 v102, v102, v12
	v_mul_f32_e32 v103, v103, v13
	v_add_f32_dpp v112, v112, v112 quad_perm:[2,3,0,1] row_mask:0xf bank_mask:0xf
	v_mul_f32_e32 v104, v104, v14
	v_mul_f32_e32 v105, v105, v15
	v_add_f32_dpp v112, v112, v112 row_half_mirror row_mask:0xf bank_mask:0xf
	v_mul_f32_e32 v106, v106, v16
	v_mul_f32_e32 v107, v107, v17
	v_add_f32_dpp v112, v112, v112 row_mirror row_mask:0xf bank_mask:0xf
	v_mul_f32_e32 v108, v108, v18
	v_mul_f32_e32 v109, v109, v19
	v_mul_f32_e32 v110, v110, v20
	v_mul_f32_e32 v111, v111, v21
	v_add_f32_e32 v112, 0x3949539c, v112
	v_rsq_f32_e32 v113, v112
	s_nop 0
	v_mul_f32_e32 v108, v108, v113
	v_mul_f32_e32 v109, v109, v113
	v_mul_f32_e32 v110, v110, v113
	v_mul_f32_e32 v111, v111, v113
	v_mul_f32_e32 v100, v100, v113
	v_mul_f32_e32 v101, v101, v113
	v_mul_f32_e32 v102, v102, v113
	v_mul_f32_e32 v103, v103, v113
	v_mul_f32_e32 v104, v104, v113
	v_mul_f32_e32 v105, v105, v113
	v_mul_f32_e32 v106, v106, v113
	v_mul_f32_e32 v107, v107, v113
	s_cbranch_scc0 .Lmp_norope_q4
	v_mul_f32_dpp v118, v108, v114 row_ror:8 row_mask:0xf bank_mask:0xf
	v_mul_f32_dpp v119, v109, v115 row_ror:8 row_mask:0xf bank_mask:0xf
	v_mul_f32_dpp v120, v110, v116 row_ror:8 row_mask:0xf bank_mask:0xf
	v_mul_f32_dpp v121, v111, v117 row_ror:8 row_mask:0xf bank_mask:0xf
	v_fmac_f32_e32 v118, v108, v70
	v_fmac_f32_e32 v119, v109, v71
	v_fmac_f32_e32 v120, v110, v72
	v_fmac_f32_e32 v121, v111, v73
	s_branch .Lmp_ropedone_q4

.Lmp_ropedone_k4:
	v_cvt_pk_bf16_f32 v100, v100, v101
	v_cvt_pk_bf16_f32 v101, v102, v103
	v_cvt_pk_bf16_f32 v102, v104, v105
	v_cvt_pk_bf16_f32 v103, v106, v107
	v_cvt_pk_bf16_f32 v118, v118, v119
	v_cvt_pk_bf16_f32 v119, v120, v121
	global_store_dwordx4 v4, v[100:103], s[30:31]
	global_store_dwordx2 v5, v[118:119], s[30:31]
	s_nop 1
	s_add_i32 s11, s10, 0x3800
	s_lshr_b32 s0, s11, 8
	s_mul_i32 s0, s0, 57
	s_lshr_b32 s0, s0, 9
	s_mul_i32 s0, s0, 0x900
	s_sub_i32 s0, s11, s0
	s_sub_i32 s0, s0, 0x100
	s_max_i32 s0, s0, 0
	s_mul_i32 s1, s11, 0x600
	s_add_u32 s12, s48, s1
	s_addc_u32 s13, s49, 0
	s_lshl_b32 s1, s11, 11
	s_add_u32 s14, s50, s1
	s_addc_u32 s15, s51, 0
	s_lshl_b32 s1, s11, 9
	s_add_u32 s16, s52, s1
	s_addc_u32 s17, s53, 0
	s_lshl_b32 s1, s0, 7
	s_add_u32 s18, s54, s1
	s_addc_u32 s19, s55, 0
	s_add_u32 s22, s56, s1
	s_addc_u32 s23, s57, 0
	global_load_dwordx4 v[56:59], v4, s[12:13]
	global_load_dwordx2 v[60:61], v5, s[12:13]
	global_load_dwordx4 v[62:65], v6, s[14:15]
	global_load_dwordx4 v[66:69], v7, s[16:17]
	global_load_dwordx4 v[70:73], v8, s[18:19]
	global_load_dwordx4 v[74:77], v8, s[22:23]
	s_waitcnt vmcnt(20)
	s_add_i32 s11, s10, 0x2800
	s_lshr_b32 s0, s11, 8
	s_mul_i32 s0, s0, 57
	s_lshr_b32 s0, s0, 9
	s_mul_i32 s0, s0, 0x900
	s_sub_i32 s0, s11, s0
	s_mul_i32 s1, s11, 0x600
	s_add_u32 s28, s58, s1
	s_addc_u32 s29, s59, 0
	s_add_u32 s30, s44, s1
	s_addc_u32 s31, s45, 0
	v_xor_b32_e32 v114, v9, v96
	v_xor_b32_e32 v115, v9, v97
	v_xor_b32_e32 v116, v9, v98
	v_xor_b32_e32 v117, v9, v99
	s_cmpk_ge_u32 s0, 0x100
	v_lshlrev_b32_e32 v100, 16, v78
	v_and_b32_e32 v101, 0xffff0000, v78
	v_lshlrev_b32_e32 v102, 16, v79
	v_and_b32_e32 v103, 0xffff0000, v79
	v_lshlrev_b32_e32 v104, 16, v80
	v_and_b32_e32 v105, 0xffff0000, v80
	v_lshlrev_b32_e32 v106, 16, v81
	v_and_b32_e32 v107, 0xffff0000, v81
	v_lshlrev_b32_e32 v108, 16, v82
	v_and_b32_e32 v109, 0xffff0000, v82
	v_lshlrev_b32_e32 v110, 16, v83
	v_and_b32_e32 v111, 0xffff0000, v83
	v_mul_f32_e32 v112, v100, v100
	v_fmac_f32_e32 v112, v101, v101
	v_fmac_f32_e32 v112, v102, v102
	v_fmac_f32_e32 v112, v103, v103
	v_fmac_f32_e32 v112, v104, v104
	v_fmac_f32_e32 v112, v105, v105
	v_fmac_f32_e32 v112, v106, v106
	v_fmac_f32_e32 v112, v107, v107
	v_fmac_f32_e32 v112, v108, v108
	v_fmac_f32_e32 v112, v109, v109
	v_fmac_f32_e32 v112, v110, v110
	v_fmac_f32_e32 v112, v111, v111
	v_mul_f32_e32 v100, v100, v10
	v_mul_f32_e32 v101, v101, v11
	v_add_f32_dpp v112, v112, v112 quad_perm:[1,0,3,2] row_mask:0xf bank_mask:0xf
	v_mul_f32_e32 v102, v102, v12
	v_mul_f32_e32 v103, v103, v13
	v_add_f32_dpp v112, v112, v112 quad_perm:[2,3,0,1] row_mask:0xf bank_mask:0xf
	v_mul_f32_e32 v104, v104, v14
	v_mul_f32_e32 v105, v105, v15
	v_add_f32_dpp v112, v112, v112 row_half_mirror row_mask:0xf bank_mask:0xf
	v_mul_f32_e32 v106, v106, v16
	v_mul_f32_e32 v107, v107, v17
	v_add_f32_dpp v112, v112, v112 row_mirror row_mask:0xf bank_mask:0xf
	v_mul_f32_e32 v108, v108, v18
	v_mul_f32_e32 v109, v109, v19
	v_mul_f32_e32 v110, v110, v20
	v_mul_f32_e32 v111, v111, v21
	v_add_f32_e32 v112, 0x3949539c, v112
	v_rsq_f32_e32 v113, v112
	s_nop 0
	v_mul_f32_e32 v108, v108, v113
	v_mul_f32_e32 v109, v109, v113
	v_mul_f32_e32 v110, v110, v113
	v_mul_f32_e32 v111, v111, v113
	v_mul_f32_e32 v100, v100, v113
	v_mul_f32_e32 v101, v101, v113
	v_mul_f32_e32 v102, v102, v113
	v_mul_f32_e32 v103, v103, v113
	v_mul_f32_e32 v104, v104, v113
	v_mul_f32_e32 v105, v105, v113
	v_mul_f32_e32 v106, v106, v113
	v_mul_f32_e32 v107, v107, v113
	s_cbranch_scc0 .Lmp_norope_q5
	v_mul_f32_dpp v118, v108, v114 row_ror:8 row_mask:0xf bank_mask:0xf
	v_mul_f32_dpp v119, v109, v115 row_ror:8 row_mask:0xf bank_mask:0xf
	v_mul_f32_dpp v120, v110, v116 row_ror:8 row_mask:0xf bank_mask:0xf
	v_mul_f32_dpp v121, v111, v117 row_ror:8 row_mask:0xf bank_mask:0xf
	v_fmac_f32_e32 v118, v108, v92
	v_fmac_f32_e32 v119, v109, v93
	v_fmac_f32_e32 v120, v110, v94
	v_fmac_f32_e32 v121, v111, v95
	s_branch .Lmp_ropedone_q5

.Lmp_ropedone_k5:
	v_cvt_pk_bf16_f32 v100, v100, v101
	v_cvt_pk_bf16_f32 v101, v102, v103
	v_cvt_pk_bf16_f32 v102, v104, v105
	v_cvt_pk_bf16_f32 v103, v106, v107
	v_cvt_pk_bf16_f32 v118, v118, v119
	v_cvt_pk_bf16_f32 v119, v120, v121
	global_store_dwordx4 v4, v[100:103], s[30:31]
	global_store_dwordx2 v5, v[118:119], s[30:31]
	s_nop 1
	s_add_i32 s11, s10, 0x4000
	s_lshr_b32 s0, s11, 8
	s_mul_i32 s0, s0, 57
	s_lshr_b32 s0, s0, 9
	s_mul_i32 s0, s0, 0x900
	s_sub_i32 s0, s11, s0
	s_sub_i32 s0, s0, 0x100
	s_max_i32 s0, s0, 0
	s_mul_i32 s1, s11, 0x600
	s_add_u32 s12, s48, s1
	s_addc_u32 s13, s49, 0
	s_lshl_b32 s1, s11, 11
	s_add_u32 s14, s50, s1
	s_addc_u32 s15, s51, 0
	s_lshl_b32 s1, s11, 9
	s_add_u32 s16, s52, s1
	s_addc_u32 s17, s53, 0
	s_lshl_b32 s1, s0, 7
	s_add_u32 s18, s54, s1
	s_addc_u32 s19, s55, 0
	s_add_u32 s22, s56, s1
	s_addc_u32 s23, s57, 0
	global_load_dwordx4 v[78:81], v4, s[12:13]
	global_load_dwordx2 v[82:83], v5, s[12:13]
	global_load_dwordx4 v[84:87], v6, s[14:15]
	global_load_dwordx4 v[88:91], v7, s[16:17]
	global_load_dwordx4 v[92:95], v8, s[18:19]
	global_load_dwordx4 v[96:99], v8, s[22:23]
	s_waitcnt vmcnt(20)
	s_add_i32 s11, s10, 0x3000
	s_lshr_b32 s0, s11, 8
	s_mul_i32 s0, s0, 57
	s_lshr_b32 s0, s0, 9
	s_mul_i32 s0, s0, 0x900
	s_sub_i32 s0, s11, s0
	s_mul_i32 s1, s11, 0x600
	s_add_u32 s28, s58, s1
	s_addc_u32 s29, s59, 0
	s_add_u32 s30, s44, s1
	s_addc_u32 s31, s45, 0
	v_xor_b32_e32 v114, v9, v52
	v_xor_b32_e32 v115, v9, v53
	v_xor_b32_e32 v116, v9, v54
	v_xor_b32_e32 v117, v9, v55
	s_cmpk_ge_u32 s0, 0x100
	v_lshlrev_b32_e32 v100, 16, v34
	v_and_b32_e32 v101, 0xffff0000, v34
	v_lshlrev_b32_e32 v102, 16, v35
	v_and_b32_e32 v103, 0xffff0000, v35
	v_lshlrev_b32_e32 v104, 16, v36
	v_and_b32_e32 v105, 0xffff0000, v36
	v_lshlrev_b32_e32 v106, 16, v37
	v_and_b32_e32 v107, 0xffff0000, v37
	v_lshlrev_b32_e32 v108, 16, v38
	v_and_b32_e32 v109, 0xffff0000, v38
	v_lshlrev_b32_e32 v110, 16, v39
	v_and_b32_e32 v111, 0xffff0000, v39
	v_mul_f32_e32 v112, v100, v100
	v_fmac_f32_e32 v112, v101, v101
	v_fmac_f32_e32 v112, v102, v102
	v_fmac_f32_e32 v112, v103, v103
	v_fmac_f32_e32 v112, v104, v104
	v_fmac_f32_e32 v112, v105, v105
	v_fmac_f32_e32 v112, v106, v106
	v_fmac_f32_e32 v112, v107, v107
	v_fmac_f32_e32 v112, v108, v108
	v_fmac_f32_e32 v112, v109, v109
	v_fmac_f32_e32 v112, v110, v110
	v_fmac_f32_e32 v112, v111, v111
	v_mul_f32_e32 v100, v100, v10
	v_mul_f32_e32 v101, v101, v11
	v_add_f32_dpp v112, v112, v112 quad_perm:[1,0,3,2] row_mask:0xf bank_mask:0xf
	v_mul_f32_e32 v102, v102, v12
	v_mul_f32_e32 v103, v103, v13
	v_add_f32_dpp v112, v112, v112 quad_perm:[2,3,0,1] row_mask:0xf bank_mask:0xf
	v_mul_f32_e32 v104, v104, v14
	v_mul_f32_e32 v105, v105, v15
	v_add_f32_dpp v112, v112, v112 row_half_mirror row_mask:0xf bank_mask:0xf
	v_mul_f32_e32 v106, v106, v16
	v_mul_f32_e32 v107, v107, v17
	v_add_f32_dpp v112, v112, v112 row_mirror row_mask:0xf bank_mask:0xf
	v_mul_f32_e32 v108, v108, v18
	v_mul_f32_e32 v109, v109, v19
	v_mul_f32_e32 v110, v110, v20
	v_mul_f32_e32 v111, v111, v21
	v_add_f32_e32 v112, 0x3949539c, v112
	v_rsq_f32_e32 v113, v112
	s_nop 0
	v_mul_f32_e32 v108, v108, v113
	v_mul_f32_e32 v109, v109, v113
	v_mul_f32_e32 v110, v110, v113
	v_mul_f32_e32 v111, v111, v113
	v_mul_f32_e32 v100, v100, v113
	v_mul_f32_e32 v101, v101, v113
	v_mul_f32_e32 v102, v102, v113
	v_mul_f32_e32 v103, v103, v113
	v_mul_f32_e32 v104, v104, v113
	v_mul_f32_e32 v105, v105, v113
	v_mul_f32_e32 v106, v106, v113
	v_mul_f32_e32 v107, v107, v113
	s_cbranch_scc0 .Lmp_norope_q6
	v_mul_f32_dpp v118, v108, v114 row_ror:8 row_mask:0xf bank_mask:0xf
	v_mul_f32_dpp v119, v109, v115 row_ror:8 row_mask:0xf bank_mask:0xf
	v_mul_f32_dpp v120, v110, v116 row_ror:8 row_mask:0xf bank_mask:0xf
	v_mul_f32_dpp v121, v111, v117 row_ror:8 row_mask:0xf bank_mask:0xf
	v_fmac_f32_e32 v118, v108, v48
	v_fmac_f32_e32 v119, v109, v49
	v_fmac_f32_e32 v120, v110, v50
	v_fmac_f32_e32 v121, v111, v51
	s_branch .Lmp_ropedone_q6

.Lmp_ropedone_k6:
	v_cvt_pk_bf16_f32 v100, v100, v101
	v_cvt_pk_bf16_f32 v101, v102, v103
	v_cvt_pk_bf16_f32 v102, v104, v105
	v_cvt_pk_bf16_f32 v103, v106, v107
	v_cvt_pk_bf16_f32 v118, v118, v119
	v_cvt_pk_bf16_f32 v119, v120, v121
	global_store_dwordx4 v4, v[100:103], s[30:31]
	global_store_dwordx2 v5, v[118:119], s[30:31]
	s_nop 1
	s_waitcnt vmcnt(14)
	s_add_i32 s11, s10, 0x3800
	s_lshr_b32 s0, s11, 8
	s_mul_i32 s0, s0, 57
	s_lshr_b32 s0, s0, 9
	s_mul_i32 s0, s0, 0x900
	s_sub_i32 s0, s11, s0
	s_mul_i32 s1, s11, 0x600
	s_add_u32 s28, s58, s1
	s_addc_u32 s29, s59, 0
	s_add_u32 s30, s44, s1
	s_addc_u32 s31, s45, 0
	v_xor_b32_e32 v114, v9, v74
	v_xor_b32_e32 v115, v9, v75
	v_xor_b32_e32 v116, v9, v76
	v_xor_b32_e32 v117, v9, v77
	s_cmpk_ge_u32 s0, 0x100
	v_lshlrev_b32_e32 v100, 16, v56
	v_and_b32_e32 v101, 0xffff0000, v56
	v_lshlrev_b32_e32 v102, 16, v57
	v_and_b32_e32 v103, 0xffff0000, v57
	v_lshlrev_b32_e32 v104, 16, v58
	v_and_b32_e32 v105, 0xffff0000, v58
	v_lshlrev_b32_e32 v106, 16, v59
	v_and_b32_e32 v107, 0xffff0000, v59
	v_lshlrev_b32_e32 v108, 16, v60
	v_and_b32_e32 v109, 0xffff0000, v60
	v_lshlrev_b32_e32 v110, 16, v61
	v_and_b32_e32 v111, 0xffff0000, v61
	v_mul_f32_e32 v112, v100, v100
	v_fmac_f32_e32 v112, v101, v101
	v_fmac_f32_e32 v112, v102, v102
	v_fmac_f32_e32 v112, v103, v103
	v_fmac_f32_e32 v112, v104, v104
	v_fmac_f32_e32 v112, v105, v105
	v_fmac_f32_e32 v112, v106, v106
	v_fmac_f32_e32 v112, v107, v107
	v_fmac_f32_e32 v112, v108, v108
	v_fmac_f32_e32 v112, v109, v109
	v_fmac_f32_e32 v112, v110, v110
	v_fmac_f32_e32 v112, v111, v111
	v_mul_f32_e32 v100, v100, v10
	v_mul_f32_e32 v101, v101, v11
	v_add_f32_dpp v112, v112, v112 quad_perm:[1,0,3,2] row_mask:0xf bank_mask:0xf
	v_mul_f32_e32 v102, v102, v12
	v_mul_f32_e32 v103, v103, v13
	v_add_f32_dpp v112, v112, v112 quad_perm:[2,3,0,1] row_mask:0xf bank_mask:0xf
	v_mul_f32_e32 v104, v104, v14
	v_mul_f32_e32 v105, v105, v15
	v_add_f32_dpp v112, v112, v112 row_half_mirror row_mask:0xf bank_mask:0xf
	v_mul_f32_e32 v106, v106, v16
	v_mul_f32_e32 v107, v107, v17
	v_add_f32_dpp v112, v112, v112 row_mirror row_mask:0xf bank_mask:0xf
	v_mul_f32_e32 v108, v108, v18
	v_mul_f32_e32 v109, v109, v19
	v_mul_f32_e32 v110, v110, v20
	v_mul_f32_e32 v111, v111, v21
	v_add_f32_e32 v112, 0x3949539c, v112
	v_rsq_f32_e32 v113, v112
	s_nop 0
	v_mul_f32_e32 v108, v108, v113
	v_mul_f32_e32 v109, v109, v113
	v_mul_f32_e32 v110, v110, v113
	v_mul_f32_e32 v111, v111, v113
	v_mul_f32_e32 v100, v100, v113
	v_mul_f32_e32 v101, v101, v113
	v_mul_f32_e32 v102, v102, v113
	v_mul_f32_e32 v103, v103, v113
	v_mul_f32_e32 v104, v104, v113
	v_mul_f32_e32 v105, v105, v113
	v_mul_f32_e32 v106, v106, v113
	v_mul_f32_e32 v107, v107, v113
	s_cbranch_scc0 .Lmp_norope_q7
	v_mul_f32_dpp v118, v108, v114 row_ror:8 row_mask:0xf bank_mask:0xf
	v_mul_f32_dpp v119, v109, v115 row_ror:8 row_mask:0xf bank_mask:0xf
	v_mul_f32_dpp v120, v110, v116 row_ror:8 row_mask:0xf bank_mask:0xf
	v_mul_f32_dpp v121, v111, v117 row_ror:8 row_mask:0xf bank_mask:0xf
	v_fmac_f32_e32 v118, v108, v70
	v_fmac_f32_e32 v119, v109, v71
	v_fmac_f32_e32 v120, v110, v72
	v_fmac_f32_e32 v121, v111, v73
	s_branch .Lmp_ropedone_q7

.Lmp_ropedone_k7:
	v_cvt_pk_bf16_f32 v100, v100, v101
	v_cvt_pk_bf16_f32 v101, v102, v103
	v_cvt_pk_bf16_f32 v102, v104, v105
	v_cvt_pk_bf16_f32 v103, v106, v107
	v_cvt_pk_bf16_f32 v118, v118, v119
	v_cvt_pk_bf16_f32 v119, v120, v121
	global_store_dwordx4 v4, v[100:103], s[30:31]
	global_store_dwordx2 v5, v[118:119], s[30:31]
	s_nop 1
	s_waitcnt vmcnt(8)
	s_add_i32 s11, s10, 0x4000
	s_lshr_b32 s0, s11, 8
	s_mul_i32 s0, s0, 57
	s_lshr_b32 s0, s0, 9
	s_mul_i32 s0, s0, 0x900
	s_sub_i32 s0, s11, s0
	s_mul_i32 s1, s11, 0x600
	s_add_u32 s28, s58, s1
	s_addc_u32 s29, s59, 0
	s_add_u32 s30, s44, s1
	s_addc_u32 s31, s45, 0
	v_xor_b32_e32 v114, v9, v96
	v_xor_b32_e32 v115, v9, v97
	v_xor_b32_e32 v116, v9, v98
	v_xor_b32_e32 v117, v9, v99
	s_cmpk_ge_u32 s0, 0x100
	v_lshlrev_b32_e32 v100, 16, v78
	v_and_b32_e32 v101, 0xffff0000, v78
	v_lshlrev_b32_e32 v102, 16, v79
	v_and_b32_e32 v103, 0xffff0000, v79
	v_lshlrev_b32_e32 v104, 16, v80
	v_and_b32_e32 v105, 0xffff0000, v80
	v_lshlrev_b32_e32 v106, 16, v81
	v_and_b32_e32 v107, 0xffff0000, v81
	v_lshlrev_b32_e32 v108, 16, v82
	v_and_b32_e32 v109, 0xffff0000, v82
	v_lshlrev_b32_e32 v110, 16, v83
	v_and_b32_e32 v111, 0xffff0000, v83
	v_mul_f32_e32 v112, v100, v100
	v_fmac_f32_e32 v112, v101, v101
	v_fmac_f32_e32 v112, v102, v102
	v_fmac_f32_e32 v112, v103, v103
	v_fmac_f32_e32 v112, v104, v104
	v_fmac_f32_e32 v112, v105, v105
	v_fmac_f32_e32 v112, v106, v106
	v_fmac_f32_e32 v112, v107, v107
	v_fmac_f32_e32 v112, v108, v108
	v_fmac_f32_e32 v112, v109, v109
	v_fmac_f32_e32 v112, v110, v110
	v_fmac_f32_e32 v112, v111, v111
	v_mul_f32_e32 v100, v100, v10
	v_mul_f32_e32 v101, v101, v11
	v_add_f32_dpp v112, v112, v112 quad_perm:[1,0,3,2] row_mask:0xf bank_mask:0xf
	v_mul_f32_e32 v102, v102, v12
	v_mul_f32_e32 v103, v103, v13
	v_add_f32_dpp v112, v112, v112 quad_perm:[2,3,0,1] row_mask:0xf bank_mask:0xf
	v_mul_f32_e32 v104, v104, v14
	v_mul_f32_e32 v105, v105, v15
	v_add_f32_dpp v112, v112, v112 row_half_mirror row_mask:0xf bank_mask:0xf
	v_mul_f32_e32 v106, v106, v16
	v_mul_f32_e32 v107, v107, v17
	v_add_f32_dpp v112, v112, v112 row_mirror row_mask:0xf bank_mask:0xf
	v_mul_f32_e32 v108, v108, v18
	v_mul_f32_e32 v109, v109, v19
	v_mul_f32_e32 v110, v110, v20
	v_mul_f32_e32 v111, v111, v21
	v_add_f32_e32 v112, 0x3949539c, v112
	v_rsq_f32_e32 v113, v112
	s_nop 0
	v_mul_f32_e32 v108, v108, v113
	v_mul_f32_e32 v109, v109, v113
	v_mul_f32_e32 v110, v110, v113
	v_mul_f32_e32 v111, v111, v113
	v_mul_f32_e32 v100, v100, v113
	v_mul_f32_e32 v101, v101, v113
	v_mul_f32_e32 v102, v102, v113
	v_mul_f32_e32 v103, v103, v113
	v_mul_f32_e32 v104, v104, v113
	v_mul_f32_e32 v105, v105, v113
	v_mul_f32_e32 v106, v106, v113
	v_mul_f32_e32 v107, v107, v113
	s_cbranch_scc0 .Lmp_norope_q8
	v_mul_f32_dpp v118, v108, v114 row_ror:8 row_mask:0xf bank_mask:0xf
	v_mul_f32_dpp v119, v109, v115 row_ror:8 row_mask:0xf bank_mask:0xf
	v_mul_f32_dpp v120, v110, v116 row_ror:8 row_mask:0xf bank_mask:0xf
	v_mul_f32_dpp v121, v111, v117 row_ror:8 row_mask:0xf bank_mask:0xf
	v_fmac_f32_e32 v118, v108, v92
	v_fmac_f32_e32 v119, v109, v93
	v_fmac_f32_e32 v120, v110, v94
	v_fmac_f32_e32 v121, v111, v95
	s_branch .Lmp_ropedone_q8

.Lmp_ropedone_k8:
	v_cvt_pk_bf16_f32 v100, v100, v101
	v_cvt_pk_bf16_f32 v101, v102, v103
	v_cvt_pk_bf16_f32 v102, v104, v105
	v_cvt_pk_bf16_f32 v103, v106, v107
	v_cvt_pk_bf16_f32 v118, v118, v119
	v_cvt_pk_bf16_f32 v119, v120, v121
	global_store_dwordx4 v4, v[100:103], s[30:31]
	global_store_dwordx2 v5, v[118:119], s[30:31]
	s_nop 1
	s_branch .LBB0_6572
.Lmp_orig:
	v_mov_b32_e32 v1, v0
	v_readlane_b32 s1, v251, 61
	v_readfirstlane_b32 s0, v1
	s_ashr_i32 s0, s0, 6
	s_add_i32 s28, s0, s1
	v_readlane_b32 s8, v251, 57
	s_cmpk_lt_i32 s28, 0x4800
	v_readlane_b32 s10, v251, 59
	v_readlane_b32 s11, v251, 60
	s_cselect_b64 s[4:5], -1, 0
	s_mov_b64 s[20:21], s[10:11]
	s_and_b64 s[0:1], s[4:5], exec
	s_cselect_b32 s26, s28, 0
	s_add_u32 s0, s20, 0x50790000
	s_addc_u32 s1, s21, 0
	s_mul_i32 s2, s26, 0x600
	s_waitcnt vmcnt(0)
	v_and_b32_e32 v6, 63, v1
	s_mul_hi_i32 s3, s26, 0x600
	s_add_u32 s2, s0, s2
	s_addc_u32 s3, s1, s3
	v_lshlrev_b32_e32 v2, 3, v6
	v_cmp_gt_u32_e64 s[38:39], 48, v6
	v_lshl_add_u64 v[4:5], s[2:3], 0, v[2:3]
	v_mov_b32_e32 v108, 0
	v_mov_b32_e32 v110, 0
	v_mov_b32_e32 v111, 0
	v_readlane_b32 s9, v251, 58
	s_and_saveexec_b64 s[24:25], s[38:39]
	s_cbranch_execz .LBB0_6457
	global_load_dwordx2 v[110:111], v[4:5], off
